# select v5: 4096-element blocks with per-256 group skipping, tail elements replaced by the lowest key at copy-out, next pass first block requested before find_bin
# speedup vs baseline: 1.0091x; 1.0091x over previous
.LBB0_1234:
	s_or_b64 exec, exec, s[4:5]
	s_lshl_b64 s[4:5], s[38:39], 10
	s_add_u32 s40, s48, s4
	s_addc_u32 s41, s49, s5
	s_cmpk_gt_i32 s38, 0xff
	s_mov_b64 s[4:5], -1
	s_cbranch_scc0 .LBB0_1866
	s_add_i32 s2, s38, 1
	s_lshl_b64 s[42:43], s[38:39], 15
	s_add_u32 s42, s46, s42
	s_addc_u32 s43, s47, s43
	v_lshlrev_b32_e32 v58, 4, v50
	v_add_u32_e32 v220, 0x1000, v58
	v_add_u32_e32 v221, 0x2000, v58
	v_add_u32_e32 v222, 0x3000, v58
	v_mov_b32_e32 v216, 0
	v_mov_b32_e32 v217, 0
	v_mov_b32_e32 v218, 0
	v_mov_b32_e32 v219, 0
	v_add_u32_e32 v64, s52, v58
	s_movk_i32 s15, 0x100
	s_mov_b64 s[8:9], s[42:43]
	global_load_dwordx4 v[150:153], v58, s[8:9]
	s_cmp_le_i32 s2, 0x100
	s_cbranch_scc1 .Lsel_ld1_end
	global_load_dwordx4 v[154:157], v58, s[8:9] offset:1024
	s_cmp_le_i32 s2, 0x200
	s_cbranch_scc1 .Lsel_ld1_end
	global_load_dwordx4 v[158:161], v58, s[8:9] offset:2048
	s_cmp_le_i32 s2, 0x300
	s_cbranch_scc1 .Lsel_ld1_end
	global_load_dwordx4 v[162:165], v58, s[8:9] offset:3072
	s_cmp_le_i32 s2, 0x400
	s_cbranch_scc1 .Lsel_ld1_end
	global_load_dwordx4 v[166:169], v220, s[8:9]
	s_cmp_le_i32 s2, 0x500
	s_cbranch_scc1 .Lsel_ld1_end
	global_load_dwordx4 v[170:173], v220, s[8:9] offset:1024
	s_cmp_le_i32 s2, 0x600
	s_cbranch_scc1 .Lsel_ld1_end
	global_load_dwordx4 v[174:177], v220, s[8:9] offset:2048
	s_cmp_le_i32 s2, 0x700
	s_cbranch_scc1 .Lsel_ld1_end
	global_load_dwordx4 v[178:181], v220, s[8:9] offset:3072
	s_cmp_le_i32 s2, 0x800
	s_cbranch_scc1 .Lsel_ld1_end
	global_load_dwordx4 v[182:185], v221, s[8:9]
	s_cmp_le_i32 s2, 0x900
	s_cbranch_scc1 .Lsel_ld1_end
	global_load_dwordx4 v[186:189], v221, s[8:9] offset:1024
	s_cmp_le_i32 s2, 0xa00
	s_cbranch_scc1 .Lsel_ld1_end
	global_load_dwordx4 v[190:193], v221, s[8:9] offset:2048
	s_cmp_le_i32 s2, 0xb00
	s_cbranch_scc1 .Lsel_ld1_end
	global_load_dwordx4 v[194:197], v221, s[8:9] offset:3072
	s_cmp_le_i32 s2, 0xc00
	s_cbranch_scc1 .Lsel_ld1_end
	global_load_dwordx4 v[198:201], v222, s[8:9]
	s_cmp_le_i32 s2, 0xd00
	s_cbranch_scc1 .Lsel_ld1_end
	global_load_dwordx4 v[202:205], v222, s[8:9] offset:1024
	s_cmp_le_i32 s2, 0xe00
	s_cbranch_scc1 .Lsel_ld1_end
	global_load_dwordx4 v[206:209], v222, s[8:9] offset:2048
	s_cmp_le_i32 s2, 0xf00
	s_cbranch_scc1 .Lsel_ld1_end
	global_load_dwordx4 v[210:213], v222, s[8:9] offset:3072
.Lsel_ld1_end:
	ds_write_b128 v64, v[216:219]
	ds_write_b128 v64, v[216:219] offset:1024
	ds_write_b128 v64, v[216:219] offset:2048
	ds_write_b128 v64, v[216:219] offset:3072
	ds_write_b128 v64, v[216:219] offset:4096
	ds_write_b128 v64, v[216:219] offset:5120
	ds_write_b128 v64, v[216:219] offset:6144
	ds_write_b128 v64, v[216:219] offset:7168
	s_mov_b32 s16, 0
	s_waitcnt vmcnt(0)
.Lsel_p1_loop:
	s_add_i32 s36, s16, 0x1000
	s_sub_i32 s37, s2, s16
	s_cmp_le_i32 s36, s2
	s_cbranch_scc0 .Lsel_p1_tail
	v_mov_b64_e32 v[2:3], v[150:151]
	v_mov_b64_e32 v[4:5], v[152:153]
	v_mov_b64_e32 v[6:7], v[154:155]
	v_mov_b64_e32 v[8:9], v[156:157]
	v_mov_b64_e32 v[10:11], v[158:159]
	v_mov_b64_e32 v[12:13], v[160:161]
	v_mov_b64_e32 v[14:15], v[162:163]
	v_mov_b64_e32 v[16:17], v[164:165]
	v_mov_b64_e32 v[18:19], v[166:167]
	v_mov_b64_e32 v[20:21], v[168:169]
	v_mov_b64_e32 v[22:23], v[170:171]
	v_mov_b64_e32 v[24:25], v[172:173]
	v_mov_b64_e32 v[26:27], v[174:175]
	v_mov_b64_e32 v[28:29], v[176:177]
	v_mov_b64_e32 v[30:31], v[178:179]
	v_mov_b64_e32 v[32:33], v[180:181]
	v_mov_b64_e32 v[34:35], v[182:183]
	v_mov_b64_e32 v[36:37], v[184:185]
	v_mov_b64_e32 v[38:39], v[186:187]
	v_mov_b64_e32 v[40:41], v[188:189]
	v_mov_b64_e32 v[42:43], v[190:191]
	v_mov_b64_e32 v[44:45], v[192:193]
	v_mov_b64_e32 v[46:47], v[194:195]
	v_mov_b64_e32 v[48:49], v[196:197]
	v_mov_b64_e32 v[118:119], v[198:199]
	v_mov_b64_e32 v[120:121], v[200:201]
	v_mov_b64_e32 v[122:123], v[202:203]
	v_mov_b64_e32 v[124:125], v[204:205]
	v_mov_b64_e32 v[126:127], v[206:207]
	v_mov_b64_e32 v[128:129], v[208:209]
	v_mov_b64_e32 v[130:131], v[210:211]
	v_mov_b64_e32 v[132:133], v[212:213]
	s_movk_i32 s79, 16
	s_cmp_lt_i32 s36, s2
	s_cbranch_scc0 .Lsel_p1_body
	s_add_u32 s8, s8, 0x4000
	s_addc_u32 s9, s9, 0
	s_sub_i32 s80, s2, s36
	global_load_dwordx4 v[150:153], v58, s[8:9]
	s_cmp_le_i32 s80, 0x100
	s_cbranch_scc1 .Lsel_ld2_end
	global_load_dwordx4 v[154:157], v58, s[8:9] offset:1024
	s_cmp_le_i32 s80, 0x200
	s_cbranch_scc1 .Lsel_ld2_end
	global_load_dwordx4 v[158:161], v58, s[8:9] offset:2048
	s_cmp_le_i32 s80, 0x300
	s_cbranch_scc1 .Lsel_ld2_end
	global_load_dwordx4 v[162:165], v58, s[8:9] offset:3072
	s_cmp_le_i32 s80, 0x400
	s_cbranch_scc1 .Lsel_ld2_end
	global_load_dwordx4 v[166:169], v220, s[8:9]
	s_cmp_le_i32 s80, 0x500
	s_cbranch_scc1 .Lsel_ld2_end
	global_load_dwordx4 v[170:173], v220, s[8:9] offset:1024
	s_cmp_le_i32 s80, 0x600
	s_cbranch_scc1 .Lsel_ld2_end
	global_load_dwordx4 v[174:177], v220, s[8:9] offset:2048
	s_cmp_le_i32 s80, 0x700
	s_cbranch_scc1 .Lsel_ld2_end
	global_load_dwordx4 v[178:181], v220, s[8:9] offset:3072
	s_cmp_le_i32 s80, 0x800
	s_cbranch_scc1 .Lsel_ld2_end
	global_load_dwordx4 v[182:185], v221, s[8:9]
	s_cmp_le_i32 s80, 0x900
	s_cbranch_scc1 .Lsel_ld2_end
	global_load_dwordx4 v[186:189], v221, s[8:9] offset:1024
	s_cmp_le_i32 s80, 0xa00
	s_cbranch_scc1 .Lsel_ld2_end
	global_load_dwordx4 v[190:193], v221, s[8:9] offset:2048
	s_cmp_le_i32 s80, 0xb00
	s_cbranch_scc1 .Lsel_ld2_end
	global_load_dwordx4 v[194:197], v221, s[8:9] offset:3072
	s_cmp_le_i32 s80, 0xc00
	s_cbranch_scc1 .Lsel_ld2_end
	global_load_dwordx4 v[198:201], v222, s[8:9]
	s_cmp_le_i32 s80, 0xd00
	s_cbranch_scc1 .Lsel_ld2_end
	global_load_dwordx4 v[202:205], v222, s[8:9] offset:1024
	s_cmp_le_i32 s80, 0xe00
	s_cbranch_scc1 .Lsel_ld2_end
	global_load_dwordx4 v[206:209], v222, s[8:9] offset:2048
	s_cmp_le_i32 s80, 0xf00
	s_cbranch_scc1 .Lsel_ld2_end
	global_load_dwordx4 v[210:213], v222, s[8:9] offset:3072

.Lsel_p1_tail:
	v_sub_u32_e32 v138, s37, v56
	s_add_i32 s79, s37, 0xff
	s_lshr_b32 s79, s79, 8
	v_cmp_lt_i32_e64 s[58:59], 0, v138
	v_cmp_lt_i32_e64 s[60:61], 1, v138
	v_cmp_lt_i32_e64 s[62:63], 2, v138
	v_cmp_lt_i32_e64 s[64:65], 3, v138
	v_cndmask_b32_e64 v2, -1, v150, s[58:59]
	v_cndmask_b32_e64 v3, -1, v151, s[60:61]
	v_cndmask_b32_e64 v4, -1, v152, s[62:63]
	v_cndmask_b32_e64 v5, -1, v153, s[64:65]
	s_cmp_le_u32 s79, 1
	s_cbranch_scc1 .Lsel_p1_body
	v_add_u32_e32 v138, 0xffffff00, v138
	v_cmp_lt_i32_e64 s[58:59], 0, v138
	v_cmp_lt_i32_e64 s[60:61], 1, v138
	v_cmp_lt_i32_e64 s[62:63], 2, v138
	v_cmp_lt_i32_e64 s[64:65], 3, v138
	v_cndmask_b32_e64 v6, -1, v154, s[58:59]
	v_cndmask_b32_e64 v7, -1, v155, s[60:61]
	v_cndmask_b32_e64 v8, -1, v156, s[62:63]
	v_cndmask_b32_e64 v9, -1, v157, s[64:65]
	s_cmp_le_u32 s79, 2
	s_cbranch_scc1 .Lsel_p1_body
	v_add_u32_e32 v138, 0xffffff00, v138
	v_cmp_lt_i32_e64 s[58:59], 0, v138
	v_cmp_lt_i32_e64 s[60:61], 1, v138
	v_cmp_lt_i32_e64 s[62:63], 2, v138
	v_cmp_lt_i32_e64 s[64:65], 3, v138
	v_cndmask_b32_e64 v10, -1, v158, s[58:59]
	v_cndmask_b32_e64 v11, -1, v159, s[60:61]
	v_cndmask_b32_e64 v12, -1, v160, s[62:63]
	v_cndmask_b32_e64 v13, -1, v161, s[64:65]
	s_cmp_le_u32 s79, 3
	s_cbranch_scc1 .Lsel_p1_body
	v_add_u32_e32 v138, 0xffffff00, v138
	v_cmp_lt_i32_e64 s[58:59], 0, v138
	v_cmp_lt_i32_e64 s[60:61], 1, v138
	v_cmp_lt_i32_e64 s[62:63], 2, v138
	v_cmp_lt_i32_e64 s[64:65], 3, v138
	v_cndmask_b32_e64 v14, -1, v162, s[58:59]
	v_cndmask_b32_e64 v15, -1, v163, s[60:61]
	v_cndmask_b32_e64 v16, -1, v164, s[62:63]
	v_cndmask_b32_e64 v17, -1, v165, s[64:65]
	s_cmp_le_u32 s79, 4
	s_cbranch_scc1 .Lsel_p1_body
	v_add_u32_e32 v138, 0xffffff00, v138
	v_cmp_lt_i32_e64 s[58:59], 0, v138
	v_cmp_lt_i32_e64 s[60:61], 1, v138
	v_cmp_lt_i32_e64 s[62:63], 2, v138
	v_cmp_lt_i32_e64 s[64:65], 3, v138
	v_cndmask_b32_e64 v18, -1, v166, s[58:59]
	v_cndmask_b32_e64 v19, -1, v167, s[60:61]
	v_cndmask_b32_e64 v20, -1, v168, s[62:63]
	v_cndmask_b32_e64 v21, -1, v169, s[64:65]
	s_cmp_le_u32 s79, 5
	s_cbranch_scc1 .Lsel_p1_body
	v_add_u32_e32 v138, 0xffffff00, v138
	v_cmp_lt_i32_e64 s[58:59], 0, v138
	v_cmp_lt_i32_e64 s[60:61], 1, v138
	v_cmp_lt_i32_e64 s[62:63], 2, v138
	v_cmp_lt_i32_e64 s[64:65], 3, v138
	v_cndmask_b32_e64 v22, -1, v170, s[58:59]
	v_cndmask_b32_e64 v23, -1, v171, s[60:61]
	v_cndmask_b32_e64 v24, -1, v172, s[62:63]
	v_cndmask_b32_e64 v25, -1, v173, s[64:65]
	s_cmp_le_u32 s79, 6
	s_cbranch_scc1 .Lsel_p1_body
	v_add_u32_e32 v138, 0xffffff00, v138
	v_cmp_lt_i32_e64 s[58:59], 0, v138
	v_cmp_lt_i32_e64 s[60:61], 1, v138
	v_cmp_lt_i32_e64 s[62:63], 2, v138
	v_cmp_lt_i32_e64 s[64:65], 3, v138
	v_cndmask_b32_e64 v26, -1, v174, s[58:59]
	v_cndmask_b32_e64 v27, -1, v175, s[60:61]
	v_cndmask_b32_e64 v28, -1, v176, s[62:63]
	v_cndmask_b32_e64 v29, -1, v177, s[64:65]
	s_cmp_le_u32 s79, 7
	s_cbranch_scc1 .Lsel_p1_body
	v_add_u32_e32 v138, 0xffffff00, v138
	v_cmp_lt_i32_e64 s[58:59], 0, v138
	v_cmp_lt_i32_e64 s[60:61], 1, v138
	v_cmp_lt_i32_e64 s[62:63], 2, v138
	v_cmp_lt_i32_e64 s[64:65], 3, v138
	v_cndmask_b32_e64 v30, -1, v178, s[58:59]
	v_cndmask_b32_e64 v31, -1, v179, s[60:61]
	v_cndmask_b32_e64 v32, -1, v180, s[62:63]
	v_cndmask_b32_e64 v33, -1, v181, s[64:65]
	s_cmp_le_u32 s79, 8
	s_cbranch_scc1 .Lsel_p1_body
	v_add_u32_e32 v138, 0xffffff00, v138
	v_cmp_lt_i32_e64 s[58:59], 0, v138
	v_cmp_lt_i32_e64 s[60:61], 1, v138
	v_cmp_lt_i32_e64 s[62:63], 2, v138
	v_cmp_lt_i32_e64 s[64:65], 3, v138
	v_cndmask_b32_e64 v34, -1, v182, s[58:59]
	v_cndmask_b32_e64 v35, -1, v183, s[60:61]
	v_cndmask_b32_e64 v36, -1, v184, s[62:63]
	v_cndmask_b32_e64 v37, -1, v185, s[64:65]
	s_cmp_le_u32 s79, 9
	s_cbranch_scc1 .Lsel_p1_body
	v_add_u32_e32 v138, 0xffffff00, v138
	v_cmp_lt_i32_e64 s[58:59], 0, v138
	v_cmp_lt_i32_e64 s[60:61], 1, v138
	v_cmp_lt_i32_e64 s[62:63], 2, v138
	v_cmp_lt_i32_e64 s[64:65], 3, v138
	v_cndmask_b32_e64 v38, -1, v186, s[58:59]
	v_cndmask_b32_e64 v39, -1, v187, s[60:61]
	v_cndmask_b32_e64 v40, -1, v188, s[62:63]
	v_cndmask_b32_e64 v41, -1, v189, s[64:65]
	s_cmp_le_u32 s79, 10
	s_cbranch_scc1 .Lsel_p1_body
	v_add_u32_e32 v138, 0xffffff00, v138
	v_cmp_lt_i32_e64 s[58:59], 0, v138
	v_cmp_lt_i32_e64 s[60:61], 1, v138
	v_cmp_lt_i32_e64 s[62:63], 2, v138
	v_cmp_lt_i32_e64 s[64:65], 3, v138
	v_cndmask_b32_e64 v42, -1, v190, s[58:59]
	v_cndmask_b32_e64 v43, -1, v191, s[60:61]
	v_cndmask_b32_e64 v44, -1, v192, s[62:63]
	v_cndmask_b32_e64 v45, -1, v193, s[64:65]
	s_cmp_le_u32 s79, 11
	s_cbranch_scc1 .Lsel_p1_body
	v_add_u32_e32 v138, 0xffffff00, v138
	v_cmp_lt_i32_e64 s[58:59], 0, v138
	v_cmp_lt_i32_e64 s[60:61], 1, v138
	v_cmp_lt_i32_e64 s[62:63], 2, v138
	v_cmp_lt_i32_e64 s[64:65], 3, v138
	v_cndmask_b32_e64 v46, -1, v194, s[58:59]
	v_cndmask_b32_e64 v47, -1, v195, s[60:61]
	v_cndmask_b32_e64 v48, -1, v196, s[62:63]
	v_cndmask_b32_e64 v49, -1, v197, s[64:65]
	s_cmp_le_u32 s79, 12
	s_cbranch_scc1 .Lsel_p1_body
	v_add_u32_e32 v138, 0xffffff00, v138
	v_cmp_lt_i32_e64 s[58:59], 0, v138
	v_cmp_lt_i32_e64 s[60:61], 1, v138
	v_cmp_lt_i32_e64 s[62:63], 2, v138
	v_cmp_lt_i32_e64 s[64:65], 3, v138
	v_cndmask_b32_e64 v118, -1, v198, s[58:59]
	v_cndmask_b32_e64 v119, -1, v199, s[60:61]
	v_cndmask_b32_e64 v120, -1, v200, s[62:63]
	v_cndmask_b32_e64 v121, -1, v201, s[64:65]
	s_cmp_le_u32 s79, 13
	s_cbranch_scc1 .Lsel_p1_body
	v_add_u32_e32 v138, 0xffffff00, v138
	v_cmp_lt_i32_e64 s[58:59], 0, v138
	v_cmp_lt_i32_e64 s[60:61], 1, v138
	v_cmp_lt_i32_e64 s[62:63], 2, v138
	v_cmp_lt_i32_e64 s[64:65], 3, v138
	v_cndmask_b32_e64 v122, -1, v202, s[58:59]
	v_cndmask_b32_e64 v123, -1, v203, s[60:61]
	v_cndmask_b32_e64 v124, -1, v204, s[62:63]
	v_cndmask_b32_e64 v125, -1, v205, s[64:65]
	s_cmp_le_u32 s79, 14
	s_cbranch_scc1 .Lsel_p1_body
	v_add_u32_e32 v138, 0xffffff00, v138
	v_cmp_lt_i32_e64 s[58:59], 0, v138
	v_cmp_lt_i32_e64 s[60:61], 1, v138
	v_cmp_lt_i32_e64 s[62:63], 2, v138
	v_cmp_lt_i32_e64 s[64:65], 3, v138
	v_cndmask_b32_e64 v126, -1, v206, s[58:59]
	v_cndmask_b32_e64 v127, -1, v207, s[60:61]
	v_cndmask_b32_e64 v128, -1, v208, s[62:63]
	v_cndmask_b32_e64 v129, -1, v209, s[64:65]
	s_cmp_le_u32 s79, 15
	s_cbranch_scc1 .Lsel_p1_body
	v_add_u32_e32 v138, 0xffffff00, v138
	v_cmp_lt_i32_e64 s[58:59], 0, v138
	v_cmp_lt_i32_e64 s[60:61], 1, v138
	v_cmp_lt_i32_e64 s[62:63], 2, v138
	v_cmp_lt_i32_e64 s[64:65], 3, v138
	v_cndmask_b32_e64 v130, -1, v210, s[58:59]
	v_cndmask_b32_e64 v131, -1, v211, s[60:61]
	v_cndmask_b32_e64 v132, -1, v212, s[62:63]
	v_cndmask_b32_e64 v133, -1, v213, s[64:65]
.Lsel_p1_body:
	v_bfe_u32 v134, v2, 21, 11
	v_lshl_add_u32 v134, v134, 2, s52
	ds_add_u32 v134, v57
	v_bfe_u32 v135, v3, 21, 11
	v_lshl_add_u32 v135, v135, 2, s52
	ds_add_u32 v135, v57
	v_bfe_u32 v136, v4, 21, 11
	v_lshl_add_u32 v136, v136, 2, s52
	ds_add_u32 v136, v57
	v_bfe_u32 v137, v5, 21, 11
	v_lshl_add_u32 v137, v137, 2, s52
	ds_add_u32 v137, v57
	s_cmp_le_u32 s79, 1
	s_cbranch_scc1 .Lsel_p1_bend
	v_bfe_u32 v134, v6, 21, 11
	v_lshl_add_u32 v134, v134, 2, s52
	ds_add_u32 v134, v57
	v_bfe_u32 v135, v7, 21, 11
	v_lshl_add_u32 v135, v135, 2, s52
	ds_add_u32 v135, v57
	v_bfe_u32 v136, v8, 21, 11
	v_lshl_add_u32 v136, v136, 2, s52
	ds_add_u32 v136, v57
	v_bfe_u32 v137, v9, 21, 11
	v_lshl_add_u32 v137, v137, 2, s52
	ds_add_u32 v137, v57
	s_cmp_le_u32 s79, 2
	s_cbranch_scc1 .Lsel_p1_bend
	v_bfe_u32 v134, v10, 21, 11
	v_lshl_add_u32 v134, v134, 2, s52
	ds_add_u32 v134, v57
	v_bfe_u32 v135, v11, 21, 11
	v_lshl_add_u32 v135, v135, 2, s52
	ds_add_u32 v135, v57
	v_bfe_u32 v136, v12, 21, 11
	v_lshl_add_u32 v136, v136, 2, s52
	ds_add_u32 v136, v57
	v_bfe_u32 v137, v13, 21, 11
	v_lshl_add_u32 v137, v137, 2, s52
	ds_add_u32 v137, v57
	s_cmp_le_u32 s79, 3
	s_cbranch_scc1 .Lsel_p1_bend
	v_bfe_u32 v134, v14, 21, 11
	v_lshl_add_u32 v134, v134, 2, s52
	ds_add_u32 v134, v57
	v_bfe_u32 v135, v15, 21, 11
	v_lshl_add_u32 v135, v135, 2, s52
	ds_add_u32 v135, v57
	v_bfe_u32 v136, v16, 21, 11
	v_lshl_add_u32 v136, v136, 2, s52
	ds_add_u32 v136, v57
	v_bfe_u32 v137, v17, 21, 11
	v_lshl_add_u32 v137, v137, 2, s52
	ds_add_u32 v137, v57
	s_cmp_le_u32 s79, 4
	s_cbranch_scc1 .Lsel_p1_bend
	v_bfe_u32 v134, v18, 21, 11
	v_lshl_add_u32 v134, v134, 2, s52
	ds_add_u32 v134, v57
	v_bfe_u32 v135, v19, 21, 11
	v_lshl_add_u32 v135, v135, 2, s52
	ds_add_u32 v135, v57
	v_bfe_u32 v136, v20, 21, 11
	v_lshl_add_u32 v136, v136, 2, s52
	ds_add_u32 v136, v57
	v_bfe_u32 v137, v21, 21, 11
	v_lshl_add_u32 v137, v137, 2, s52
	ds_add_u32 v137, v57
	s_cmp_le_u32 s79, 5
	s_cbranch_scc1 .Lsel_p1_bend
	v_bfe_u32 v134, v22, 21, 11
	v_lshl_add_u32 v134, v134, 2, s52
	ds_add_u32 v134, v57
	v_bfe_u32 v135, v23, 21, 11
	v_lshl_add_u32 v135, v135, 2, s52
	ds_add_u32 v135, v57
	v_bfe_u32 v136, v24, 21, 11
	v_lshl_add_u32 v136, v136, 2, s52
	ds_add_u32 v136, v57
	v_bfe_u32 v137, v25, 21, 11
	v_lshl_add_u32 v137, v137, 2, s52
	ds_add_u32 v137, v57
	s_cmp_le_u32 s79, 6
	s_cbranch_scc1 .Lsel_p1_bend
	v_bfe_u32 v134, v26, 21, 11
	v_lshl_add_u32 v134, v134, 2, s52
	ds_add_u32 v134, v57
	v_bfe_u32 v135, v27, 21, 11
	v_lshl_add_u32 v135, v135, 2, s52
	ds_add_u32 v135, v57
	v_bfe_u32 v136, v28, 21, 11
	v_lshl_add_u32 v136, v136, 2, s52
	ds_add_u32 v136, v57
	v_bfe_u32 v137, v29, 21, 11
	v_lshl_add_u32 v137, v137, 2, s52
	ds_add_u32 v137, v57
	s_cmp_le_u32 s79, 7
	s_cbranch_scc1 .Lsel_p1_bend
	v_bfe_u32 v134, v30, 21, 11
	v_lshl_add_u32 v134, v134, 2, s52
	ds_add_u32 v134, v57
	v_bfe_u32 v135, v31, 21, 11
	v_lshl_add_u32 v135, v135, 2, s52
	ds_add_u32 v135, v57
	v_bfe_u32 v136, v32, 21, 11
	v_lshl_add_u32 v136, v136, 2, s52
	ds_add_u32 v136, v57
	v_bfe_u32 v137, v33, 21, 11
	v_lshl_add_u32 v137, v137, 2, s52
	ds_add_u32 v137, v57
	s_cmp_le_u32 s79, 8
	s_cbranch_scc1 .Lsel_p1_bend
	v_bfe_u32 v134, v34, 21, 11
	v_lshl_add_u32 v134, v134, 2, s52
	ds_add_u32 v134, v57
	v_bfe_u32 v135, v35, 21, 11
	v_lshl_add_u32 v135, v135, 2, s52
	ds_add_u32 v135, v57
	v_bfe_u32 v136, v36, 21, 11
	v_lshl_add_u32 v136, v136, 2, s52
	ds_add_u32 v136, v57
	v_bfe_u32 v137, v37, 21, 11
	v_lshl_add_u32 v137, v137, 2, s52
	ds_add_u32 v137, v57
	s_cmp_le_u32 s79, 9
	s_cbranch_scc1 .Lsel_p1_bend
	v_bfe_u32 v134, v38, 21, 11
	v_lshl_add_u32 v134, v134, 2, s52
	ds_add_u32 v134, v57
	v_bfe_u32 v135, v39, 21, 11
	v_lshl_add_u32 v135, v135, 2, s52
	ds_add_u32 v135, v57
	v_bfe_u32 v136, v40, 21, 11
	v_lshl_add_u32 v136, v136, 2, s52
	ds_add_u32 v136, v57
	v_bfe_u32 v137, v41, 21, 11
	v_lshl_add_u32 v137, v137, 2, s52
	ds_add_u32 v137, v57
	s_cmp_le_u32 s79, 10
	s_cbranch_scc1 .Lsel_p1_bend
	v_bfe_u32 v134, v42, 21, 11
	v_lshl_add_u32 v134, v134, 2, s52
	ds_add_u32 v134, v57
	v_bfe_u32 v135, v43, 21, 11
	v_lshl_add_u32 v135, v135, 2, s52
	ds_add_u32 v135, v57
	v_bfe_u32 v136, v44, 21, 11
	v_lshl_add_u32 v136, v136, 2, s52
	ds_add_u32 v136, v57
	v_bfe_u32 v137, v45, 21, 11
	v_lshl_add_u32 v137, v137, 2, s52
	ds_add_u32 v137, v57
	s_cmp_le_u32 s79, 11
	s_cbranch_scc1 .Lsel_p1_bend
	v_bfe_u32 v134, v46, 21, 11
	v_lshl_add_u32 v134, v134, 2, s52
	ds_add_u32 v134, v57
	v_bfe_u32 v135, v47, 21, 11
	v_lshl_add_u32 v135, v135, 2, s52
	ds_add_u32 v135, v57
	v_bfe_u32 v136, v48, 21, 11
	v_lshl_add_u32 v136, v136, 2, s52
	ds_add_u32 v136, v57
	v_bfe_u32 v137, v49, 21, 11
	v_lshl_add_u32 v137, v137, 2, s52
	ds_add_u32 v137, v57
	s_cmp_le_u32 s79, 12
	s_cbranch_scc1 .Lsel_p1_bend
	v_bfe_u32 v134, v118, 21, 11
	v_lshl_add_u32 v134, v134, 2, s52
	ds_add_u32 v134, v57
	v_bfe_u32 v135, v119, 21, 11
	v_lshl_add_u32 v135, v135, 2, s52
	ds_add_u32 v135, v57
	v_bfe_u32 v136, v120, 21, 11
	v_lshl_add_u32 v136, v136, 2, s52
	ds_add_u32 v136, v57
	v_bfe_u32 v137, v121, 21, 11
	v_lshl_add_u32 v137, v137, 2, s52
	ds_add_u32 v137, v57
	s_cmp_le_u32 s79, 13
	s_cbranch_scc1 .Lsel_p1_bend
	v_bfe_u32 v134, v122, 21, 11
	v_lshl_add_u32 v134, v134, 2, s52
	ds_add_u32 v134, v57
	v_bfe_u32 v135, v123, 21, 11
	v_lshl_add_u32 v135, v135, 2, s52
	ds_add_u32 v135, v57
	v_bfe_u32 v136, v124, 21, 11
	v_lshl_add_u32 v136, v136, 2, s52
	ds_add_u32 v136, v57
	v_bfe_u32 v137, v125, 21, 11
	v_lshl_add_u32 v137, v137, 2, s52
	ds_add_u32 v137, v57
	s_cmp_le_u32 s79, 14
	s_cbranch_scc1 .Lsel_p1_bend
	v_bfe_u32 v134, v126, 21, 11
	v_lshl_add_u32 v134, v134, 2, s52
	ds_add_u32 v134, v57
	v_bfe_u32 v135, v127, 21, 11
	v_lshl_add_u32 v135, v135, 2, s52
	ds_add_u32 v135, v57
	v_bfe_u32 v136, v128, 21, 11
	v_lshl_add_u32 v136, v136, 2, s52
	ds_add_u32 v136, v57
	v_bfe_u32 v137, v129, 21, 11
	v_lshl_add_u32 v137, v137, 2, s52
	ds_add_u32 v137, v57
	s_cmp_le_u32 s79, 15
	s_cbranch_scc1 .Lsel_p1_bend
	v_bfe_u32 v134, v130, 21, 11
	v_lshl_add_u32 v134, v134, 2, s52
	ds_add_u32 v134, v57
	v_bfe_u32 v135, v131, 21, 11
	v_lshl_add_u32 v135, v135, 2, s52
	ds_add_u32 v135, v57
	v_bfe_u32 v136, v132, 21, 11
	v_lshl_add_u32 v136, v136, 2, s52
	ds_add_u32 v136, v57
	v_bfe_u32 v137, v133, 21, 11
	v_lshl_add_u32 v137, v137, 2, s52
	ds_add_u32 v137, v57
.Lsel_p1_bend:
	s_mov_b32 s16, s36
	s_cmp_lt_i32 s16, s2
	s_cbranch_scc0 .Lsel_p1_done
	s_waitcnt vmcnt(0)
	s_branch .Lsel_p1_loop
.Lsel_p1_done:
	s_mov_b64 s[8:9], s[42:43]
	global_load_dwordx4 v[150:153], v58, s[8:9]
	s_cmp_le_i32 s2, 0x100
	s_cbranch_scc1 .Lsel_ld3_end
	global_load_dwordx4 v[154:157], v58, s[8:9] offset:1024
	s_cmp_le_i32 s2, 0x200
	s_cbranch_scc1 .Lsel_ld3_end
	global_load_dwordx4 v[158:161], v58, s[8:9] offset:2048
	s_cmp_le_i32 s2, 0x300
	s_cbranch_scc1 .Lsel_ld3_end
	global_load_dwordx4 v[162:165], v58, s[8:9] offset:3072
	s_cmp_le_i32 s2, 0x400
	s_cbranch_scc1 .Lsel_ld3_end
	global_load_dwordx4 v[166:169], v220, s[8:9]
	s_cmp_le_i32 s2, 0x500
	s_cbranch_scc1 .Lsel_ld3_end
	global_load_dwordx4 v[170:173], v220, s[8:9] offset:1024
	s_cmp_le_i32 s2, 0x600
	s_cbranch_scc1 .Lsel_ld3_end
	global_load_dwordx4 v[174:177], v220, s[8:9] offset:2048
	s_cmp_le_i32 s2, 0x700
	s_cbranch_scc1 .Lsel_ld3_end
	global_load_dwordx4 v[178:181], v220, s[8:9] offset:3072
	s_cmp_le_i32 s2, 0x800
	s_cbranch_scc1 .Lsel_ld3_end
	global_load_dwordx4 v[182:185], v221, s[8:9]
	s_cmp_le_i32 s2, 0x900
	s_cbranch_scc1 .Lsel_ld3_end
	global_load_dwordx4 v[186:189], v221, s[8:9] offset:1024
	s_cmp_le_i32 s2, 0xa00
	s_cbranch_scc1 .Lsel_ld3_end
	global_load_dwordx4 v[190:193], v221, s[8:9] offset:2048
	s_cmp_le_i32 s2, 0xb00
	s_cbranch_scc1 .Lsel_ld3_end
	global_load_dwordx4 v[194:197], v221, s[8:9] offset:3072
	s_cmp_le_i32 s2, 0xc00
	s_cbranch_scc1 .Lsel_ld3_end
	global_load_dwordx4 v[198:201], v222, s[8:9]
	s_cmp_le_i32 s2, 0xd00
	s_cbranch_scc1 .Lsel_ld3_end
	global_load_dwordx4 v[202:205], v222, s[8:9] offset:1024
	s_cmp_le_i32 s2, 0xe00
	s_cbranch_scc1 .Lsel_ld3_end
	global_load_dwordx4 v[206:209], v222, s[8:9] offset:2048
	s_cmp_le_i32 s2, 0xf00
	s_cbranch_scc1 .Lsel_ld3_end
	global_load_dwordx4 v[210:213], v222, s[8:9] offset:3072
.Lsel_ld3_end:
	s_waitcnt lgkmcnt(0)
	v_lshlrev_b32_e32 v34, 7, v50
	v_sub_u32_e32 v44, 0x1f80, v34
	v_add_u32_e32 v34, 0xfffff000, v34
	v_cmp_gt_u32_e32 vcc, 32, v50
	s_nop 1
	v_cndmask_b32_e32 v34, v34, v44, vcc
	v_add_u32_e32 v34, s52, v34
	ds_read_b128 v[2:5], v34
	ds_read_b128 v[6:9], v34 offset:16
	ds_read_b128 v[10:13], v34 offset:32
	ds_read_b128 v[14:17], v34 offset:48
	ds_read_b128 v[18:21], v34 offset:64
	ds_read_b128 v[22:25], v34 offset:80
	ds_read_b128 v[26:29], v34 offset:96
	ds_read_b128 v[30:33], v34 offset:112
	s_waitcnt lgkmcnt(0)
	v_add_u32_e32 v35, v2, v3
	v_add3_u32 v35, v35, v4, v5
	v_add3_u32 v35, v35, v6, v7
	v_add3_u32 v35, v35, v8, v9
	v_add3_u32 v35, v35, v10, v11
	v_add3_u32 v35, v35, v12, v13
	v_add3_u32 v35, v35, v14, v15
	v_add3_u32 v35, v35, v16, v17
	v_add3_u32 v35, v35, v18, v19
	v_add3_u32 v35, v35, v20, v21
	v_add3_u32 v35, v35, v22, v23
	v_add3_u32 v35, v35, v24, v25
	v_add3_u32 v35, v35, v26, v27
	v_add3_u32 v35, v35, v28, v29
	v_add3_u32 v35, v35, v30, v31
	v_add3_u32 v35, v35, v32, v33
	v_mov_b32_e32 v36, v35
	s_nop 1
	v_add_u32_dpp v36, v36, v36 row_shr:1 row_mask:0xf bank_mask:0xf bound_ctrl:1
	s_nop 1
	v_add_u32_dpp v36, v36, v36 row_shr:2 row_mask:0xf bank_mask:0xf bound_ctrl:1
	s_nop 1
	v_add_u32_dpp v36, v36, v36 row_shr:4 row_mask:0xf bank_mask:0xf bound_ctrl:1
	s_nop 1
	v_add_u32_dpp v36, v36, v36 row_shr:8 row_mask:0xf bank_mask:0xf bound_ctrl:1
	s_nop 1
	v_add_u32_dpp v36, v36, v36 row_bcast:15 row_mask:0xa bank_mask:0xf
	s_nop 1
	v_add_u32_dpp v36, v36, v36 row_bcast:31 row_mask:0xc bank_mask:0xf
	s_nop 0
	v_readlane_b32 s4, v36, 63
	s_nop 1
	v_sub_u32_e32 v37, s4, v36
	v_add_u32_e32 v38, v37, v35
	v_cmp_gt_u32_e32 vcc, s15, v37
	v_cmp_le_u32_e64 s[4:5], s15, v38
	s_and_b64 s[4:5], vcc, s[4:5]
	s_ff1_i32_b64 s6, s[4:5]
	v_readlane_b32 s7, v37, s6
	s_lshl_b32 s10, s6, 7
	s_sub_i32 s11, 0x1f80, s10
	s_add_i32 s10, s10, 0xfffff07c
	s_cmp_ge_u32 s6, 32
	s_cselect_b32 s10, s10, s11
	s_cselect_b32 s34, -1, 1
	s_add_i32 s10, s10, s52
	v_and_b32_e32 v39, 31, v50
	v_lshlrev_b32_e32 v39, 2, v39
	v_mul_i32_i24_e32 v39, s34, v39
	v_add_u32_e32 v39, s10, v39
	ds_read_b32 v40, v39
	v_cmp_gt_u32_e32 vcc, 32, v50
	s_waitcnt lgkmcnt(0)
	s_nop 1
	v_cndmask_b32_e32 v40, 0, v40, vcc
	v_mov_b32_e32 v41, v40
	s_nop 1
	v_add_u32_dpp v41, v41, v41 row_shr:1 row_mask:0xf bank_mask:0xf bound_ctrl:1
	s_nop 1
	v_add_u32_dpp v41, v41, v41 row_shr:2 row_mask:0xf bank_mask:0xf bound_ctrl:1
	s_nop 1
	v_add_u32_dpp v41, v41, v41 row_shr:4 row_mask:0xf bank_mask:0xf bound_ctrl:1
	s_nop 1
	v_add_u32_dpp v41, v41, v41 row_shr:8 row_mask:0xf bank_mask:0xf bound_ctrl:1
	s_nop 1
	v_add_u32_dpp v41, v41, v41 row_bcast:15 row_mask:0xa bank_mask:0xf
	s_nop 1
	v_add_u32_dpp v41, v41, v41 row_bcast:31 row_mask:0xc bank_mask:0xf
	s_nop 0
	v_sub_u32_e32 v42, v41, v40
	v_add_u32_e32 v42, s7, v42
	v_add_u32_e32 v43, v42, v40
	v_cmp_gt_u32_e32 vcc, s15, v42
	v_cmp_le_u32_e64 s[4:5], s15, v43
	s_and_b64 s[4:5], vcc, s[4:5]
	s_ff1_i32_b64 s11, s[4:5]
	v_readlane_b32 s14, v40, s11
	v_readlane_b32 s5, v42, s11
	s_lshl_b32 s30, s6, 5
	s_sub_i32 s4, 31, s11
	s_add_i32 s30, s30, s4
	s_sub_i32 s15, s15, s5
	s_cmp_lt_u32 s30, 0x400
	s_cselect_b32 s31, 1, 0
	s_add_i32 s4, s30, 0xfffffc00
	s_sub_i32 s5, 0x7ff, s30
	s_cmp_lg_u32 s31, 0
	s_cselect_b32 s13, s5, s4
	ds_write_b128 v64, v[216:219]
	ds_write_b128 v64, v[216:219] offset:1024
	ds_write_b128 v64, v[216:219] offset:2048
	ds_write_b128 v64, v[216:219] offset:3072
	ds_write_b128 v64, v[216:219] offset:4096
	ds_write_b128 v64, v[216:219] offset:5120
	ds_write_b128 v64, v[216:219] offset:6144
	ds_write_b128 v64, v[216:219] offset:7168
	s_cmpk_le_u32 s14, 0x800
	s_cselect_b32 s25, -1, 0
	s_add_i32 s24, s52, 0x2000
	s_mov_b32 s16, 0
	s_waitcnt vmcnt(0)

.Lsel_p2_body:
	v_lshrrev_b32_e32 v134, 21, v2
	v_cmpx_eq_u32_e32 vcc, s13, v134
	v_bfe_u32 v134, v2, 10, 11
	v_lshl_add_u32 v134, v134, 2, s52
	ds_add_u32 v134, v57
	v_mbcnt_lo_u32_b32 v134, vcc_lo, 0
	v_mbcnt_hi_u32_b32 v134, vcc_hi, v134
	v_lshl_add_u32 v134, v134, 2, s24
	ds_write_b32 v134, v2
	s_bcnt1_i32_b64 s5, vcc
	s_and_b32 s5, s5, s25
	s_lshl2_add_u32 s24, s5, s24
	s_mov_b64 exec, -1
	v_lshrrev_b32_e32 v135, 21, v3
	v_cmpx_eq_u32_e32 vcc, s13, v135
	v_bfe_u32 v135, v3, 10, 11
	v_lshl_add_u32 v135, v135, 2, s52
	ds_add_u32 v135, v57
	v_mbcnt_lo_u32_b32 v135, vcc_lo, 0
	v_mbcnt_hi_u32_b32 v135, vcc_hi, v135
	v_lshl_add_u32 v135, v135, 2, s24
	ds_write_b32 v135, v3
	s_bcnt1_i32_b64 s5, vcc
	s_and_b32 s5, s5, s25
	s_lshl2_add_u32 s24, s5, s24
	s_mov_b64 exec, -1
	v_lshrrev_b32_e32 v136, 21, v4
	v_cmpx_eq_u32_e32 vcc, s13, v136
	v_bfe_u32 v136, v4, 10, 11
	v_lshl_add_u32 v136, v136, 2, s52
	ds_add_u32 v136, v57
	v_mbcnt_lo_u32_b32 v136, vcc_lo, 0
	v_mbcnt_hi_u32_b32 v136, vcc_hi, v136
	v_lshl_add_u32 v136, v136, 2, s24
	ds_write_b32 v136, v4
	s_bcnt1_i32_b64 s5, vcc
	s_and_b32 s5, s5, s25
	s_lshl2_add_u32 s24, s5, s24
	s_mov_b64 exec, -1
	v_lshrrev_b32_e32 v137, 21, v5
	v_cmpx_eq_u32_e32 vcc, s13, v137
	v_bfe_u32 v137, v5, 10, 11
	v_lshl_add_u32 v137, v137, 2, s52
	ds_add_u32 v137, v57
	v_mbcnt_lo_u32_b32 v137, vcc_lo, 0
	v_mbcnt_hi_u32_b32 v137, vcc_hi, v137
	v_lshl_add_u32 v137, v137, 2, s24
	ds_write_b32 v137, v5
	s_bcnt1_i32_b64 s5, vcc
	s_and_b32 s5, s5, s25
	s_lshl2_add_u32 s24, s5, s24
	s_mov_b64 exec, -1
	s_cmp_le_u32 s79, 1
	s_cbranch_scc1 .Lsel_p2_bend
	v_lshrrev_b32_e32 v134, 21, v6
	v_cmpx_eq_u32_e32 vcc, s13, v134
	v_bfe_u32 v134, v6, 10, 11
	v_lshl_add_u32 v134, v134, 2, s52
	ds_add_u32 v134, v57
	v_mbcnt_lo_u32_b32 v134, vcc_lo, 0
	v_mbcnt_hi_u32_b32 v134, vcc_hi, v134
	v_lshl_add_u32 v134, v134, 2, s24
	ds_write_b32 v134, v6
	s_bcnt1_i32_b64 s5, vcc
	s_and_b32 s5, s5, s25
	s_lshl2_add_u32 s24, s5, s24
	s_mov_b64 exec, -1
	v_lshrrev_b32_e32 v135, 21, v7
	v_cmpx_eq_u32_e32 vcc, s13, v135
	v_bfe_u32 v135, v7, 10, 11
	v_lshl_add_u32 v135, v135, 2, s52
	ds_add_u32 v135, v57
	v_mbcnt_lo_u32_b32 v135, vcc_lo, 0
	v_mbcnt_hi_u32_b32 v135, vcc_hi, v135
	v_lshl_add_u32 v135, v135, 2, s24
	ds_write_b32 v135, v7
	s_bcnt1_i32_b64 s5, vcc
	s_and_b32 s5, s5, s25
	s_lshl2_add_u32 s24, s5, s24
	s_mov_b64 exec, -1
	v_lshrrev_b32_e32 v136, 21, v8
	v_cmpx_eq_u32_e32 vcc, s13, v136
	v_bfe_u32 v136, v8, 10, 11
	v_lshl_add_u32 v136, v136, 2, s52
	ds_add_u32 v136, v57
	v_mbcnt_lo_u32_b32 v136, vcc_lo, 0
	v_mbcnt_hi_u32_b32 v136, vcc_hi, v136
	v_lshl_add_u32 v136, v136, 2, s24
	ds_write_b32 v136, v8
	s_bcnt1_i32_b64 s5, vcc
	s_and_b32 s5, s5, s25
	s_lshl2_add_u32 s24, s5, s24
	s_mov_b64 exec, -1
	v_lshrrev_b32_e32 v137, 21, v9
	v_cmpx_eq_u32_e32 vcc, s13, v137
	v_bfe_u32 v137, v9, 10, 11
	v_lshl_add_u32 v137, v137, 2, s52
	ds_add_u32 v137, v57
	v_mbcnt_lo_u32_b32 v137, vcc_lo, 0
	v_mbcnt_hi_u32_b32 v137, vcc_hi, v137
	v_lshl_add_u32 v137, v137, 2, s24
	ds_write_b32 v137, v9
	s_bcnt1_i32_b64 s5, vcc
	s_and_b32 s5, s5, s25
	s_lshl2_add_u32 s24, s5, s24
	s_mov_b64 exec, -1
	s_cmp_le_u32 s79, 2
	s_cbranch_scc1 .Lsel_p2_bend
	v_lshrrev_b32_e32 v134, 21, v10
	v_cmpx_eq_u32_e32 vcc, s13, v134
	v_bfe_u32 v134, v10, 10, 11
	v_lshl_add_u32 v134, v134, 2, s52
	ds_add_u32 v134, v57
	v_mbcnt_lo_u32_b32 v134, vcc_lo, 0
	v_mbcnt_hi_u32_b32 v134, vcc_hi, v134
	v_lshl_add_u32 v134, v134, 2, s24
	ds_write_b32 v134, v10
	s_bcnt1_i32_b64 s5, vcc
	s_and_b32 s5, s5, s25
	s_lshl2_add_u32 s24, s5, s24
	s_mov_b64 exec, -1
	v_lshrrev_b32_e32 v135, 21, v11
	v_cmpx_eq_u32_e32 vcc, s13, v135
	v_bfe_u32 v135, v11, 10, 11
	v_lshl_add_u32 v135, v135, 2, s52
	ds_add_u32 v135, v57
	v_mbcnt_lo_u32_b32 v135, vcc_lo, 0
	v_mbcnt_hi_u32_b32 v135, vcc_hi, v135
	v_lshl_add_u32 v135, v135, 2, s24
	ds_write_b32 v135, v11
	s_bcnt1_i32_b64 s5, vcc
	s_and_b32 s5, s5, s25
	s_lshl2_add_u32 s24, s5, s24
	s_mov_b64 exec, -1
	v_lshrrev_b32_e32 v136, 21, v12
	v_cmpx_eq_u32_e32 vcc, s13, v136
	v_bfe_u32 v136, v12, 10, 11
	v_lshl_add_u32 v136, v136, 2, s52
	ds_add_u32 v136, v57
	v_mbcnt_lo_u32_b32 v136, vcc_lo, 0
	v_mbcnt_hi_u32_b32 v136, vcc_hi, v136
	v_lshl_add_u32 v136, v136, 2, s24
	ds_write_b32 v136, v12
	s_bcnt1_i32_b64 s5, vcc
	s_and_b32 s5, s5, s25
	s_lshl2_add_u32 s24, s5, s24
	s_mov_b64 exec, -1
	v_lshrrev_b32_e32 v137, 21, v13
	v_cmpx_eq_u32_e32 vcc, s13, v137
	v_bfe_u32 v137, v13, 10, 11
	v_lshl_add_u32 v137, v137, 2, s52
	ds_add_u32 v137, v57
	v_mbcnt_lo_u32_b32 v137, vcc_lo, 0
	v_mbcnt_hi_u32_b32 v137, vcc_hi, v137
	v_lshl_add_u32 v137, v137, 2, s24
	ds_write_b32 v137, v13
	s_bcnt1_i32_b64 s5, vcc
	s_and_b32 s5, s5, s25
	s_lshl2_add_u32 s24, s5, s24
	s_mov_b64 exec, -1
	s_cmp_le_u32 s79, 3
	s_cbranch_scc1 .Lsel_p2_bend
	v_lshrrev_b32_e32 v134, 21, v14
	v_cmpx_eq_u32_e32 vcc, s13, v134
	v_bfe_u32 v134, v14, 10, 11
	v_lshl_add_u32 v134, v134, 2, s52
	ds_add_u32 v134, v57
	v_mbcnt_lo_u32_b32 v134, vcc_lo, 0
	v_mbcnt_hi_u32_b32 v134, vcc_hi, v134
	v_lshl_add_u32 v134, v134, 2, s24
	ds_write_b32 v134, v14
	s_bcnt1_i32_b64 s5, vcc
	s_and_b32 s5, s5, s25
	s_lshl2_add_u32 s24, s5, s24
	s_mov_b64 exec, -1
	v_lshrrev_b32_e32 v135, 21, v15
	v_cmpx_eq_u32_e32 vcc, s13, v135
	v_bfe_u32 v135, v15, 10, 11
	v_lshl_add_u32 v135, v135, 2, s52
	ds_add_u32 v135, v57
	v_mbcnt_lo_u32_b32 v135, vcc_lo, 0
	v_mbcnt_hi_u32_b32 v135, vcc_hi, v135
	v_lshl_add_u32 v135, v135, 2, s24
	ds_write_b32 v135, v15
	s_bcnt1_i32_b64 s5, vcc
	s_and_b32 s5, s5, s25
	s_lshl2_add_u32 s24, s5, s24
	s_mov_b64 exec, -1
	v_lshrrev_b32_e32 v136, 21, v16
	v_cmpx_eq_u32_e32 vcc, s13, v136
	v_bfe_u32 v136, v16, 10, 11
	v_lshl_add_u32 v136, v136, 2, s52
	ds_add_u32 v136, v57
	v_mbcnt_lo_u32_b32 v136, vcc_lo, 0
	v_mbcnt_hi_u32_b32 v136, vcc_hi, v136
	v_lshl_add_u32 v136, v136, 2, s24
	ds_write_b32 v136, v16
	s_bcnt1_i32_b64 s5, vcc
	s_and_b32 s5, s5, s25
	s_lshl2_add_u32 s24, s5, s24
	s_mov_b64 exec, -1
	v_lshrrev_b32_e32 v137, 21, v17
	v_cmpx_eq_u32_e32 vcc, s13, v137
	v_bfe_u32 v137, v17, 10, 11
	v_lshl_add_u32 v137, v137, 2, s52
	ds_add_u32 v137, v57
	v_mbcnt_lo_u32_b32 v137, vcc_lo, 0
	v_mbcnt_hi_u32_b32 v137, vcc_hi, v137
	v_lshl_add_u32 v137, v137, 2, s24
	ds_write_b32 v137, v17
	s_bcnt1_i32_b64 s5, vcc
	s_and_b32 s5, s5, s25
	s_lshl2_add_u32 s24, s5, s24
	s_mov_b64 exec, -1
	s_cmp_le_u32 s79, 4
	s_cbranch_scc1 .Lsel_p2_bend
	v_lshrrev_b32_e32 v134, 21, v18
	v_cmpx_eq_u32_e32 vcc, s13, v134
	v_bfe_u32 v134, v18, 10, 11
	v_lshl_add_u32 v134, v134, 2, s52
	ds_add_u32 v134, v57
	v_mbcnt_lo_u32_b32 v134, vcc_lo, 0
	v_mbcnt_hi_u32_b32 v134, vcc_hi, v134
	v_lshl_add_u32 v134, v134, 2, s24
	ds_write_b32 v134, v18
	s_bcnt1_i32_b64 s5, vcc
	s_and_b32 s5, s5, s25
	s_lshl2_add_u32 s24, s5, s24
	s_mov_b64 exec, -1
	v_lshrrev_b32_e32 v135, 21, v19
	v_cmpx_eq_u32_e32 vcc, s13, v135
	v_bfe_u32 v135, v19, 10, 11
	v_lshl_add_u32 v135, v135, 2, s52
	ds_add_u32 v135, v57
	v_mbcnt_lo_u32_b32 v135, vcc_lo, 0
	v_mbcnt_hi_u32_b32 v135, vcc_hi, v135
	v_lshl_add_u32 v135, v135, 2, s24
	ds_write_b32 v135, v19
	s_bcnt1_i32_b64 s5, vcc
	s_and_b32 s5, s5, s25
	s_lshl2_add_u32 s24, s5, s24
	s_mov_b64 exec, -1
	v_lshrrev_b32_e32 v136, 21, v20
	v_cmpx_eq_u32_e32 vcc, s13, v136
	v_bfe_u32 v136, v20, 10, 11
	v_lshl_add_u32 v136, v136, 2, s52
	ds_add_u32 v136, v57
	v_mbcnt_lo_u32_b32 v136, vcc_lo, 0
	v_mbcnt_hi_u32_b32 v136, vcc_hi, v136
	v_lshl_add_u32 v136, v136, 2, s24
	ds_write_b32 v136, v20
	s_bcnt1_i32_b64 s5, vcc
	s_and_b32 s5, s5, s25
	s_lshl2_add_u32 s24, s5, s24
	s_mov_b64 exec, -1
	v_lshrrev_b32_e32 v137, 21, v21
	v_cmpx_eq_u32_e32 vcc, s13, v137
	v_bfe_u32 v137, v21, 10, 11
	v_lshl_add_u32 v137, v137, 2, s52
	ds_add_u32 v137, v57
	v_mbcnt_lo_u32_b32 v137, vcc_lo, 0
	v_mbcnt_hi_u32_b32 v137, vcc_hi, v137
	v_lshl_add_u32 v137, v137, 2, s24
	ds_write_b32 v137, v21
	s_bcnt1_i32_b64 s5, vcc
	s_and_b32 s5, s5, s25
	s_lshl2_add_u32 s24, s5, s24
	s_mov_b64 exec, -1
	s_cmp_le_u32 s79, 5
	s_cbranch_scc1 .Lsel_p2_bend
	v_lshrrev_b32_e32 v134, 21, v22
	v_cmpx_eq_u32_e32 vcc, s13, v134
	v_bfe_u32 v134, v22, 10, 11
	v_lshl_add_u32 v134, v134, 2, s52
	ds_add_u32 v134, v57
	v_mbcnt_lo_u32_b32 v134, vcc_lo, 0
	v_mbcnt_hi_u32_b32 v134, vcc_hi, v134
	v_lshl_add_u32 v134, v134, 2, s24
	ds_write_b32 v134, v22
	s_bcnt1_i32_b64 s5, vcc
	s_and_b32 s5, s5, s25
	s_lshl2_add_u32 s24, s5, s24
	s_mov_b64 exec, -1
	v_lshrrev_b32_e32 v135, 21, v23
	v_cmpx_eq_u32_e32 vcc, s13, v135
	v_bfe_u32 v135, v23, 10, 11
	v_lshl_add_u32 v135, v135, 2, s52
	ds_add_u32 v135, v57
	v_mbcnt_lo_u32_b32 v135, vcc_lo, 0
	v_mbcnt_hi_u32_b32 v135, vcc_hi, v135
	v_lshl_add_u32 v135, v135, 2, s24
	ds_write_b32 v135, v23
	s_bcnt1_i32_b64 s5, vcc
	s_and_b32 s5, s5, s25
	s_lshl2_add_u32 s24, s5, s24
	s_mov_b64 exec, -1
	v_lshrrev_b32_e32 v136, 21, v24
	v_cmpx_eq_u32_e32 vcc, s13, v136
	v_bfe_u32 v136, v24, 10, 11
	v_lshl_add_u32 v136, v136, 2, s52
	ds_add_u32 v136, v57
	v_mbcnt_lo_u32_b32 v136, vcc_lo, 0
	v_mbcnt_hi_u32_b32 v136, vcc_hi, v136
	v_lshl_add_u32 v136, v136, 2, s24
	ds_write_b32 v136, v24
	s_bcnt1_i32_b64 s5, vcc
	s_and_b32 s5, s5, s25
	s_lshl2_add_u32 s24, s5, s24
	s_mov_b64 exec, -1
	v_lshrrev_b32_e32 v137, 21, v25
	v_cmpx_eq_u32_e32 vcc, s13, v137
	v_bfe_u32 v137, v25, 10, 11
	v_lshl_add_u32 v137, v137, 2, s52
	ds_add_u32 v137, v57
	v_mbcnt_lo_u32_b32 v137, vcc_lo, 0
	v_mbcnt_hi_u32_b32 v137, vcc_hi, v137
	v_lshl_add_u32 v137, v137, 2, s24
	ds_write_b32 v137, v25
	s_bcnt1_i32_b64 s5, vcc
	s_and_b32 s5, s5, s25
	s_lshl2_add_u32 s24, s5, s24
	s_mov_b64 exec, -1
	s_cmp_le_u32 s79, 6
	s_cbranch_scc1 .Lsel_p2_bend
	v_lshrrev_b32_e32 v134, 21, v26
	v_cmpx_eq_u32_e32 vcc, s13, v134
	v_bfe_u32 v134, v26, 10, 11
	v_lshl_add_u32 v134, v134, 2, s52
	ds_add_u32 v134, v57
	v_mbcnt_lo_u32_b32 v134, vcc_lo, 0
	v_mbcnt_hi_u32_b32 v134, vcc_hi, v134
	v_lshl_add_u32 v134, v134, 2, s24
	ds_write_b32 v134, v26
	s_bcnt1_i32_b64 s5, vcc
	s_and_b32 s5, s5, s25
	s_lshl2_add_u32 s24, s5, s24
	s_mov_b64 exec, -1
	v_lshrrev_b32_e32 v135, 21, v27
	v_cmpx_eq_u32_e32 vcc, s13, v135
	v_bfe_u32 v135, v27, 10, 11
	v_lshl_add_u32 v135, v135, 2, s52
	ds_add_u32 v135, v57
	v_mbcnt_lo_u32_b32 v135, vcc_lo, 0
	v_mbcnt_hi_u32_b32 v135, vcc_hi, v135
	v_lshl_add_u32 v135, v135, 2, s24
	ds_write_b32 v135, v27
	s_bcnt1_i32_b64 s5, vcc
	s_and_b32 s5, s5, s25
	s_lshl2_add_u32 s24, s5, s24
	s_mov_b64 exec, -1
	v_lshrrev_b32_e32 v136, 21, v28
	v_cmpx_eq_u32_e32 vcc, s13, v136
	v_bfe_u32 v136, v28, 10, 11
	v_lshl_add_u32 v136, v136, 2, s52
	ds_add_u32 v136, v57
	v_mbcnt_lo_u32_b32 v136, vcc_lo, 0
	v_mbcnt_hi_u32_b32 v136, vcc_hi, v136
	v_lshl_add_u32 v136, v136, 2, s24
	ds_write_b32 v136, v28
	s_bcnt1_i32_b64 s5, vcc
	s_and_b32 s5, s5, s25
	s_lshl2_add_u32 s24, s5, s24
	s_mov_b64 exec, -1
	v_lshrrev_b32_e32 v137, 21, v29
	v_cmpx_eq_u32_e32 vcc, s13, v137
	v_bfe_u32 v137, v29, 10, 11
	v_lshl_add_u32 v137, v137, 2, s52
	ds_add_u32 v137, v57
	v_mbcnt_lo_u32_b32 v137, vcc_lo, 0
	v_mbcnt_hi_u32_b32 v137, vcc_hi, v137
	v_lshl_add_u32 v137, v137, 2, s24
	ds_write_b32 v137, v29
	s_bcnt1_i32_b64 s5, vcc
	s_and_b32 s5, s5, s25
	s_lshl2_add_u32 s24, s5, s24
	s_mov_b64 exec, -1
	s_cmp_le_u32 s79, 7
	s_cbranch_scc1 .Lsel_p2_bend
	v_lshrrev_b32_e32 v134, 21, v30
	v_cmpx_eq_u32_e32 vcc, s13, v134
	v_bfe_u32 v134, v30, 10, 11
	v_lshl_add_u32 v134, v134, 2, s52
	ds_add_u32 v134, v57
	v_mbcnt_lo_u32_b32 v134, vcc_lo, 0
	v_mbcnt_hi_u32_b32 v134, vcc_hi, v134
	v_lshl_add_u32 v134, v134, 2, s24
	ds_write_b32 v134, v30
	s_bcnt1_i32_b64 s5, vcc
	s_and_b32 s5, s5, s25
	s_lshl2_add_u32 s24, s5, s24
	s_mov_b64 exec, -1
	v_lshrrev_b32_e32 v135, 21, v31
	v_cmpx_eq_u32_e32 vcc, s13, v135
	v_bfe_u32 v135, v31, 10, 11
	v_lshl_add_u32 v135, v135, 2, s52
	ds_add_u32 v135, v57
	v_mbcnt_lo_u32_b32 v135, vcc_lo, 0
	v_mbcnt_hi_u32_b32 v135, vcc_hi, v135
	v_lshl_add_u32 v135, v135, 2, s24
	ds_write_b32 v135, v31
	s_bcnt1_i32_b64 s5, vcc
	s_and_b32 s5, s5, s25
	s_lshl2_add_u32 s24, s5, s24
	s_mov_b64 exec, -1
	v_lshrrev_b32_e32 v136, 21, v32
	v_cmpx_eq_u32_e32 vcc, s13, v136
	v_bfe_u32 v136, v32, 10, 11
	v_lshl_add_u32 v136, v136, 2, s52
	ds_add_u32 v136, v57
	v_mbcnt_lo_u32_b32 v136, vcc_lo, 0
	v_mbcnt_hi_u32_b32 v136, vcc_hi, v136
	v_lshl_add_u32 v136, v136, 2, s24
	ds_write_b32 v136, v32
	s_bcnt1_i32_b64 s5, vcc
	s_and_b32 s5, s5, s25
	s_lshl2_add_u32 s24, s5, s24
	s_mov_b64 exec, -1
	v_lshrrev_b32_e32 v137, 21, v33
	v_cmpx_eq_u32_e32 vcc, s13, v137
	v_bfe_u32 v137, v33, 10, 11
	v_lshl_add_u32 v137, v137, 2, s52
	ds_add_u32 v137, v57
	v_mbcnt_lo_u32_b32 v137, vcc_lo, 0
	v_mbcnt_hi_u32_b32 v137, vcc_hi, v137
	v_lshl_add_u32 v137, v137, 2, s24
	ds_write_b32 v137, v33
	s_bcnt1_i32_b64 s5, vcc
	s_and_b32 s5, s5, s25
	s_lshl2_add_u32 s24, s5, s24
	s_mov_b64 exec, -1
	s_cmp_le_u32 s79, 8
	s_cbranch_scc1 .Lsel_p2_bend
	v_lshrrev_b32_e32 v134, 21, v34
	v_cmpx_eq_u32_e32 vcc, s13, v134
	v_bfe_u32 v134, v34, 10, 11
	v_lshl_add_u32 v134, v134, 2, s52
	ds_add_u32 v134, v57
	v_mbcnt_lo_u32_b32 v134, vcc_lo, 0
	v_mbcnt_hi_u32_b32 v134, vcc_hi, v134
	v_lshl_add_u32 v134, v134, 2, s24
	ds_write_b32 v134, v34
	s_bcnt1_i32_b64 s5, vcc
	s_and_b32 s5, s5, s25
	s_lshl2_add_u32 s24, s5, s24
	s_mov_b64 exec, -1
	v_lshrrev_b32_e32 v135, 21, v35
	v_cmpx_eq_u32_e32 vcc, s13, v135
	v_bfe_u32 v135, v35, 10, 11
	v_lshl_add_u32 v135, v135, 2, s52
	ds_add_u32 v135, v57
	v_mbcnt_lo_u32_b32 v135, vcc_lo, 0
	v_mbcnt_hi_u32_b32 v135, vcc_hi, v135
	v_lshl_add_u32 v135, v135, 2, s24
	ds_write_b32 v135, v35
	s_bcnt1_i32_b64 s5, vcc
	s_and_b32 s5, s5, s25
	s_lshl2_add_u32 s24, s5, s24
	s_mov_b64 exec, -1
	v_lshrrev_b32_e32 v136, 21, v36
	v_cmpx_eq_u32_e32 vcc, s13, v136
	v_bfe_u32 v136, v36, 10, 11
	v_lshl_add_u32 v136, v136, 2, s52
	ds_add_u32 v136, v57
	v_mbcnt_lo_u32_b32 v136, vcc_lo, 0
	v_mbcnt_hi_u32_b32 v136, vcc_hi, v136
	v_lshl_add_u32 v136, v136, 2, s24
	ds_write_b32 v136, v36
	s_bcnt1_i32_b64 s5, vcc
	s_and_b32 s5, s5, s25
	s_lshl2_add_u32 s24, s5, s24
	s_mov_b64 exec, -1
	v_lshrrev_b32_e32 v137, 21, v37
	v_cmpx_eq_u32_e32 vcc, s13, v137
	v_bfe_u32 v137, v37, 10, 11
	v_lshl_add_u32 v137, v137, 2, s52
	ds_add_u32 v137, v57
	v_mbcnt_lo_u32_b32 v137, vcc_lo, 0
	v_mbcnt_hi_u32_b32 v137, vcc_hi, v137
	v_lshl_add_u32 v137, v137, 2, s24
	ds_write_b32 v137, v37
	s_bcnt1_i32_b64 s5, vcc
	s_and_b32 s5, s5, s25
	s_lshl2_add_u32 s24, s5, s24
	s_mov_b64 exec, -1
	s_cmp_le_u32 s79, 9
	s_cbranch_scc1 .Lsel_p2_bend
	v_lshrrev_b32_e32 v134, 21, v38
	v_cmpx_eq_u32_e32 vcc, s13, v134
	v_bfe_u32 v134, v38, 10, 11
	v_lshl_add_u32 v134, v134, 2, s52
	ds_add_u32 v134, v57
	v_mbcnt_lo_u32_b32 v134, vcc_lo, 0
	v_mbcnt_hi_u32_b32 v134, vcc_hi, v134
	v_lshl_add_u32 v134, v134, 2, s24
	ds_write_b32 v134, v38
	s_bcnt1_i32_b64 s5, vcc
	s_and_b32 s5, s5, s25
	s_lshl2_add_u32 s24, s5, s24
	s_mov_b64 exec, -1
	v_lshrrev_b32_e32 v135, 21, v39
	v_cmpx_eq_u32_e32 vcc, s13, v135
	v_bfe_u32 v135, v39, 10, 11
	v_lshl_add_u32 v135, v135, 2, s52
	ds_add_u32 v135, v57
	v_mbcnt_lo_u32_b32 v135, vcc_lo, 0
	v_mbcnt_hi_u32_b32 v135, vcc_hi, v135
	v_lshl_add_u32 v135, v135, 2, s24
	ds_write_b32 v135, v39
	s_bcnt1_i32_b64 s5, vcc
	s_and_b32 s5, s5, s25
	s_lshl2_add_u32 s24, s5, s24
	s_mov_b64 exec, -1
	v_lshrrev_b32_e32 v136, 21, v40
	v_cmpx_eq_u32_e32 vcc, s13, v136
	v_bfe_u32 v136, v40, 10, 11
	v_lshl_add_u32 v136, v136, 2, s52
	ds_add_u32 v136, v57
	v_mbcnt_lo_u32_b32 v136, vcc_lo, 0
	v_mbcnt_hi_u32_b32 v136, vcc_hi, v136
	v_lshl_add_u32 v136, v136, 2, s24
	ds_write_b32 v136, v40
	s_bcnt1_i32_b64 s5, vcc
	s_and_b32 s5, s5, s25
	s_lshl2_add_u32 s24, s5, s24
	s_mov_b64 exec, -1
	v_lshrrev_b32_e32 v137, 21, v41
	v_cmpx_eq_u32_e32 vcc, s13, v137
	v_bfe_u32 v137, v41, 10, 11
	v_lshl_add_u32 v137, v137, 2, s52
	ds_add_u32 v137, v57
	v_mbcnt_lo_u32_b32 v137, vcc_lo, 0
	v_mbcnt_hi_u32_b32 v137, vcc_hi, v137
	v_lshl_add_u32 v137, v137, 2, s24
	ds_write_b32 v137, v41
	s_bcnt1_i32_b64 s5, vcc
	s_and_b32 s5, s5, s25
	s_lshl2_add_u32 s24, s5, s24
	s_mov_b64 exec, -1
	s_cmp_le_u32 s79, 10
	s_cbranch_scc1 .Lsel_p2_bend
	v_lshrrev_b32_e32 v134, 21, v42
	v_cmpx_eq_u32_e32 vcc, s13, v134
	v_bfe_u32 v134, v42, 10, 11
	v_lshl_add_u32 v134, v134, 2, s52
	ds_add_u32 v134, v57
	v_mbcnt_lo_u32_b32 v134, vcc_lo, 0
	v_mbcnt_hi_u32_b32 v134, vcc_hi, v134
	v_lshl_add_u32 v134, v134, 2, s24
	ds_write_b32 v134, v42
	s_bcnt1_i32_b64 s5, vcc
	s_and_b32 s5, s5, s25
	s_lshl2_add_u32 s24, s5, s24
	s_mov_b64 exec, -1
	v_lshrrev_b32_e32 v135, 21, v43
	v_cmpx_eq_u32_e32 vcc, s13, v135
	v_bfe_u32 v135, v43, 10, 11
	v_lshl_add_u32 v135, v135, 2, s52
	ds_add_u32 v135, v57
	v_mbcnt_lo_u32_b32 v135, vcc_lo, 0
	v_mbcnt_hi_u32_b32 v135, vcc_hi, v135
	v_lshl_add_u32 v135, v135, 2, s24
	ds_write_b32 v135, v43
	s_bcnt1_i32_b64 s5, vcc
	s_and_b32 s5, s5, s25
	s_lshl2_add_u32 s24, s5, s24
	s_mov_b64 exec, -1
	v_lshrrev_b32_e32 v136, 21, v44
	v_cmpx_eq_u32_e32 vcc, s13, v136
	v_bfe_u32 v136, v44, 10, 11
	v_lshl_add_u32 v136, v136, 2, s52
	ds_add_u32 v136, v57
	v_mbcnt_lo_u32_b32 v136, vcc_lo, 0
	v_mbcnt_hi_u32_b32 v136, vcc_hi, v136
	v_lshl_add_u32 v136, v136, 2, s24
	ds_write_b32 v136, v44
	s_bcnt1_i32_b64 s5, vcc
	s_and_b32 s5, s5, s25
	s_lshl2_add_u32 s24, s5, s24
	s_mov_b64 exec, -1
	v_lshrrev_b32_e32 v137, 21, v45
	v_cmpx_eq_u32_e32 vcc, s13, v137
	v_bfe_u32 v137, v45, 10, 11
	v_lshl_add_u32 v137, v137, 2, s52
	ds_add_u32 v137, v57
	v_mbcnt_lo_u32_b32 v137, vcc_lo, 0
	v_mbcnt_hi_u32_b32 v137, vcc_hi, v137
	v_lshl_add_u32 v137, v137, 2, s24
	ds_write_b32 v137, v45
	s_bcnt1_i32_b64 s5, vcc
	s_and_b32 s5, s5, s25
	s_lshl2_add_u32 s24, s5, s24
	s_mov_b64 exec, -1
	s_cmp_le_u32 s79, 11
	s_cbranch_scc1 .Lsel_p2_bend
	v_lshrrev_b32_e32 v134, 21, v46
	v_cmpx_eq_u32_e32 vcc, s13, v134
	v_bfe_u32 v134, v46, 10, 11
	v_lshl_add_u32 v134, v134, 2, s52
	ds_add_u32 v134, v57
	v_mbcnt_lo_u32_b32 v134, vcc_lo, 0
	v_mbcnt_hi_u32_b32 v134, vcc_hi, v134
	v_lshl_add_u32 v134, v134, 2, s24
	ds_write_b32 v134, v46
	s_bcnt1_i32_b64 s5, vcc
	s_and_b32 s5, s5, s25
	s_lshl2_add_u32 s24, s5, s24
	s_mov_b64 exec, -1
	v_lshrrev_b32_e32 v135, 21, v47
	v_cmpx_eq_u32_e32 vcc, s13, v135
	v_bfe_u32 v135, v47, 10, 11
	v_lshl_add_u32 v135, v135, 2, s52
	ds_add_u32 v135, v57
	v_mbcnt_lo_u32_b32 v135, vcc_lo, 0
	v_mbcnt_hi_u32_b32 v135, vcc_hi, v135
	v_lshl_add_u32 v135, v135, 2, s24
	ds_write_b32 v135, v47
	s_bcnt1_i32_b64 s5, vcc
	s_and_b32 s5, s5, s25
	s_lshl2_add_u32 s24, s5, s24
	s_mov_b64 exec, -1
	v_lshrrev_b32_e32 v136, 21, v48
	v_cmpx_eq_u32_e32 vcc, s13, v136
	v_bfe_u32 v136, v48, 10, 11
	v_lshl_add_u32 v136, v136, 2, s52
	ds_add_u32 v136, v57
	v_mbcnt_lo_u32_b32 v136, vcc_lo, 0
	v_mbcnt_hi_u32_b32 v136, vcc_hi, v136
	v_lshl_add_u32 v136, v136, 2, s24
	ds_write_b32 v136, v48
	s_bcnt1_i32_b64 s5, vcc
	s_and_b32 s5, s5, s25
	s_lshl2_add_u32 s24, s5, s24
	s_mov_b64 exec, -1
	v_lshrrev_b32_e32 v137, 21, v49
	v_cmpx_eq_u32_e32 vcc, s13, v137
	v_bfe_u32 v137, v49, 10, 11
	v_lshl_add_u32 v137, v137, 2, s52
	ds_add_u32 v137, v57
	v_mbcnt_lo_u32_b32 v137, vcc_lo, 0
	v_mbcnt_hi_u32_b32 v137, vcc_hi, v137
	v_lshl_add_u32 v137, v137, 2, s24
	ds_write_b32 v137, v49
	s_bcnt1_i32_b64 s5, vcc
	s_and_b32 s5, s5, s25
	s_lshl2_add_u32 s24, s5, s24
	s_mov_b64 exec, -1
	s_cmp_le_u32 s79, 12
	s_cbranch_scc1 .Lsel_p2_bend
	v_lshrrev_b32_e32 v134, 21, v118
	v_cmpx_eq_u32_e32 vcc, s13, v134
	v_bfe_u32 v134, v118, 10, 11
	v_lshl_add_u32 v134, v134, 2, s52
	ds_add_u32 v134, v57
	v_mbcnt_lo_u32_b32 v134, vcc_lo, 0
	v_mbcnt_hi_u32_b32 v134, vcc_hi, v134
	v_lshl_add_u32 v134, v134, 2, s24
	ds_write_b32 v134, v118
	s_bcnt1_i32_b64 s5, vcc
	s_and_b32 s5, s5, s25
	s_lshl2_add_u32 s24, s5, s24
	s_mov_b64 exec, -1
	v_lshrrev_b32_e32 v135, 21, v119
	v_cmpx_eq_u32_e32 vcc, s13, v135
	v_bfe_u32 v135, v119, 10, 11
	v_lshl_add_u32 v135, v135, 2, s52
	ds_add_u32 v135, v57
	v_mbcnt_lo_u32_b32 v135, vcc_lo, 0
	v_mbcnt_hi_u32_b32 v135, vcc_hi, v135
	v_lshl_add_u32 v135, v135, 2, s24
	ds_write_b32 v135, v119
	s_bcnt1_i32_b64 s5, vcc
	s_and_b32 s5, s5, s25
	s_lshl2_add_u32 s24, s5, s24
	s_mov_b64 exec, -1
	v_lshrrev_b32_e32 v136, 21, v120
	v_cmpx_eq_u32_e32 vcc, s13, v136
	v_bfe_u32 v136, v120, 10, 11
	v_lshl_add_u32 v136, v136, 2, s52
	ds_add_u32 v136, v57
	v_mbcnt_lo_u32_b32 v136, vcc_lo, 0
	v_mbcnt_hi_u32_b32 v136, vcc_hi, v136
	v_lshl_add_u32 v136, v136, 2, s24
	ds_write_b32 v136, v120
	s_bcnt1_i32_b64 s5, vcc
	s_and_b32 s5, s5, s25
	s_lshl2_add_u32 s24, s5, s24
	s_mov_b64 exec, -1
	v_lshrrev_b32_e32 v137, 21, v121
	v_cmpx_eq_u32_e32 vcc, s13, v137
	v_bfe_u32 v137, v121, 10, 11
	v_lshl_add_u32 v137, v137, 2, s52
	ds_add_u32 v137, v57
	v_mbcnt_lo_u32_b32 v137, vcc_lo, 0
	v_mbcnt_hi_u32_b32 v137, vcc_hi, v137
	v_lshl_add_u32 v137, v137, 2, s24
	ds_write_b32 v137, v121
	s_bcnt1_i32_b64 s5, vcc
	s_and_b32 s5, s5, s25
	s_lshl2_add_u32 s24, s5, s24
	s_mov_b64 exec, -1
	s_cmp_le_u32 s79, 13
	s_cbranch_scc1 .Lsel_p2_bend
	v_lshrrev_b32_e32 v134, 21, v122
	v_cmpx_eq_u32_e32 vcc, s13, v134
	v_bfe_u32 v134, v122, 10, 11
	v_lshl_add_u32 v134, v134, 2, s52
	ds_add_u32 v134, v57
	v_mbcnt_lo_u32_b32 v134, vcc_lo, 0
	v_mbcnt_hi_u32_b32 v134, vcc_hi, v134
	v_lshl_add_u32 v134, v134, 2, s24
	ds_write_b32 v134, v122
	s_bcnt1_i32_b64 s5, vcc
	s_and_b32 s5, s5, s25
	s_lshl2_add_u32 s24, s5, s24
	s_mov_b64 exec, -1
	v_lshrrev_b32_e32 v135, 21, v123
	v_cmpx_eq_u32_e32 vcc, s13, v135
	v_bfe_u32 v135, v123, 10, 11
	v_lshl_add_u32 v135, v135, 2, s52
	ds_add_u32 v135, v57
	v_mbcnt_lo_u32_b32 v135, vcc_lo, 0
	v_mbcnt_hi_u32_b32 v135, vcc_hi, v135
	v_lshl_add_u32 v135, v135, 2, s24
	ds_write_b32 v135, v123
	s_bcnt1_i32_b64 s5, vcc
	s_and_b32 s5, s5, s25
	s_lshl2_add_u32 s24, s5, s24
	s_mov_b64 exec, -1
	v_lshrrev_b32_e32 v136, 21, v124
	v_cmpx_eq_u32_e32 vcc, s13, v136
	v_bfe_u32 v136, v124, 10, 11
	v_lshl_add_u32 v136, v136, 2, s52
	ds_add_u32 v136, v57
	v_mbcnt_lo_u32_b32 v136, vcc_lo, 0
	v_mbcnt_hi_u32_b32 v136, vcc_hi, v136
	v_lshl_add_u32 v136, v136, 2, s24
	ds_write_b32 v136, v124
	s_bcnt1_i32_b64 s5, vcc
	s_and_b32 s5, s5, s25
	s_lshl2_add_u32 s24, s5, s24
	s_mov_b64 exec, -1
	v_lshrrev_b32_e32 v137, 21, v125
	v_cmpx_eq_u32_e32 vcc, s13, v137
	v_bfe_u32 v137, v125, 10, 11
	v_lshl_add_u32 v137, v137, 2, s52
	ds_add_u32 v137, v57
	v_mbcnt_lo_u32_b32 v137, vcc_lo, 0
	v_mbcnt_hi_u32_b32 v137, vcc_hi, v137
	v_lshl_add_u32 v137, v137, 2, s24
	ds_write_b32 v137, v125
	s_bcnt1_i32_b64 s5, vcc
	s_and_b32 s5, s5, s25
	s_lshl2_add_u32 s24, s5, s24
	s_mov_b64 exec, -1
	s_cmp_le_u32 s79, 14
	s_cbranch_scc1 .Lsel_p2_bend
	v_lshrrev_b32_e32 v134, 21, v126
	v_cmpx_eq_u32_e32 vcc, s13, v134
	v_bfe_u32 v134, v126, 10, 11
	v_lshl_add_u32 v134, v134, 2, s52
	ds_add_u32 v134, v57
	v_mbcnt_lo_u32_b32 v134, vcc_lo, 0
	v_mbcnt_hi_u32_b32 v134, vcc_hi, v134
	v_lshl_add_u32 v134, v134, 2, s24
	ds_write_b32 v134, v126
	s_bcnt1_i32_b64 s5, vcc
	s_and_b32 s5, s5, s25
	s_lshl2_add_u32 s24, s5, s24
	s_mov_b64 exec, -1
	v_lshrrev_b32_e32 v135, 21, v127
	v_cmpx_eq_u32_e32 vcc, s13, v135
	v_bfe_u32 v135, v127, 10, 11
	v_lshl_add_u32 v135, v135, 2, s52
	ds_add_u32 v135, v57
	v_mbcnt_lo_u32_b32 v135, vcc_lo, 0
	v_mbcnt_hi_u32_b32 v135, vcc_hi, v135
	v_lshl_add_u32 v135, v135, 2, s24
	ds_write_b32 v135, v127
	s_bcnt1_i32_b64 s5, vcc
	s_and_b32 s5, s5, s25
	s_lshl2_add_u32 s24, s5, s24
	s_mov_b64 exec, -1
	v_lshrrev_b32_e32 v136, 21, v128
	v_cmpx_eq_u32_e32 vcc, s13, v136
	v_bfe_u32 v136, v128, 10, 11
	v_lshl_add_u32 v136, v136, 2, s52
	ds_add_u32 v136, v57
	v_mbcnt_lo_u32_b32 v136, vcc_lo, 0
	v_mbcnt_hi_u32_b32 v136, vcc_hi, v136
	v_lshl_add_u32 v136, v136, 2, s24
	ds_write_b32 v136, v128
	s_bcnt1_i32_b64 s5, vcc
	s_and_b32 s5, s5, s25
	s_lshl2_add_u32 s24, s5, s24
	s_mov_b64 exec, -1
	v_lshrrev_b32_e32 v137, 21, v129
	v_cmpx_eq_u32_e32 vcc, s13, v137
	v_bfe_u32 v137, v129, 10, 11
	v_lshl_add_u32 v137, v137, 2, s52
	ds_add_u32 v137, v57
	v_mbcnt_lo_u32_b32 v137, vcc_lo, 0
	v_mbcnt_hi_u32_b32 v137, vcc_hi, v137
	v_lshl_add_u32 v137, v137, 2, s24
	ds_write_b32 v137, v129
	s_bcnt1_i32_b64 s5, vcc
	s_and_b32 s5, s5, s25
	s_lshl2_add_u32 s24, s5, s24
	s_mov_b64 exec, -1
	s_cmp_le_u32 s79, 15
	s_cbranch_scc1 .Lsel_p2_bend
	v_lshrrev_b32_e32 v134, 21, v130
	v_cmpx_eq_u32_e32 vcc, s13, v134
	v_bfe_u32 v134, v130, 10, 11
	v_lshl_add_u32 v134, v134, 2, s52
	ds_add_u32 v134, v57
	v_mbcnt_lo_u32_b32 v134, vcc_lo, 0
	v_mbcnt_hi_u32_b32 v134, vcc_hi, v134
	v_lshl_add_u32 v134, v134, 2, s24
	ds_write_b32 v134, v130
	s_bcnt1_i32_b64 s5, vcc
	s_and_b32 s5, s5, s25
	s_lshl2_add_u32 s24, s5, s24
	s_mov_b64 exec, -1
	v_lshrrev_b32_e32 v135, 21, v131
	v_cmpx_eq_u32_e32 vcc, s13, v135
	v_bfe_u32 v135, v131, 10, 11
	v_lshl_add_u32 v135, v135, 2, s52
	ds_add_u32 v135, v57
	v_mbcnt_lo_u32_b32 v135, vcc_lo, 0
	v_mbcnt_hi_u32_b32 v135, vcc_hi, v135
	v_lshl_add_u32 v135, v135, 2, s24
	ds_write_b32 v135, v131
	s_bcnt1_i32_b64 s5, vcc
	s_and_b32 s5, s5, s25
	s_lshl2_add_u32 s24, s5, s24
	s_mov_b64 exec, -1
	v_lshrrev_b32_e32 v136, 21, v132
	v_cmpx_eq_u32_e32 vcc, s13, v136
	v_bfe_u32 v136, v132, 10, 11
	v_lshl_add_u32 v136, v136, 2, s52
	ds_add_u32 v136, v57
	v_mbcnt_lo_u32_b32 v136, vcc_lo, 0
	v_mbcnt_hi_u32_b32 v136, vcc_hi, v136
	v_lshl_add_u32 v136, v136, 2, s24
	ds_write_b32 v136, v132
	s_bcnt1_i32_b64 s5, vcc
	s_and_b32 s5, s5, s25
	s_lshl2_add_u32 s24, s5, s24
	s_mov_b64 exec, -1
	v_lshrrev_b32_e32 v137, 21, v133
	v_cmpx_eq_u32_e32 vcc, s13, v137
	v_bfe_u32 v137, v133, 10, 11
	v_lshl_add_u32 v137, v137, 2, s52
	ds_add_u32 v137, v57
	v_mbcnt_lo_u32_b32 v137, vcc_lo, 0
	v_mbcnt_hi_u32_b32 v137, vcc_hi, v137
	v_lshl_add_u32 v137, v137, 2, s24
	ds_write_b32 v137, v133
	s_bcnt1_i32_b64 s5, vcc
	s_and_b32 s5, s5, s25
	s_lshl2_add_u32 s24, s5, s24
	s_mov_b64 exec, -1

.Lsel_ld5_end:
	s_waitcnt lgkmcnt(0)
	v_lshlrev_b32_e32 v34, 7, v50
	v_sub_u32_e32 v44, 0x1f80, v34
	s_cmp_lg_u32 s31, 0
	s_cselect_b64 vcc, -1, 0
	v_cndmask_b32_e32 v34, v34, v44, vcc
	v_add_u32_e32 v34, s52, v34
	ds_read_b128 v[2:5], v34
	ds_read_b128 v[6:9], v34 offset:16
	ds_read_b128 v[10:13], v34 offset:32
	ds_read_b128 v[14:17], v34 offset:48
	ds_read_b128 v[18:21], v34 offset:64
	ds_read_b128 v[22:25], v34 offset:80
	ds_read_b128 v[26:29], v34 offset:96
	ds_read_b128 v[30:33], v34 offset:112
	s_waitcnt lgkmcnt(0)
	v_add_u32_e32 v35, v2, v3
	v_add3_u32 v35, v35, v4, v5
	v_add3_u32 v35, v35, v6, v7
	v_add3_u32 v35, v35, v8, v9
	v_add3_u32 v35, v35, v10, v11
	v_add3_u32 v35, v35, v12, v13
	v_add3_u32 v35, v35, v14, v15
	v_add3_u32 v35, v35, v16, v17
	v_add3_u32 v35, v35, v18, v19
	v_add3_u32 v35, v35, v20, v21
	v_add3_u32 v35, v35, v22, v23
	v_add3_u32 v35, v35, v24, v25
	v_add3_u32 v35, v35, v26, v27
	v_add3_u32 v35, v35, v28, v29
	v_add3_u32 v35, v35, v30, v31
	v_add3_u32 v35, v35, v32, v33
	v_mov_b32_e32 v36, v35
	s_nop 1
	v_add_u32_dpp v36, v36, v36 row_shr:1 row_mask:0xf bank_mask:0xf bound_ctrl:1
	s_nop 1
	v_add_u32_dpp v36, v36, v36 row_shr:2 row_mask:0xf bank_mask:0xf bound_ctrl:1
	s_nop 1
	v_add_u32_dpp v36, v36, v36 row_shr:4 row_mask:0xf bank_mask:0xf bound_ctrl:1
	s_nop 1
	v_add_u32_dpp v36, v36, v36 row_shr:8 row_mask:0xf bank_mask:0xf bound_ctrl:1
	s_nop 1
	v_add_u32_dpp v36, v36, v36 row_bcast:15 row_mask:0xa bank_mask:0xf
	s_nop 1
	v_add_u32_dpp v36, v36, v36 row_bcast:31 row_mask:0xc bank_mask:0xf
	s_nop 0
	v_readlane_b32 s4, v36, 63
	s_nop 1
	v_sub_u32_e32 v37, s4, v36
	v_add_u32_e32 v38, v37, v35
	v_cmp_gt_u32_e32 vcc, s15, v37
	v_cmp_le_u32_e64 s[4:5], s15, v38
	s_and_b64 s[4:5], vcc, s[4:5]
	s_ff1_i32_b64 s6, s[4:5]
	v_readlane_b32 s7, v37, s6
	s_lshl_b32 s10, s6, 7
	s_sub_i32 s11, 0x1f80, s10
	s_add_i32 s10, s10, 124
	s_cmp_lg_u32 s31, 0
	s_cselect_b32 s10, s11, s10
	s_cselect_b32 s34, 1, -1
	s_add_i32 s10, s10, s52
	v_and_b32_e32 v39, 31, v50
	v_lshlrev_b32_e32 v39, 2, v39
	v_mul_i32_i24_e32 v39, s34, v39
	v_add_u32_e32 v39, s10, v39
	ds_read_b32 v40, v39
	v_cmp_gt_u32_e32 vcc, 32, v50
	s_waitcnt lgkmcnt(0)
	s_nop 1
	v_cndmask_b32_e32 v40, 0, v40, vcc
	v_mov_b32_e32 v41, v40
	s_nop 1
	v_add_u32_dpp v41, v41, v41 row_shr:1 row_mask:0xf bank_mask:0xf bound_ctrl:1
	s_nop 1
	v_add_u32_dpp v41, v41, v41 row_shr:2 row_mask:0xf bank_mask:0xf bound_ctrl:1
	s_nop 1
	v_add_u32_dpp v41, v41, v41 row_shr:4 row_mask:0xf bank_mask:0xf bound_ctrl:1
	s_nop 1
	v_add_u32_dpp v41, v41, v41 row_shr:8 row_mask:0xf bank_mask:0xf bound_ctrl:1
	s_nop 1
	v_add_u32_dpp v41, v41, v41 row_bcast:15 row_mask:0xa bank_mask:0xf
	s_nop 1
	v_add_u32_dpp v41, v41, v41 row_bcast:31 row_mask:0xc bank_mask:0xf
	s_nop 0
	v_sub_u32_e32 v42, v41, v40
	v_add_u32_e32 v42, s7, v42
	v_add_u32_e32 v43, v42, v40
	v_cmp_gt_u32_e32 vcc, s15, v42
	v_cmp_le_u32_e64 s[4:5], s15, v43
	s_and_b64 s[4:5], vcc, s[4:5]
	s_ff1_i32_b64 s11, s[4:5]
	v_readlane_b32 s29, v40, s11
	v_readlane_b32 s5, v42, s11
	s_lshl_b32 s28, s6, 5
	s_sub_i32 s4, 31, s11
	s_add_i32 s28, s28, s4
	s_sub_i32 s15, s15, s5
	s_sub_i32 s5, 0x7ff, s28
	s_cmp_lg_u32 s31, 0
	s_cselect_b32 s33, s5, s28
	s_lshl_b32 s4, s13, 11
	s_or_b32 s78, s4, s33
	s_lshl_b32 s4, s30, 11
	s_or_b32 s17, s4, s28
	ds_write_b128 v64, v[216:219]
	ds_write_b128 v64, v[216:219] offset:1024
	ds_write_b128 v64, v[216:219] offset:2048
	ds_write_b128 v64, v[216:219] offset:3072
	s_cmp_lg_u32 s25, 0
	s_cbranch_scc0 .Lsel_p3_row
	s_mov_b32 s10, 0

.Lsel_p3_done:
	s_waitcnt lgkmcnt(0)
	v_lshlrev_b32_e32 v34, 6, v50
	v_sub_u32_e32 v44, 0xfc0, v34
	s_cmp_lg_u32 s31, 0
	s_cselect_b64 vcc, -1, 0
	v_cndmask_b32_e32 v34, v34, v44, vcc
	v_add_u32_e32 v34, s52, v34
	ds_read_b128 v[2:5], v34
	ds_read_b128 v[6:9], v34 offset:16
	ds_read_b128 v[10:13], v34 offset:32
	ds_read_b128 v[14:17], v34 offset:48
	s_waitcnt lgkmcnt(0)
	v_add_u32_e32 v35, v2, v3
	v_add3_u32 v35, v35, v4, v5
	v_add3_u32 v35, v35, v6, v7
	v_add3_u32 v35, v35, v8, v9
	v_add3_u32 v35, v35, v10, v11
	v_add3_u32 v35, v35, v12, v13
	v_add3_u32 v35, v35, v14, v15
	v_add3_u32 v35, v35, v16, v17
	v_mov_b32_e32 v36, v35
	s_nop 1
	v_add_u32_dpp v36, v36, v36 row_shr:1 row_mask:0xf bank_mask:0xf bound_ctrl:1
	s_nop 1
	v_add_u32_dpp v36, v36, v36 row_shr:2 row_mask:0xf bank_mask:0xf bound_ctrl:1
	s_nop 1
	v_add_u32_dpp v36, v36, v36 row_shr:4 row_mask:0xf bank_mask:0xf bound_ctrl:1
	s_nop 1
	v_add_u32_dpp v36, v36, v36 row_shr:8 row_mask:0xf bank_mask:0xf bound_ctrl:1
	s_nop 1
	v_add_u32_dpp v36, v36, v36 row_bcast:15 row_mask:0xa bank_mask:0xf
	s_nop 1
	v_add_u32_dpp v36, v36, v36 row_bcast:31 row_mask:0xc bank_mask:0xf
	s_nop 0
	v_readlane_b32 s4, v36, 63
	s_nop 1
	v_sub_u32_e32 v37, s4, v36
	v_add_u32_e32 v38, v37, v35
	v_cmp_gt_u32_e32 vcc, s15, v37
	v_cmp_le_u32_e64 s[4:5], s15, v38
	s_and_b64 s[4:5], vcc, s[4:5]
	s_ff1_i32_b64 s6, s[4:5]
	v_readlane_b32 s7, v37, s6
	s_lshl_b32 s10, s6, 6
	s_sub_i32 s11, 0xfc0, s10
	s_add_i32 s10, s10, 60
	s_cmp_lg_u32 s31, 0
	s_cselect_b32 s10, s11, s10
	s_cselect_b32 s34, 1, -1
	s_add_i32 s10, s10, s52
	v_and_b32_e32 v39, 15, v50
	v_lshlrev_b32_e32 v39, 2, v39
	v_mul_i32_i24_e32 v39, s34, v39
	v_add_u32_e32 v39, s10, v39
	ds_read_b32 v40, v39
	v_cmp_gt_u32_e32 vcc, 16, v50
	s_waitcnt lgkmcnt(0)
	s_nop 1
	v_cndmask_b32_e32 v40, 0, v40, vcc
	v_mov_b32_e32 v41, v40
	s_nop 1
	v_add_u32_dpp v41, v41, v41 row_shr:1 row_mask:0xf bank_mask:0xf bound_ctrl:1
	s_nop 1
	v_add_u32_dpp v41, v41, v41 row_shr:2 row_mask:0xf bank_mask:0xf bound_ctrl:1
	s_nop 1
	v_add_u32_dpp v41, v41, v41 row_shr:4 row_mask:0xf bank_mask:0xf bound_ctrl:1
	s_nop 1
	v_add_u32_dpp v41, v41, v41 row_shr:8 row_mask:0xf bank_mask:0xf bound_ctrl:1
	s_nop 1
	v_add_u32_dpp v41, v41, v41 row_bcast:15 row_mask:0xa bank_mask:0xf
	s_nop 1
	v_add_u32_dpp v41, v41, v41 row_bcast:31 row_mask:0xc bank_mask:0xf
	s_nop 0
	v_sub_u32_e32 v42, v41, v40
	v_add_u32_e32 v42, s7, v42
	v_add_u32_e32 v43, v42, v40
	v_cmp_gt_u32_e32 vcc, s15, v42
	v_cmp_le_u32_e64 s[4:5], s15, v43
	s_and_b64 s[4:5], vcc, s[4:5]
	s_ff1_i32_b64 s11, s[4:5]
	v_readlane_b32 s29, v40, s11
	v_readlane_b32 s5, v42, s11
	s_lshl_b32 s28, s6, 4
	s_sub_i32 s4, 15, s11
	s_add_i32 s28, s28, s4
	s_sub_i32 s15, s15, s5
	s_sub_i32 s5, 0x3ff, s28
	s_cmp_lg_u32 s31, 0
	s_cselect_b32 s5, s5, s28
	s_lshl_b32 s76, s78, 10
	s_or_b32 s76, s76, s5
	s_lshl_b32 s17, s17, 10
	s_or_b32 s17, s17, s28
	s_mov_b32 s26, 0
	s_mov_b32 s27, 0
	s_cmp_eq_u32 s15, s29
	s_cbranch_scc1 .Lsel_simple
	s_mov_b32 s16, 0
	s_waitcnt vmcnt(0)

.Lsel_fin_body:
	v_add_u32_e32 v141, s16, v56
	v_ashrrev_i32_e32 v224, 31, v2
	v_or_b32_e32 v224, 0x80000000, v224
	v_xor_b32_e32 v224, v2, v224
	v_ashrrev_i32_e32 v225, 31, v3
	v_or_b32_e32 v225, 0x80000000, v225
	v_xor_b32_e32 v225, v3, v225
	v_ashrrev_i32_e32 v226, 31, v4
	v_or_b32_e32 v226, 0x80000000, v226
	v_xor_b32_e32 v226, v4, v226
	v_ashrrev_i32_e32 v227, 31, v5
	v_or_b32_e32 v227, 0x80000000, v227
	v_xor_b32_e32 v227, v5, v227
	v_cmp_lt_u32_e64 s[58:59], s17, v224
	v_cmp_eq_u32_e64 s[66:67], s17, v224
	v_cmp_lt_u32_e64 s[60:61], s17, v225
	v_cmp_eq_u32_e64 s[68:69], s17, v225
	v_cmp_lt_u32_e64 s[62:63], s17, v226
	v_cmp_eq_u32_e64 s[72:73], s17, v226
	v_cmp_lt_u32_e64 s[64:65], s17, v227
	v_cmp_eq_u32_e64 s[74:75], s17, v227
	s_or_b64 s[4:5], s[66:67], s[68:69]
	s_or_b64 s[6:7], s[72:73], s[74:75]
	s_or_b64 s[4:5], s[4:5], s[6:7]
	s_cmp_lg_u64 s[4:5], 0
	s_cbranch_scc0 .Lsel_fg_st0
	v_mov_b32_e32 v140, s27
	v_mbcnt_lo_u32_b32 v140, s66, v140
	v_mbcnt_hi_u32_b32 v140, s67, v140
	v_mbcnt_lo_u32_b32 v140, s68, v140
	v_mbcnt_hi_u32_b32 v140, s69, v140
	v_mbcnt_lo_u32_b32 v140, s72, v140
	v_mbcnt_hi_u32_b32 v140, s73, v140
	v_mbcnt_lo_u32_b32 v140, s74, v140
	v_mbcnt_hi_u32_b32 v140, s75, v140
	s_mov_b64 exec, s[66:67]
	v_cmp_gt_u32_e64 s[4:5], s15, v140
	v_add_u32_e32 v140, 1, v140
	s_or_b64 s[58:59], s[58:59], s[4:5]
	s_mov_b64 exec, s[68:69]
	v_cmp_gt_u32_e64 s[4:5], s15, v140
	v_add_u32_e32 v140, 1, v140
	s_or_b64 s[60:61], s[60:61], s[4:5]
	s_mov_b64 exec, s[72:73]
	v_cmp_gt_u32_e64 s[4:5], s15, v140
	v_add_u32_e32 v140, 1, v140
	s_or_b64 s[62:63], s[62:63], s[4:5]
	s_mov_b64 exec, s[74:75]
	v_cmp_gt_u32_e64 s[4:5], s15, v140
	v_add_u32_e32 v140, 1, v140
	s_or_b64 s[64:65], s[64:65], s[4:5]
	s_mov_b64 exec, -1
	s_bcnt1_i32_b64 s4, s[66:67]
	s_add_i32 s27, s27, s4
	s_bcnt1_i32_b64 s4, s[68:69]
	s_add_i32 s27, s27, s4
	s_bcnt1_i32_b64 s4, s[72:73]
	s_add_i32 s27, s27, s4
	s_bcnt1_i32_b64 s4, s[74:75]
	s_add_i32 s27, s27, s4
.Lsel_fg_st0:
	v_mov_b32_e32 v139, s26
	v_mbcnt_lo_u32_b32 v139, s58, v139
	v_mbcnt_hi_u32_b32 v139, s59, v139
	v_mbcnt_lo_u32_b32 v139, s60, v139
	v_mbcnt_hi_u32_b32 v139, s61, v139
	v_mbcnt_lo_u32_b32 v139, s62, v139
	v_mbcnt_hi_u32_b32 v139, s63, v139
	v_mbcnt_lo_u32_b32 v139, s64, v139
	v_mbcnt_hi_u32_b32 v139, s65, v139
	s_mov_b64 exec, s[58:59]
	v_lshlrev_b32_e32 v146, 2, v139
	v_add_u32_e32 v139, 1, v139
	v_add_u32_e32 v142, 0, v141
	v_cmpx_gt_u32_e32 vcc, 0x400, v146
	global_store_dword v146, v142, s[40:41]
	s_mov_b64 exec, s[60:61]
	v_lshlrev_b32_e32 v147, 2, v139
	v_add_u32_e32 v139, 1, v139
	v_add_u32_e32 v143, 1, v141
	v_cmpx_gt_u32_e32 vcc, 0x400, v147
	global_store_dword v147, v143, s[40:41]
	s_mov_b64 exec, s[62:63]
	v_lshlrev_b32_e32 v148, 2, v139
	v_add_u32_e32 v139, 1, v139
	v_add_u32_e32 v144, 2, v141
	v_cmpx_gt_u32_e32 vcc, 0x400, v148
	global_store_dword v148, v144, s[40:41]
	s_mov_b64 exec, s[64:65]
	v_lshlrev_b32_e32 v214, 2, v139
	v_add_u32_e32 v139, 1, v139
	v_add_u32_e32 v145, 3, v141
	v_cmpx_gt_u32_e32 vcc, 0x400, v214
	global_store_dword v214, v145, s[40:41]
	s_mov_b64 exec, -1
	s_bcnt1_i32_b64 s4, s[58:59]
	s_add_i32 s26, s26, s4
	s_bcnt1_i32_b64 s4, s[60:61]
	s_add_i32 s26, s26, s4
	s_bcnt1_i32_b64 s4, s[62:63]
	s_add_i32 s26, s26, s4
	s_bcnt1_i32_b64 s4, s[64:65]
	s_add_i32 s26, s26, s4
	s_cmp_le_u32 s79, 1
	s_cbranch_scc1 .Lsel_fin_bend
	v_ashrrev_i32_e32 v224, 31, v6
	v_or_b32_e32 v224, 0x80000000, v224
	v_xor_b32_e32 v224, v6, v224
	v_ashrrev_i32_e32 v225, 31, v7
	v_or_b32_e32 v225, 0x80000000, v225
	v_xor_b32_e32 v225, v7, v225
	v_ashrrev_i32_e32 v226, 31, v8
	v_or_b32_e32 v226, 0x80000000, v226
	v_xor_b32_e32 v226, v8, v226
	v_ashrrev_i32_e32 v227, 31, v9
	v_or_b32_e32 v227, 0x80000000, v227
	v_xor_b32_e32 v227, v9, v227
	v_cmp_lt_u32_e64 s[58:59], s17, v224
	v_cmp_eq_u32_e64 s[66:67], s17, v224
	v_cmp_lt_u32_e64 s[60:61], s17, v225
	v_cmp_eq_u32_e64 s[68:69], s17, v225
	v_cmp_lt_u32_e64 s[62:63], s17, v226
	v_cmp_eq_u32_e64 s[72:73], s17, v226
	v_cmp_lt_u32_e64 s[64:65], s17, v227
	v_cmp_eq_u32_e64 s[74:75], s17, v227
	s_or_b64 s[4:5], s[66:67], s[68:69]
	s_or_b64 s[6:7], s[72:73], s[74:75]
	s_or_b64 s[4:5], s[4:5], s[6:7]
	s_cmp_lg_u64 s[4:5], 0
	s_cbranch_scc0 .Lsel_fg_st1
	v_mov_b32_e32 v140, s27
	v_mbcnt_lo_u32_b32 v140, s66, v140
	v_mbcnt_hi_u32_b32 v140, s67, v140
	v_mbcnt_lo_u32_b32 v140, s68, v140
	v_mbcnt_hi_u32_b32 v140, s69, v140
	v_mbcnt_lo_u32_b32 v140, s72, v140
	v_mbcnt_hi_u32_b32 v140, s73, v140
	v_mbcnt_lo_u32_b32 v140, s74, v140
	v_mbcnt_hi_u32_b32 v140, s75, v140
	s_mov_b64 exec, s[66:67]
	v_cmp_gt_u32_e64 s[4:5], s15, v140
	v_add_u32_e32 v140, 1, v140
	s_or_b64 s[58:59], s[58:59], s[4:5]
	s_mov_b64 exec, s[68:69]
	v_cmp_gt_u32_e64 s[4:5], s15, v140
	v_add_u32_e32 v140, 1, v140
	s_or_b64 s[60:61], s[60:61], s[4:5]
	s_mov_b64 exec, s[72:73]
	v_cmp_gt_u32_e64 s[4:5], s15, v140
	v_add_u32_e32 v140, 1, v140
	s_or_b64 s[62:63], s[62:63], s[4:5]
	s_mov_b64 exec, s[74:75]
	v_cmp_gt_u32_e64 s[4:5], s15, v140
	v_add_u32_e32 v140, 1, v140
	s_or_b64 s[64:65], s[64:65], s[4:5]
	s_mov_b64 exec, -1
	s_bcnt1_i32_b64 s4, s[66:67]
	s_add_i32 s27, s27, s4
	s_bcnt1_i32_b64 s4, s[68:69]
	s_add_i32 s27, s27, s4
	s_bcnt1_i32_b64 s4, s[72:73]
	s_add_i32 s27, s27, s4
	s_bcnt1_i32_b64 s4, s[74:75]
	s_add_i32 s27, s27, s4
.Lsel_fg_st1:
	v_mov_b32_e32 v139, s26
	v_mbcnt_lo_u32_b32 v139, s58, v139
	v_mbcnt_hi_u32_b32 v139, s59, v139
	v_mbcnt_lo_u32_b32 v139, s60, v139
	v_mbcnt_hi_u32_b32 v139, s61, v139
	v_mbcnt_lo_u32_b32 v139, s62, v139
	v_mbcnt_hi_u32_b32 v139, s63, v139
	v_mbcnt_lo_u32_b32 v139, s64, v139
	v_mbcnt_hi_u32_b32 v139, s65, v139
	s_mov_b64 exec, s[58:59]
	v_lshlrev_b32_e32 v146, 2, v139
	v_add_u32_e32 v139, 1, v139
	v_add_u32_e32 v142, 0x100, v141
	v_cmpx_gt_u32_e32 vcc, 0x400, v146
	global_store_dword v146, v142, s[40:41]
	s_mov_b64 exec, s[60:61]
	v_lshlrev_b32_e32 v147, 2, v139
	v_add_u32_e32 v139, 1, v139
	v_add_u32_e32 v143, 0x101, v141
	v_cmpx_gt_u32_e32 vcc, 0x400, v147
	global_store_dword v147, v143, s[40:41]
	s_mov_b64 exec, s[62:63]
	v_lshlrev_b32_e32 v148, 2, v139
	v_add_u32_e32 v139, 1, v139
	v_add_u32_e32 v144, 0x102, v141
	v_cmpx_gt_u32_e32 vcc, 0x400, v148
	global_store_dword v148, v144, s[40:41]
	s_mov_b64 exec, s[64:65]
	v_lshlrev_b32_e32 v214, 2, v139
	v_add_u32_e32 v139, 1, v139
	v_add_u32_e32 v145, 0x103, v141
	v_cmpx_gt_u32_e32 vcc, 0x400, v214
	global_store_dword v214, v145, s[40:41]
	s_mov_b64 exec, -1
	s_bcnt1_i32_b64 s4, s[58:59]
	s_add_i32 s26, s26, s4
	s_bcnt1_i32_b64 s4, s[60:61]
	s_add_i32 s26, s26, s4
	s_bcnt1_i32_b64 s4, s[62:63]
	s_add_i32 s26, s26, s4
	s_bcnt1_i32_b64 s4, s[64:65]
	s_add_i32 s26, s26, s4
	s_cmp_le_u32 s79, 2
	s_cbranch_scc1 .Lsel_fin_bend
	v_ashrrev_i32_e32 v224, 31, v10
	v_or_b32_e32 v224, 0x80000000, v224
	v_xor_b32_e32 v224, v10, v224
	v_ashrrev_i32_e32 v225, 31, v11
	v_or_b32_e32 v225, 0x80000000, v225
	v_xor_b32_e32 v225, v11, v225
	v_ashrrev_i32_e32 v226, 31, v12
	v_or_b32_e32 v226, 0x80000000, v226
	v_xor_b32_e32 v226, v12, v226
	v_ashrrev_i32_e32 v227, 31, v13
	v_or_b32_e32 v227, 0x80000000, v227
	v_xor_b32_e32 v227, v13, v227
	v_cmp_lt_u32_e64 s[58:59], s17, v224
	v_cmp_eq_u32_e64 s[66:67], s17, v224
	v_cmp_lt_u32_e64 s[60:61], s17, v225
	v_cmp_eq_u32_e64 s[68:69], s17, v225
	v_cmp_lt_u32_e64 s[62:63], s17, v226
	v_cmp_eq_u32_e64 s[72:73], s17, v226
	v_cmp_lt_u32_e64 s[64:65], s17, v227
	v_cmp_eq_u32_e64 s[74:75], s17, v227
	s_or_b64 s[4:5], s[66:67], s[68:69]
	s_or_b64 s[6:7], s[72:73], s[74:75]
	s_or_b64 s[4:5], s[4:5], s[6:7]
	s_cmp_lg_u64 s[4:5], 0
	s_cbranch_scc0 .Lsel_fg_st2
	v_mov_b32_e32 v140, s27
	v_mbcnt_lo_u32_b32 v140, s66, v140
	v_mbcnt_hi_u32_b32 v140, s67, v140
	v_mbcnt_lo_u32_b32 v140, s68, v140
	v_mbcnt_hi_u32_b32 v140, s69, v140
	v_mbcnt_lo_u32_b32 v140, s72, v140
	v_mbcnt_hi_u32_b32 v140, s73, v140
	v_mbcnt_lo_u32_b32 v140, s74, v140
	v_mbcnt_hi_u32_b32 v140, s75, v140
	s_mov_b64 exec, s[66:67]
	v_cmp_gt_u32_e64 s[4:5], s15, v140
	v_add_u32_e32 v140, 1, v140
	s_or_b64 s[58:59], s[58:59], s[4:5]
	s_mov_b64 exec, s[68:69]
	v_cmp_gt_u32_e64 s[4:5], s15, v140
	v_add_u32_e32 v140, 1, v140
	s_or_b64 s[60:61], s[60:61], s[4:5]
	s_mov_b64 exec, s[72:73]
	v_cmp_gt_u32_e64 s[4:5], s15, v140
	v_add_u32_e32 v140, 1, v140
	s_or_b64 s[62:63], s[62:63], s[4:5]
	s_mov_b64 exec, s[74:75]
	v_cmp_gt_u32_e64 s[4:5], s15, v140
	v_add_u32_e32 v140, 1, v140
	s_or_b64 s[64:65], s[64:65], s[4:5]
	s_mov_b64 exec, -1
	s_bcnt1_i32_b64 s4, s[66:67]
	s_add_i32 s27, s27, s4
	s_bcnt1_i32_b64 s4, s[68:69]
	s_add_i32 s27, s27, s4
	s_bcnt1_i32_b64 s4, s[72:73]
	s_add_i32 s27, s27, s4
	s_bcnt1_i32_b64 s4, s[74:75]
	s_add_i32 s27, s27, s4
.Lsel_fg_st2:
	v_mov_b32_e32 v139, s26
	v_mbcnt_lo_u32_b32 v139, s58, v139
	v_mbcnt_hi_u32_b32 v139, s59, v139
	v_mbcnt_lo_u32_b32 v139, s60, v139
	v_mbcnt_hi_u32_b32 v139, s61, v139
	v_mbcnt_lo_u32_b32 v139, s62, v139
	v_mbcnt_hi_u32_b32 v139, s63, v139
	v_mbcnt_lo_u32_b32 v139, s64, v139
	v_mbcnt_hi_u32_b32 v139, s65, v139
	s_mov_b64 exec, s[58:59]
	v_lshlrev_b32_e32 v146, 2, v139
	v_add_u32_e32 v139, 1, v139
	v_add_u32_e32 v142, 0x200, v141
	v_cmpx_gt_u32_e32 vcc, 0x400, v146
	global_store_dword v146, v142, s[40:41]
	s_mov_b64 exec, s[60:61]
	v_lshlrev_b32_e32 v147, 2, v139
	v_add_u32_e32 v139, 1, v139
	v_add_u32_e32 v143, 0x201, v141
	v_cmpx_gt_u32_e32 vcc, 0x400, v147
	global_store_dword v147, v143, s[40:41]
	s_mov_b64 exec, s[62:63]
	v_lshlrev_b32_e32 v148, 2, v139
	v_add_u32_e32 v139, 1, v139
	v_add_u32_e32 v144, 0x202, v141
	v_cmpx_gt_u32_e32 vcc, 0x400, v148
	global_store_dword v148, v144, s[40:41]
	s_mov_b64 exec, s[64:65]
	v_lshlrev_b32_e32 v214, 2, v139
	v_add_u32_e32 v139, 1, v139
	v_add_u32_e32 v145, 0x203, v141
	v_cmpx_gt_u32_e32 vcc, 0x400, v214
	global_store_dword v214, v145, s[40:41]
	s_mov_b64 exec, -1
	s_bcnt1_i32_b64 s4, s[58:59]
	s_add_i32 s26, s26, s4
	s_bcnt1_i32_b64 s4, s[60:61]
	s_add_i32 s26, s26, s4
	s_bcnt1_i32_b64 s4, s[62:63]
	s_add_i32 s26, s26, s4
	s_bcnt1_i32_b64 s4, s[64:65]
	s_add_i32 s26, s26, s4
	s_cmp_le_u32 s79, 3
	s_cbranch_scc1 .Lsel_fin_bend
	v_ashrrev_i32_e32 v224, 31, v14
	v_or_b32_e32 v224, 0x80000000, v224
	v_xor_b32_e32 v224, v14, v224
	v_ashrrev_i32_e32 v225, 31, v15
	v_or_b32_e32 v225, 0x80000000, v225
	v_xor_b32_e32 v225, v15, v225
	v_ashrrev_i32_e32 v226, 31, v16
	v_or_b32_e32 v226, 0x80000000, v226
	v_xor_b32_e32 v226, v16, v226
	v_ashrrev_i32_e32 v227, 31, v17
	v_or_b32_e32 v227, 0x80000000, v227
	v_xor_b32_e32 v227, v17, v227
	v_cmp_lt_u32_e64 s[58:59], s17, v224
	v_cmp_eq_u32_e64 s[66:67], s17, v224
	v_cmp_lt_u32_e64 s[60:61], s17, v225
	v_cmp_eq_u32_e64 s[68:69], s17, v225
	v_cmp_lt_u32_e64 s[62:63], s17, v226
	v_cmp_eq_u32_e64 s[72:73], s17, v226
	v_cmp_lt_u32_e64 s[64:65], s17, v227
	v_cmp_eq_u32_e64 s[74:75], s17, v227
	s_or_b64 s[4:5], s[66:67], s[68:69]
	s_or_b64 s[6:7], s[72:73], s[74:75]
	s_or_b64 s[4:5], s[4:5], s[6:7]
	s_cmp_lg_u64 s[4:5], 0
	s_cbranch_scc0 .Lsel_fg_st3
	v_mov_b32_e32 v140, s27
	v_mbcnt_lo_u32_b32 v140, s66, v140
	v_mbcnt_hi_u32_b32 v140, s67, v140
	v_mbcnt_lo_u32_b32 v140, s68, v140
	v_mbcnt_hi_u32_b32 v140, s69, v140
	v_mbcnt_lo_u32_b32 v140, s72, v140
	v_mbcnt_hi_u32_b32 v140, s73, v140
	v_mbcnt_lo_u32_b32 v140, s74, v140
	v_mbcnt_hi_u32_b32 v140, s75, v140
	s_mov_b64 exec, s[66:67]
	v_cmp_gt_u32_e64 s[4:5], s15, v140
	v_add_u32_e32 v140, 1, v140
	s_or_b64 s[58:59], s[58:59], s[4:5]
	s_mov_b64 exec, s[68:69]
	v_cmp_gt_u32_e64 s[4:5], s15, v140
	v_add_u32_e32 v140, 1, v140
	s_or_b64 s[60:61], s[60:61], s[4:5]
	s_mov_b64 exec, s[72:73]
	v_cmp_gt_u32_e64 s[4:5], s15, v140
	v_add_u32_e32 v140, 1, v140
	s_or_b64 s[62:63], s[62:63], s[4:5]
	s_mov_b64 exec, s[74:75]
	v_cmp_gt_u32_e64 s[4:5], s15, v140
	v_add_u32_e32 v140, 1, v140
	s_or_b64 s[64:65], s[64:65], s[4:5]
	s_mov_b64 exec, -1
	s_bcnt1_i32_b64 s4, s[66:67]
	s_add_i32 s27, s27, s4
	s_bcnt1_i32_b64 s4, s[68:69]
	s_add_i32 s27, s27, s4
	s_bcnt1_i32_b64 s4, s[72:73]
	s_add_i32 s27, s27, s4
	s_bcnt1_i32_b64 s4, s[74:75]
	s_add_i32 s27, s27, s4
.Lsel_fg_st3:
	v_mov_b32_e32 v139, s26
	v_mbcnt_lo_u32_b32 v139, s58, v139
	v_mbcnt_hi_u32_b32 v139, s59, v139
	v_mbcnt_lo_u32_b32 v139, s60, v139
	v_mbcnt_hi_u32_b32 v139, s61, v139
	v_mbcnt_lo_u32_b32 v139, s62, v139
	v_mbcnt_hi_u32_b32 v139, s63, v139
	v_mbcnt_lo_u32_b32 v139, s64, v139
	v_mbcnt_hi_u32_b32 v139, s65, v139
	s_mov_b64 exec, s[58:59]
	v_lshlrev_b32_e32 v146, 2, v139
	v_add_u32_e32 v139, 1, v139
	v_add_u32_e32 v142, 0x300, v141
	v_cmpx_gt_u32_e32 vcc, 0x400, v146
	global_store_dword v146, v142, s[40:41]
	s_mov_b64 exec, s[60:61]
	v_lshlrev_b32_e32 v147, 2, v139
	v_add_u32_e32 v139, 1, v139
	v_add_u32_e32 v143, 0x301, v141
	v_cmpx_gt_u32_e32 vcc, 0x400, v147
	global_store_dword v147, v143, s[40:41]
	s_mov_b64 exec, s[62:63]
	v_lshlrev_b32_e32 v148, 2, v139
	v_add_u32_e32 v139, 1, v139
	v_add_u32_e32 v144, 0x302, v141
	v_cmpx_gt_u32_e32 vcc, 0x400, v148
	global_store_dword v148, v144, s[40:41]
	s_mov_b64 exec, s[64:65]
	v_lshlrev_b32_e32 v214, 2, v139
	v_add_u32_e32 v139, 1, v139
	v_add_u32_e32 v145, 0x303, v141
	v_cmpx_gt_u32_e32 vcc, 0x400, v214
	global_store_dword v214, v145, s[40:41]
	s_mov_b64 exec, -1
	s_bcnt1_i32_b64 s4, s[58:59]
	s_add_i32 s26, s26, s4
	s_bcnt1_i32_b64 s4, s[60:61]
	s_add_i32 s26, s26, s4
	s_bcnt1_i32_b64 s4, s[62:63]
	s_add_i32 s26, s26, s4
	s_bcnt1_i32_b64 s4, s[64:65]
	s_add_i32 s26, s26, s4
	s_cmp_le_u32 s79, 4
	s_cbranch_scc1 .Lsel_fin_bend
	v_ashrrev_i32_e32 v224, 31, v18
	v_or_b32_e32 v224, 0x80000000, v224
	v_xor_b32_e32 v224, v18, v224
	v_ashrrev_i32_e32 v225, 31, v19
	v_or_b32_e32 v225, 0x80000000, v225
	v_xor_b32_e32 v225, v19, v225
	v_ashrrev_i32_e32 v226, 31, v20
	v_or_b32_e32 v226, 0x80000000, v226
	v_xor_b32_e32 v226, v20, v226
	v_ashrrev_i32_e32 v227, 31, v21
	v_or_b32_e32 v227, 0x80000000, v227
	v_xor_b32_e32 v227, v21, v227
	v_cmp_lt_u32_e64 s[58:59], s17, v224
	v_cmp_eq_u32_e64 s[66:67], s17, v224
	v_cmp_lt_u32_e64 s[60:61], s17, v225
	v_cmp_eq_u32_e64 s[68:69], s17, v225
	v_cmp_lt_u32_e64 s[62:63], s17, v226
	v_cmp_eq_u32_e64 s[72:73], s17, v226
	v_cmp_lt_u32_e64 s[64:65], s17, v227
	v_cmp_eq_u32_e64 s[74:75], s17, v227
	s_or_b64 s[4:5], s[66:67], s[68:69]
	s_or_b64 s[6:7], s[72:73], s[74:75]
	s_or_b64 s[4:5], s[4:5], s[6:7]
	s_cmp_lg_u64 s[4:5], 0
	s_cbranch_scc0 .Lsel_fg_st4
	v_mov_b32_e32 v140, s27
	v_mbcnt_lo_u32_b32 v140, s66, v140
	v_mbcnt_hi_u32_b32 v140, s67, v140
	v_mbcnt_lo_u32_b32 v140, s68, v140
	v_mbcnt_hi_u32_b32 v140, s69, v140
	v_mbcnt_lo_u32_b32 v140, s72, v140
	v_mbcnt_hi_u32_b32 v140, s73, v140
	v_mbcnt_lo_u32_b32 v140, s74, v140
	v_mbcnt_hi_u32_b32 v140, s75, v140
	s_mov_b64 exec, s[66:67]
	v_cmp_gt_u32_e64 s[4:5], s15, v140
	v_add_u32_e32 v140, 1, v140
	s_or_b64 s[58:59], s[58:59], s[4:5]
	s_mov_b64 exec, s[68:69]
	v_cmp_gt_u32_e64 s[4:5], s15, v140
	v_add_u32_e32 v140, 1, v140
	s_or_b64 s[60:61], s[60:61], s[4:5]
	s_mov_b64 exec, s[72:73]
	v_cmp_gt_u32_e64 s[4:5], s15, v140
	v_add_u32_e32 v140, 1, v140
	s_or_b64 s[62:63], s[62:63], s[4:5]
	s_mov_b64 exec, s[74:75]
	v_cmp_gt_u32_e64 s[4:5], s15, v140
	v_add_u32_e32 v140, 1, v140
	s_or_b64 s[64:65], s[64:65], s[4:5]
	s_mov_b64 exec, -1
	s_bcnt1_i32_b64 s4, s[66:67]
	s_add_i32 s27, s27, s4
	s_bcnt1_i32_b64 s4, s[68:69]
	s_add_i32 s27, s27, s4
	s_bcnt1_i32_b64 s4, s[72:73]
	s_add_i32 s27, s27, s4
	s_bcnt1_i32_b64 s4, s[74:75]
	s_add_i32 s27, s27, s4
.Lsel_fg_st4:
	v_mov_b32_e32 v139, s26
	v_mbcnt_lo_u32_b32 v139, s58, v139
	v_mbcnt_hi_u32_b32 v139, s59, v139
	v_mbcnt_lo_u32_b32 v139, s60, v139
	v_mbcnt_hi_u32_b32 v139, s61, v139
	v_mbcnt_lo_u32_b32 v139, s62, v139
	v_mbcnt_hi_u32_b32 v139, s63, v139
	v_mbcnt_lo_u32_b32 v139, s64, v139
	v_mbcnt_hi_u32_b32 v139, s65, v139
	s_mov_b64 exec, s[58:59]
	v_lshlrev_b32_e32 v146, 2, v139
	v_add_u32_e32 v139, 1, v139
	v_add_u32_e32 v142, 0x400, v141
	v_cmpx_gt_u32_e32 vcc, 0x400, v146
	global_store_dword v146, v142, s[40:41]
	s_mov_b64 exec, s[60:61]
	v_lshlrev_b32_e32 v147, 2, v139
	v_add_u32_e32 v139, 1, v139
	v_add_u32_e32 v143, 0x401, v141
	v_cmpx_gt_u32_e32 vcc, 0x400, v147
	global_store_dword v147, v143, s[40:41]
	s_mov_b64 exec, s[62:63]
	v_lshlrev_b32_e32 v148, 2, v139
	v_add_u32_e32 v139, 1, v139
	v_add_u32_e32 v144, 0x402, v141
	v_cmpx_gt_u32_e32 vcc, 0x400, v148
	global_store_dword v148, v144, s[40:41]
	s_mov_b64 exec, s[64:65]
	v_lshlrev_b32_e32 v214, 2, v139
	v_add_u32_e32 v139, 1, v139
	v_add_u32_e32 v145, 0x403, v141
	v_cmpx_gt_u32_e32 vcc, 0x400, v214
	global_store_dword v214, v145, s[40:41]
	s_mov_b64 exec, -1
	s_bcnt1_i32_b64 s4, s[58:59]
	s_add_i32 s26, s26, s4
	s_bcnt1_i32_b64 s4, s[60:61]
	s_add_i32 s26, s26, s4
	s_bcnt1_i32_b64 s4, s[62:63]
	s_add_i32 s26, s26, s4
	s_bcnt1_i32_b64 s4, s[64:65]
	s_add_i32 s26, s26, s4
	s_cmp_le_u32 s79, 5
	s_cbranch_scc1 .Lsel_fin_bend
	v_ashrrev_i32_e32 v224, 31, v22
	v_or_b32_e32 v224, 0x80000000, v224
	v_xor_b32_e32 v224, v22, v224
	v_ashrrev_i32_e32 v225, 31, v23
	v_or_b32_e32 v225, 0x80000000, v225
	v_xor_b32_e32 v225, v23, v225
	v_ashrrev_i32_e32 v226, 31, v24
	v_or_b32_e32 v226, 0x80000000, v226
	v_xor_b32_e32 v226, v24, v226
	v_ashrrev_i32_e32 v227, 31, v25
	v_or_b32_e32 v227, 0x80000000, v227
	v_xor_b32_e32 v227, v25, v227
	v_cmp_lt_u32_e64 s[58:59], s17, v224
	v_cmp_eq_u32_e64 s[66:67], s17, v224
	v_cmp_lt_u32_e64 s[60:61], s17, v225
	v_cmp_eq_u32_e64 s[68:69], s17, v225
	v_cmp_lt_u32_e64 s[62:63], s17, v226
	v_cmp_eq_u32_e64 s[72:73], s17, v226
	v_cmp_lt_u32_e64 s[64:65], s17, v227
	v_cmp_eq_u32_e64 s[74:75], s17, v227
	s_or_b64 s[4:5], s[66:67], s[68:69]
	s_or_b64 s[6:7], s[72:73], s[74:75]
	s_or_b64 s[4:5], s[4:5], s[6:7]
	s_cmp_lg_u64 s[4:5], 0
	s_cbranch_scc0 .Lsel_fg_st5
	v_mov_b32_e32 v140, s27
	v_mbcnt_lo_u32_b32 v140, s66, v140
	v_mbcnt_hi_u32_b32 v140, s67, v140
	v_mbcnt_lo_u32_b32 v140, s68, v140
	v_mbcnt_hi_u32_b32 v140, s69, v140
	v_mbcnt_lo_u32_b32 v140, s72, v140
	v_mbcnt_hi_u32_b32 v140, s73, v140
	v_mbcnt_lo_u32_b32 v140, s74, v140
	v_mbcnt_hi_u32_b32 v140, s75, v140
	s_mov_b64 exec, s[66:67]
	v_cmp_gt_u32_e64 s[4:5], s15, v140
	v_add_u32_e32 v140, 1, v140
	s_or_b64 s[58:59], s[58:59], s[4:5]
	s_mov_b64 exec, s[68:69]
	v_cmp_gt_u32_e64 s[4:5], s15, v140
	v_add_u32_e32 v140, 1, v140
	s_or_b64 s[60:61], s[60:61], s[4:5]
	s_mov_b64 exec, s[72:73]
	v_cmp_gt_u32_e64 s[4:5], s15, v140
	v_add_u32_e32 v140, 1, v140
	s_or_b64 s[62:63], s[62:63], s[4:5]
	s_mov_b64 exec, s[74:75]
	v_cmp_gt_u32_e64 s[4:5], s15, v140
	v_add_u32_e32 v140, 1, v140
	s_or_b64 s[64:65], s[64:65], s[4:5]
	s_mov_b64 exec, -1
	s_bcnt1_i32_b64 s4, s[66:67]
	s_add_i32 s27, s27, s4
	s_bcnt1_i32_b64 s4, s[68:69]
	s_add_i32 s27, s27, s4
	s_bcnt1_i32_b64 s4, s[72:73]
	s_add_i32 s27, s27, s4
	s_bcnt1_i32_b64 s4, s[74:75]
	s_add_i32 s27, s27, s4
.Lsel_fg_st5:
	v_mov_b32_e32 v139, s26
	v_mbcnt_lo_u32_b32 v139, s58, v139
	v_mbcnt_hi_u32_b32 v139, s59, v139
	v_mbcnt_lo_u32_b32 v139, s60, v139
	v_mbcnt_hi_u32_b32 v139, s61, v139
	v_mbcnt_lo_u32_b32 v139, s62, v139
	v_mbcnt_hi_u32_b32 v139, s63, v139
	v_mbcnt_lo_u32_b32 v139, s64, v139
	v_mbcnt_hi_u32_b32 v139, s65, v139
	s_mov_b64 exec, s[58:59]
	v_lshlrev_b32_e32 v146, 2, v139
	v_add_u32_e32 v139, 1, v139
	v_add_u32_e32 v142, 0x500, v141
	v_cmpx_gt_u32_e32 vcc, 0x400, v146
	global_store_dword v146, v142, s[40:41]
	s_mov_b64 exec, s[60:61]
	v_lshlrev_b32_e32 v147, 2, v139
	v_add_u32_e32 v139, 1, v139
	v_add_u32_e32 v143, 0x501, v141
	v_cmpx_gt_u32_e32 vcc, 0x400, v147
	global_store_dword v147, v143, s[40:41]
	s_mov_b64 exec, s[62:63]
	v_lshlrev_b32_e32 v148, 2, v139
	v_add_u32_e32 v139, 1, v139
	v_add_u32_e32 v144, 0x502, v141
	v_cmpx_gt_u32_e32 vcc, 0x400, v148
	global_store_dword v148, v144, s[40:41]
	s_mov_b64 exec, s[64:65]
	v_lshlrev_b32_e32 v214, 2, v139
	v_add_u32_e32 v139, 1, v139
	v_add_u32_e32 v145, 0x503, v141
	v_cmpx_gt_u32_e32 vcc, 0x400, v214
	global_store_dword v214, v145, s[40:41]
	s_mov_b64 exec, -1
	s_bcnt1_i32_b64 s4, s[58:59]
	s_add_i32 s26, s26, s4
	s_bcnt1_i32_b64 s4, s[60:61]
	s_add_i32 s26, s26, s4
	s_bcnt1_i32_b64 s4, s[62:63]
	s_add_i32 s26, s26, s4
	s_bcnt1_i32_b64 s4, s[64:65]
	s_add_i32 s26, s26, s4
	s_cmp_le_u32 s79, 6
	s_cbranch_scc1 .Lsel_fin_bend
	v_ashrrev_i32_e32 v224, 31, v26
	v_or_b32_e32 v224, 0x80000000, v224
	v_xor_b32_e32 v224, v26, v224
	v_ashrrev_i32_e32 v225, 31, v27
	v_or_b32_e32 v225, 0x80000000, v225
	v_xor_b32_e32 v225, v27, v225
	v_ashrrev_i32_e32 v226, 31, v28
	v_or_b32_e32 v226, 0x80000000, v226
	v_xor_b32_e32 v226, v28, v226
	v_ashrrev_i32_e32 v227, 31, v29
	v_or_b32_e32 v227, 0x80000000, v227
	v_xor_b32_e32 v227, v29, v227
	v_cmp_lt_u32_e64 s[58:59], s17, v224
	v_cmp_eq_u32_e64 s[66:67], s17, v224
	v_cmp_lt_u32_e64 s[60:61], s17, v225
	v_cmp_eq_u32_e64 s[68:69], s17, v225
	v_cmp_lt_u32_e64 s[62:63], s17, v226
	v_cmp_eq_u32_e64 s[72:73], s17, v226
	v_cmp_lt_u32_e64 s[64:65], s17, v227
	v_cmp_eq_u32_e64 s[74:75], s17, v227
	s_or_b64 s[4:5], s[66:67], s[68:69]
	s_or_b64 s[6:7], s[72:73], s[74:75]
	s_or_b64 s[4:5], s[4:5], s[6:7]
	s_cmp_lg_u64 s[4:5], 0
	s_cbranch_scc0 .Lsel_fg_st6
	v_mov_b32_e32 v140, s27
	v_mbcnt_lo_u32_b32 v140, s66, v140
	v_mbcnt_hi_u32_b32 v140, s67, v140
	v_mbcnt_lo_u32_b32 v140, s68, v140
	v_mbcnt_hi_u32_b32 v140, s69, v140
	v_mbcnt_lo_u32_b32 v140, s72, v140
	v_mbcnt_hi_u32_b32 v140, s73, v140
	v_mbcnt_lo_u32_b32 v140, s74, v140
	v_mbcnt_hi_u32_b32 v140, s75, v140
	s_mov_b64 exec, s[66:67]
	v_cmp_gt_u32_e64 s[4:5], s15, v140
	v_add_u32_e32 v140, 1, v140
	s_or_b64 s[58:59], s[58:59], s[4:5]
	s_mov_b64 exec, s[68:69]
	v_cmp_gt_u32_e64 s[4:5], s15, v140
	v_add_u32_e32 v140, 1, v140
	s_or_b64 s[60:61], s[60:61], s[4:5]
	s_mov_b64 exec, s[72:73]
	v_cmp_gt_u32_e64 s[4:5], s15, v140
	v_add_u32_e32 v140, 1, v140
	s_or_b64 s[62:63], s[62:63], s[4:5]
	s_mov_b64 exec, s[74:75]
	v_cmp_gt_u32_e64 s[4:5], s15, v140
	v_add_u32_e32 v140, 1, v140
	s_or_b64 s[64:65], s[64:65], s[4:5]
	s_mov_b64 exec, -1
	s_bcnt1_i32_b64 s4, s[66:67]
	s_add_i32 s27, s27, s4
	s_bcnt1_i32_b64 s4, s[68:69]
	s_add_i32 s27, s27, s4
	s_bcnt1_i32_b64 s4, s[72:73]
	s_add_i32 s27, s27, s4
	s_bcnt1_i32_b64 s4, s[74:75]
	s_add_i32 s27, s27, s4
.Lsel_fg_st6:
	v_mov_b32_e32 v139, s26
	v_mbcnt_lo_u32_b32 v139, s58, v139
	v_mbcnt_hi_u32_b32 v139, s59, v139
	v_mbcnt_lo_u32_b32 v139, s60, v139
	v_mbcnt_hi_u32_b32 v139, s61, v139
	v_mbcnt_lo_u32_b32 v139, s62, v139
	v_mbcnt_hi_u32_b32 v139, s63, v139
	v_mbcnt_lo_u32_b32 v139, s64, v139
	v_mbcnt_hi_u32_b32 v139, s65, v139
	s_mov_b64 exec, s[58:59]
	v_lshlrev_b32_e32 v146, 2, v139
	v_add_u32_e32 v139, 1, v139
	v_add_u32_e32 v142, 0x600, v141
	v_cmpx_gt_u32_e32 vcc, 0x400, v146
	global_store_dword v146, v142, s[40:41]
	s_mov_b64 exec, s[60:61]
	v_lshlrev_b32_e32 v147, 2, v139
	v_add_u32_e32 v139, 1, v139
	v_add_u32_e32 v143, 0x601, v141
	v_cmpx_gt_u32_e32 vcc, 0x400, v147
	global_store_dword v147, v143, s[40:41]
	s_mov_b64 exec, s[62:63]
	v_lshlrev_b32_e32 v148, 2, v139
	v_add_u32_e32 v139, 1, v139
	v_add_u32_e32 v144, 0x602, v141
	v_cmpx_gt_u32_e32 vcc, 0x400, v148
	global_store_dword v148, v144, s[40:41]
	s_mov_b64 exec, s[64:65]
	v_lshlrev_b32_e32 v214, 2, v139
	v_add_u32_e32 v139, 1, v139
	v_add_u32_e32 v145, 0x603, v141
	v_cmpx_gt_u32_e32 vcc, 0x400, v214
	global_store_dword v214, v145, s[40:41]
	s_mov_b64 exec, -1
	s_bcnt1_i32_b64 s4, s[58:59]
	s_add_i32 s26, s26, s4
	s_bcnt1_i32_b64 s4, s[60:61]
	s_add_i32 s26, s26, s4
	s_bcnt1_i32_b64 s4, s[62:63]
	s_add_i32 s26, s26, s4
	s_bcnt1_i32_b64 s4, s[64:65]
	s_add_i32 s26, s26, s4
	s_cmp_le_u32 s79, 7
	s_cbranch_scc1 .Lsel_fin_bend
	v_ashrrev_i32_e32 v224, 31, v30
	v_or_b32_e32 v224, 0x80000000, v224
	v_xor_b32_e32 v224, v30, v224
	v_ashrrev_i32_e32 v225, 31, v31
	v_or_b32_e32 v225, 0x80000000, v225
	v_xor_b32_e32 v225, v31, v225
	v_ashrrev_i32_e32 v226, 31, v32
	v_or_b32_e32 v226, 0x80000000, v226
	v_xor_b32_e32 v226, v32, v226
	v_ashrrev_i32_e32 v227, 31, v33
	v_or_b32_e32 v227, 0x80000000, v227
	v_xor_b32_e32 v227, v33, v227
	v_cmp_lt_u32_e64 s[58:59], s17, v224
	v_cmp_eq_u32_e64 s[66:67], s17, v224
	v_cmp_lt_u32_e64 s[60:61], s17, v225
	v_cmp_eq_u32_e64 s[68:69], s17, v225
	v_cmp_lt_u32_e64 s[62:63], s17, v226
	v_cmp_eq_u32_e64 s[72:73], s17, v226
	v_cmp_lt_u32_e64 s[64:65], s17, v227
	v_cmp_eq_u32_e64 s[74:75], s17, v227
	s_or_b64 s[4:5], s[66:67], s[68:69]
	s_or_b64 s[6:7], s[72:73], s[74:75]
	s_or_b64 s[4:5], s[4:5], s[6:7]
	s_cmp_lg_u64 s[4:5], 0
	s_cbranch_scc0 .Lsel_fg_st7
	v_mov_b32_e32 v140, s27
	v_mbcnt_lo_u32_b32 v140, s66, v140
	v_mbcnt_hi_u32_b32 v140, s67, v140
	v_mbcnt_lo_u32_b32 v140, s68, v140
	v_mbcnt_hi_u32_b32 v140, s69, v140
	v_mbcnt_lo_u32_b32 v140, s72, v140
	v_mbcnt_hi_u32_b32 v140, s73, v140
	v_mbcnt_lo_u32_b32 v140, s74, v140
	v_mbcnt_hi_u32_b32 v140, s75, v140
	s_mov_b64 exec, s[66:67]
	v_cmp_gt_u32_e64 s[4:5], s15, v140
	v_add_u32_e32 v140, 1, v140
	s_or_b64 s[58:59], s[58:59], s[4:5]
	s_mov_b64 exec, s[68:69]
	v_cmp_gt_u32_e64 s[4:5], s15, v140
	v_add_u32_e32 v140, 1, v140
	s_or_b64 s[60:61], s[60:61], s[4:5]
	s_mov_b64 exec, s[72:73]
	v_cmp_gt_u32_e64 s[4:5], s15, v140
	v_add_u32_e32 v140, 1, v140
	s_or_b64 s[62:63], s[62:63], s[4:5]
	s_mov_b64 exec, s[74:75]
	v_cmp_gt_u32_e64 s[4:5], s15, v140
	v_add_u32_e32 v140, 1, v140
	s_or_b64 s[64:65], s[64:65], s[4:5]
	s_mov_b64 exec, -1
	s_bcnt1_i32_b64 s4, s[66:67]
	s_add_i32 s27, s27, s4
	s_bcnt1_i32_b64 s4, s[68:69]
	s_add_i32 s27, s27, s4
	s_bcnt1_i32_b64 s4, s[72:73]
	s_add_i32 s27, s27, s4
	s_bcnt1_i32_b64 s4, s[74:75]
	s_add_i32 s27, s27, s4
.Lsel_fg_st7:
	v_mov_b32_e32 v139, s26
	v_mbcnt_lo_u32_b32 v139, s58, v139
	v_mbcnt_hi_u32_b32 v139, s59, v139
	v_mbcnt_lo_u32_b32 v139, s60, v139
	v_mbcnt_hi_u32_b32 v139, s61, v139
	v_mbcnt_lo_u32_b32 v139, s62, v139
	v_mbcnt_hi_u32_b32 v139, s63, v139
	v_mbcnt_lo_u32_b32 v139, s64, v139
	v_mbcnt_hi_u32_b32 v139, s65, v139
	s_mov_b64 exec, s[58:59]
	v_lshlrev_b32_e32 v146, 2, v139
	v_add_u32_e32 v139, 1, v139
	v_add_u32_e32 v142, 0x700, v141
	v_cmpx_gt_u32_e32 vcc, 0x400, v146
	global_store_dword v146, v142, s[40:41]
	s_mov_b64 exec, s[60:61]
	v_lshlrev_b32_e32 v147, 2, v139
	v_add_u32_e32 v139, 1, v139
	v_add_u32_e32 v143, 0x701, v141
	v_cmpx_gt_u32_e32 vcc, 0x400, v147
	global_store_dword v147, v143, s[40:41]
	s_mov_b64 exec, s[62:63]
	v_lshlrev_b32_e32 v148, 2, v139
	v_add_u32_e32 v139, 1, v139
	v_add_u32_e32 v144, 0x702, v141
	v_cmpx_gt_u32_e32 vcc, 0x400, v148
	global_store_dword v148, v144, s[40:41]
	s_mov_b64 exec, s[64:65]
	v_lshlrev_b32_e32 v214, 2, v139
	v_add_u32_e32 v139, 1, v139
	v_add_u32_e32 v145, 0x703, v141
	v_cmpx_gt_u32_e32 vcc, 0x400, v214
	global_store_dword v214, v145, s[40:41]
	s_mov_b64 exec, -1
	s_bcnt1_i32_b64 s4, s[58:59]
	s_add_i32 s26, s26, s4
	s_bcnt1_i32_b64 s4, s[60:61]
	s_add_i32 s26, s26, s4
	s_bcnt1_i32_b64 s4, s[62:63]
	s_add_i32 s26, s26, s4
	s_bcnt1_i32_b64 s4, s[64:65]
	s_add_i32 s26, s26, s4
	s_cmp_le_u32 s79, 8
	s_cbranch_scc1 .Lsel_fin_bend
	v_ashrrev_i32_e32 v224, 31, v34
	v_or_b32_e32 v224, 0x80000000, v224
	v_xor_b32_e32 v224, v34, v224
	v_ashrrev_i32_e32 v225, 31, v35
	v_or_b32_e32 v225, 0x80000000, v225
	v_xor_b32_e32 v225, v35, v225
	v_ashrrev_i32_e32 v226, 31, v36
	v_or_b32_e32 v226, 0x80000000, v226
	v_xor_b32_e32 v226, v36, v226
	v_ashrrev_i32_e32 v227, 31, v37
	v_or_b32_e32 v227, 0x80000000, v227
	v_xor_b32_e32 v227, v37, v227
	v_cmp_lt_u32_e64 s[58:59], s17, v224
	v_cmp_eq_u32_e64 s[66:67], s17, v224
	v_cmp_lt_u32_e64 s[60:61], s17, v225
	v_cmp_eq_u32_e64 s[68:69], s17, v225
	v_cmp_lt_u32_e64 s[62:63], s17, v226
	v_cmp_eq_u32_e64 s[72:73], s17, v226
	v_cmp_lt_u32_e64 s[64:65], s17, v227
	v_cmp_eq_u32_e64 s[74:75], s17, v227
	s_or_b64 s[4:5], s[66:67], s[68:69]
	s_or_b64 s[6:7], s[72:73], s[74:75]
	s_or_b64 s[4:5], s[4:5], s[6:7]
	s_cmp_lg_u64 s[4:5], 0
	s_cbranch_scc0 .Lsel_fg_st8
	v_mov_b32_e32 v140, s27
	v_mbcnt_lo_u32_b32 v140, s66, v140
	v_mbcnt_hi_u32_b32 v140, s67, v140
	v_mbcnt_lo_u32_b32 v140, s68, v140
	v_mbcnt_hi_u32_b32 v140, s69, v140
	v_mbcnt_lo_u32_b32 v140, s72, v140
	v_mbcnt_hi_u32_b32 v140, s73, v140
	v_mbcnt_lo_u32_b32 v140, s74, v140
	v_mbcnt_hi_u32_b32 v140, s75, v140
	s_mov_b64 exec, s[66:67]
	v_cmp_gt_u32_e64 s[4:5], s15, v140
	v_add_u32_e32 v140, 1, v140
	s_or_b64 s[58:59], s[58:59], s[4:5]
	s_mov_b64 exec, s[68:69]
	v_cmp_gt_u32_e64 s[4:5], s15, v140
	v_add_u32_e32 v140, 1, v140
	s_or_b64 s[60:61], s[60:61], s[4:5]
	s_mov_b64 exec, s[72:73]
	v_cmp_gt_u32_e64 s[4:5], s15, v140
	v_add_u32_e32 v140, 1, v140
	s_or_b64 s[62:63], s[62:63], s[4:5]
	s_mov_b64 exec, s[74:75]
	v_cmp_gt_u32_e64 s[4:5], s15, v140
	v_add_u32_e32 v140, 1, v140
	s_or_b64 s[64:65], s[64:65], s[4:5]
	s_mov_b64 exec, -1
	s_bcnt1_i32_b64 s4, s[66:67]
	s_add_i32 s27, s27, s4
	s_bcnt1_i32_b64 s4, s[68:69]
	s_add_i32 s27, s27, s4
	s_bcnt1_i32_b64 s4, s[72:73]
	s_add_i32 s27, s27, s4
	s_bcnt1_i32_b64 s4, s[74:75]
	s_add_i32 s27, s27, s4
.Lsel_fg_st8:
	v_mov_b32_e32 v139, s26
	v_mbcnt_lo_u32_b32 v139, s58, v139
	v_mbcnt_hi_u32_b32 v139, s59, v139
	v_mbcnt_lo_u32_b32 v139, s60, v139
	v_mbcnt_hi_u32_b32 v139, s61, v139
	v_mbcnt_lo_u32_b32 v139, s62, v139
	v_mbcnt_hi_u32_b32 v139, s63, v139
	v_mbcnt_lo_u32_b32 v139, s64, v139
	v_mbcnt_hi_u32_b32 v139, s65, v139
	s_mov_b64 exec, s[58:59]
	v_lshlrev_b32_e32 v146, 2, v139
	v_add_u32_e32 v139, 1, v139
	v_add_u32_e32 v142, 0x800, v141
	v_cmpx_gt_u32_e32 vcc, 0x400, v146
	global_store_dword v146, v142, s[40:41]
	s_mov_b64 exec, s[60:61]
	v_lshlrev_b32_e32 v147, 2, v139
	v_add_u32_e32 v139, 1, v139
	v_add_u32_e32 v143, 0x801, v141
	v_cmpx_gt_u32_e32 vcc, 0x400, v147
	global_store_dword v147, v143, s[40:41]
	s_mov_b64 exec, s[62:63]
	v_lshlrev_b32_e32 v148, 2, v139
	v_add_u32_e32 v139, 1, v139
	v_add_u32_e32 v144, 0x802, v141
	v_cmpx_gt_u32_e32 vcc, 0x400, v148
	global_store_dword v148, v144, s[40:41]
	s_mov_b64 exec, s[64:65]
	v_lshlrev_b32_e32 v214, 2, v139
	v_add_u32_e32 v139, 1, v139
	v_add_u32_e32 v145, 0x803, v141
	v_cmpx_gt_u32_e32 vcc, 0x400, v214
	global_store_dword v214, v145, s[40:41]
	s_mov_b64 exec, -1
	s_bcnt1_i32_b64 s4, s[58:59]
	s_add_i32 s26, s26, s4
	s_bcnt1_i32_b64 s4, s[60:61]
	s_add_i32 s26, s26, s4
	s_bcnt1_i32_b64 s4, s[62:63]
	s_add_i32 s26, s26, s4
	s_bcnt1_i32_b64 s4, s[64:65]
	s_add_i32 s26, s26, s4
	s_cmp_le_u32 s79, 9
	s_cbranch_scc1 .Lsel_fin_bend
	v_ashrrev_i32_e32 v224, 31, v38
	v_or_b32_e32 v224, 0x80000000, v224
	v_xor_b32_e32 v224, v38, v224
	v_ashrrev_i32_e32 v225, 31, v39
	v_or_b32_e32 v225, 0x80000000, v225
	v_xor_b32_e32 v225, v39, v225
	v_ashrrev_i32_e32 v226, 31, v40
	v_or_b32_e32 v226, 0x80000000, v226
	v_xor_b32_e32 v226, v40, v226
	v_ashrrev_i32_e32 v227, 31, v41
	v_or_b32_e32 v227, 0x80000000, v227
	v_xor_b32_e32 v227, v41, v227
	v_cmp_lt_u32_e64 s[58:59], s17, v224
	v_cmp_eq_u32_e64 s[66:67], s17, v224
	v_cmp_lt_u32_e64 s[60:61], s17, v225
	v_cmp_eq_u32_e64 s[68:69], s17, v225
	v_cmp_lt_u32_e64 s[62:63], s17, v226
	v_cmp_eq_u32_e64 s[72:73], s17, v226
	v_cmp_lt_u32_e64 s[64:65], s17, v227
	v_cmp_eq_u32_e64 s[74:75], s17, v227
	s_or_b64 s[4:5], s[66:67], s[68:69]
	s_or_b64 s[6:7], s[72:73], s[74:75]
	s_or_b64 s[4:5], s[4:5], s[6:7]
	s_cmp_lg_u64 s[4:5], 0
	s_cbranch_scc0 .Lsel_fg_st9
	v_mov_b32_e32 v140, s27
	v_mbcnt_lo_u32_b32 v140, s66, v140
	v_mbcnt_hi_u32_b32 v140, s67, v140
	v_mbcnt_lo_u32_b32 v140, s68, v140
	v_mbcnt_hi_u32_b32 v140, s69, v140
	v_mbcnt_lo_u32_b32 v140, s72, v140
	v_mbcnt_hi_u32_b32 v140, s73, v140
	v_mbcnt_lo_u32_b32 v140, s74, v140
	v_mbcnt_hi_u32_b32 v140, s75, v140
	s_mov_b64 exec, s[66:67]
	v_cmp_gt_u32_e64 s[4:5], s15, v140
	v_add_u32_e32 v140, 1, v140
	s_or_b64 s[58:59], s[58:59], s[4:5]
	s_mov_b64 exec, s[68:69]
	v_cmp_gt_u32_e64 s[4:5], s15, v140
	v_add_u32_e32 v140, 1, v140
	s_or_b64 s[60:61], s[60:61], s[4:5]
	s_mov_b64 exec, s[72:73]
	v_cmp_gt_u32_e64 s[4:5], s15, v140
	v_add_u32_e32 v140, 1, v140
	s_or_b64 s[62:63], s[62:63], s[4:5]
	s_mov_b64 exec, s[74:75]
	v_cmp_gt_u32_e64 s[4:5], s15, v140
	v_add_u32_e32 v140, 1, v140
	s_or_b64 s[64:65], s[64:65], s[4:5]
	s_mov_b64 exec, -1
	s_bcnt1_i32_b64 s4, s[66:67]
	s_add_i32 s27, s27, s4
	s_bcnt1_i32_b64 s4, s[68:69]
	s_add_i32 s27, s27, s4
	s_bcnt1_i32_b64 s4, s[72:73]
	s_add_i32 s27, s27, s4
	s_bcnt1_i32_b64 s4, s[74:75]
	s_add_i32 s27, s27, s4
.Lsel_fg_st9:
	v_mov_b32_e32 v139, s26
	v_mbcnt_lo_u32_b32 v139, s58, v139
	v_mbcnt_hi_u32_b32 v139, s59, v139
	v_mbcnt_lo_u32_b32 v139, s60, v139
	v_mbcnt_hi_u32_b32 v139, s61, v139
	v_mbcnt_lo_u32_b32 v139, s62, v139
	v_mbcnt_hi_u32_b32 v139, s63, v139
	v_mbcnt_lo_u32_b32 v139, s64, v139
	v_mbcnt_hi_u32_b32 v139, s65, v139
	s_mov_b64 exec, s[58:59]
	v_lshlrev_b32_e32 v146, 2, v139
	v_add_u32_e32 v139, 1, v139
	v_add_u32_e32 v142, 0x900, v141
	v_cmpx_gt_u32_e32 vcc, 0x400, v146
	global_store_dword v146, v142, s[40:41]
	s_mov_b64 exec, s[60:61]
	v_lshlrev_b32_e32 v147, 2, v139
	v_add_u32_e32 v139, 1, v139
	v_add_u32_e32 v143, 0x901, v141
	v_cmpx_gt_u32_e32 vcc, 0x400, v147
	global_store_dword v147, v143, s[40:41]
	s_mov_b64 exec, s[62:63]
	v_lshlrev_b32_e32 v148, 2, v139
	v_add_u32_e32 v139, 1, v139
	v_add_u32_e32 v144, 0x902, v141
	v_cmpx_gt_u32_e32 vcc, 0x400, v148
	global_store_dword v148, v144, s[40:41]
	s_mov_b64 exec, s[64:65]
	v_lshlrev_b32_e32 v214, 2, v139
	v_add_u32_e32 v139, 1, v139
	v_add_u32_e32 v145, 0x903, v141
	v_cmpx_gt_u32_e32 vcc, 0x400, v214
	global_store_dword v214, v145, s[40:41]
	s_mov_b64 exec, -1
	s_bcnt1_i32_b64 s4, s[58:59]
	s_add_i32 s26, s26, s4
	s_bcnt1_i32_b64 s4, s[60:61]
	s_add_i32 s26, s26, s4
	s_bcnt1_i32_b64 s4, s[62:63]
	s_add_i32 s26, s26, s4
	s_bcnt1_i32_b64 s4, s[64:65]
	s_add_i32 s26, s26, s4
	s_cmp_le_u32 s79, 10
	s_cbranch_scc1 .Lsel_fin_bend
	v_ashrrev_i32_e32 v224, 31, v42
	v_or_b32_e32 v224, 0x80000000, v224
	v_xor_b32_e32 v224, v42, v224
	v_ashrrev_i32_e32 v225, 31, v43
	v_or_b32_e32 v225, 0x80000000, v225
	v_xor_b32_e32 v225, v43, v225
	v_ashrrev_i32_e32 v226, 31, v44
	v_or_b32_e32 v226, 0x80000000, v226
	v_xor_b32_e32 v226, v44, v226
	v_ashrrev_i32_e32 v227, 31, v45
	v_or_b32_e32 v227, 0x80000000, v227
	v_xor_b32_e32 v227, v45, v227
	v_cmp_lt_u32_e64 s[58:59], s17, v224
	v_cmp_eq_u32_e64 s[66:67], s17, v224
	v_cmp_lt_u32_e64 s[60:61], s17, v225
	v_cmp_eq_u32_e64 s[68:69], s17, v225
	v_cmp_lt_u32_e64 s[62:63], s17, v226
	v_cmp_eq_u32_e64 s[72:73], s17, v226
	v_cmp_lt_u32_e64 s[64:65], s17, v227
	v_cmp_eq_u32_e64 s[74:75], s17, v227
	s_or_b64 s[4:5], s[66:67], s[68:69]
	s_or_b64 s[6:7], s[72:73], s[74:75]
	s_or_b64 s[4:5], s[4:5], s[6:7]
	s_cmp_lg_u64 s[4:5], 0
	s_cbranch_scc0 .Lsel_fg_st10
	v_mov_b32_e32 v140, s27
	v_mbcnt_lo_u32_b32 v140, s66, v140
	v_mbcnt_hi_u32_b32 v140, s67, v140
	v_mbcnt_lo_u32_b32 v140, s68, v140
	v_mbcnt_hi_u32_b32 v140, s69, v140
	v_mbcnt_lo_u32_b32 v140, s72, v140
	v_mbcnt_hi_u32_b32 v140, s73, v140
	v_mbcnt_lo_u32_b32 v140, s74, v140
	v_mbcnt_hi_u32_b32 v140, s75, v140
	s_mov_b64 exec, s[66:67]
	v_cmp_gt_u32_e64 s[4:5], s15, v140
	v_add_u32_e32 v140, 1, v140
	s_or_b64 s[58:59], s[58:59], s[4:5]
	s_mov_b64 exec, s[68:69]
	v_cmp_gt_u32_e64 s[4:5], s15, v140
	v_add_u32_e32 v140, 1, v140
	s_or_b64 s[60:61], s[60:61], s[4:5]
	s_mov_b64 exec, s[72:73]
	v_cmp_gt_u32_e64 s[4:5], s15, v140
	v_add_u32_e32 v140, 1, v140
	s_or_b64 s[62:63], s[62:63], s[4:5]
	s_mov_b64 exec, s[74:75]
	v_cmp_gt_u32_e64 s[4:5], s15, v140
	v_add_u32_e32 v140, 1, v140
	s_or_b64 s[64:65], s[64:65], s[4:5]
	s_mov_b64 exec, -1
	s_bcnt1_i32_b64 s4, s[66:67]
	s_add_i32 s27, s27, s4
	s_bcnt1_i32_b64 s4, s[68:69]
	s_add_i32 s27, s27, s4
	s_bcnt1_i32_b64 s4, s[72:73]
	s_add_i32 s27, s27, s4
	s_bcnt1_i32_b64 s4, s[74:75]
	s_add_i32 s27, s27, s4
.Lsel_fg_st10:
	v_mov_b32_e32 v139, s26
	v_mbcnt_lo_u32_b32 v139, s58, v139
	v_mbcnt_hi_u32_b32 v139, s59, v139
	v_mbcnt_lo_u32_b32 v139, s60, v139
	v_mbcnt_hi_u32_b32 v139, s61, v139
	v_mbcnt_lo_u32_b32 v139, s62, v139
	v_mbcnt_hi_u32_b32 v139, s63, v139
	v_mbcnt_lo_u32_b32 v139, s64, v139
	v_mbcnt_hi_u32_b32 v139, s65, v139
	s_mov_b64 exec, s[58:59]
	v_lshlrev_b32_e32 v146, 2, v139
	v_add_u32_e32 v139, 1, v139
	v_add_u32_e32 v142, 0xa00, v141
	v_cmpx_gt_u32_e32 vcc, 0x400, v146
	global_store_dword v146, v142, s[40:41]
	s_mov_b64 exec, s[60:61]
	v_lshlrev_b32_e32 v147, 2, v139
	v_add_u32_e32 v139, 1, v139
	v_add_u32_e32 v143, 0xa01, v141
	v_cmpx_gt_u32_e32 vcc, 0x400, v147
	global_store_dword v147, v143, s[40:41]
	s_mov_b64 exec, s[62:63]
	v_lshlrev_b32_e32 v148, 2, v139
	v_add_u32_e32 v139, 1, v139
	v_add_u32_e32 v144, 0xa02, v141
	v_cmpx_gt_u32_e32 vcc, 0x400, v148
	global_store_dword v148, v144, s[40:41]
	s_mov_b64 exec, s[64:65]
	v_lshlrev_b32_e32 v214, 2, v139
	v_add_u32_e32 v139, 1, v139
	v_add_u32_e32 v145, 0xa03, v141
	v_cmpx_gt_u32_e32 vcc, 0x400, v214
	global_store_dword v214, v145, s[40:41]
	s_mov_b64 exec, -1
	s_bcnt1_i32_b64 s4, s[58:59]
	s_add_i32 s26, s26, s4
	s_bcnt1_i32_b64 s4, s[60:61]
	s_add_i32 s26, s26, s4
	s_bcnt1_i32_b64 s4, s[62:63]
	s_add_i32 s26, s26, s4
	s_bcnt1_i32_b64 s4, s[64:65]
	s_add_i32 s26, s26, s4
	s_cmp_le_u32 s79, 11
	s_cbranch_scc1 .Lsel_fin_bend
	v_ashrrev_i32_e32 v224, 31, v46
	v_or_b32_e32 v224, 0x80000000, v224
	v_xor_b32_e32 v224, v46, v224
	v_ashrrev_i32_e32 v225, 31, v47
	v_or_b32_e32 v225, 0x80000000, v225
	v_xor_b32_e32 v225, v47, v225
	v_ashrrev_i32_e32 v226, 31, v48
	v_or_b32_e32 v226, 0x80000000, v226
	v_xor_b32_e32 v226, v48, v226
	v_ashrrev_i32_e32 v227, 31, v49
	v_or_b32_e32 v227, 0x80000000, v227
	v_xor_b32_e32 v227, v49, v227
	v_cmp_lt_u32_e64 s[58:59], s17, v224
	v_cmp_eq_u32_e64 s[66:67], s17, v224
	v_cmp_lt_u32_e64 s[60:61], s17, v225
	v_cmp_eq_u32_e64 s[68:69], s17, v225
	v_cmp_lt_u32_e64 s[62:63], s17, v226
	v_cmp_eq_u32_e64 s[72:73], s17, v226
	v_cmp_lt_u32_e64 s[64:65], s17, v227
	v_cmp_eq_u32_e64 s[74:75], s17, v227
	s_or_b64 s[4:5], s[66:67], s[68:69]
	s_or_b64 s[6:7], s[72:73], s[74:75]
	s_or_b64 s[4:5], s[4:5], s[6:7]
	s_cmp_lg_u64 s[4:5], 0
	s_cbranch_scc0 .Lsel_fg_st11
	v_mov_b32_e32 v140, s27
	v_mbcnt_lo_u32_b32 v140, s66, v140
	v_mbcnt_hi_u32_b32 v140, s67, v140
	v_mbcnt_lo_u32_b32 v140, s68, v140
	v_mbcnt_hi_u32_b32 v140, s69, v140
	v_mbcnt_lo_u32_b32 v140, s72, v140
	v_mbcnt_hi_u32_b32 v140, s73, v140
	v_mbcnt_lo_u32_b32 v140, s74, v140
	v_mbcnt_hi_u32_b32 v140, s75, v140
	s_mov_b64 exec, s[66:67]
	v_cmp_gt_u32_e64 s[4:5], s15, v140
	v_add_u32_e32 v140, 1, v140
	s_or_b64 s[58:59], s[58:59], s[4:5]
	s_mov_b64 exec, s[68:69]
	v_cmp_gt_u32_e64 s[4:5], s15, v140
	v_add_u32_e32 v140, 1, v140
	s_or_b64 s[60:61], s[60:61], s[4:5]
	s_mov_b64 exec, s[72:73]
	v_cmp_gt_u32_e64 s[4:5], s15, v140
	v_add_u32_e32 v140, 1, v140
	s_or_b64 s[62:63], s[62:63], s[4:5]
	s_mov_b64 exec, s[74:75]
	v_cmp_gt_u32_e64 s[4:5], s15, v140
	v_add_u32_e32 v140, 1, v140
	s_or_b64 s[64:65], s[64:65], s[4:5]
	s_mov_b64 exec, -1
	s_bcnt1_i32_b64 s4, s[66:67]
	s_add_i32 s27, s27, s4
	s_bcnt1_i32_b64 s4, s[68:69]
	s_add_i32 s27, s27, s4
	s_bcnt1_i32_b64 s4, s[72:73]
	s_add_i32 s27, s27, s4
	s_bcnt1_i32_b64 s4, s[74:75]
	s_add_i32 s27, s27, s4
.Lsel_fg_st11:
	v_mov_b32_e32 v139, s26
	v_mbcnt_lo_u32_b32 v139, s58, v139
	v_mbcnt_hi_u32_b32 v139, s59, v139
	v_mbcnt_lo_u32_b32 v139, s60, v139
	v_mbcnt_hi_u32_b32 v139, s61, v139
	v_mbcnt_lo_u32_b32 v139, s62, v139
	v_mbcnt_hi_u32_b32 v139, s63, v139
	v_mbcnt_lo_u32_b32 v139, s64, v139
	v_mbcnt_hi_u32_b32 v139, s65, v139
	s_mov_b64 exec, s[58:59]
	v_lshlrev_b32_e32 v146, 2, v139
	v_add_u32_e32 v139, 1, v139
	v_add_u32_e32 v142, 0xb00, v141
	v_cmpx_gt_u32_e32 vcc, 0x400, v146
	global_store_dword v146, v142, s[40:41]
	s_mov_b64 exec, s[60:61]
	v_lshlrev_b32_e32 v147, 2, v139
	v_add_u32_e32 v139, 1, v139
	v_add_u32_e32 v143, 0xb01, v141
	v_cmpx_gt_u32_e32 vcc, 0x400, v147
	global_store_dword v147, v143, s[40:41]
	s_mov_b64 exec, s[62:63]
	v_lshlrev_b32_e32 v148, 2, v139
	v_add_u32_e32 v139, 1, v139
	v_add_u32_e32 v144, 0xb02, v141
	v_cmpx_gt_u32_e32 vcc, 0x400, v148
	global_store_dword v148, v144, s[40:41]
	s_mov_b64 exec, s[64:65]
	v_lshlrev_b32_e32 v214, 2, v139
	v_add_u32_e32 v139, 1, v139
	v_add_u32_e32 v145, 0xb03, v141
	v_cmpx_gt_u32_e32 vcc, 0x400, v214
	global_store_dword v214, v145, s[40:41]
	s_mov_b64 exec, -1
	s_bcnt1_i32_b64 s4, s[58:59]
	s_add_i32 s26, s26, s4
	s_bcnt1_i32_b64 s4, s[60:61]
	s_add_i32 s26, s26, s4
	s_bcnt1_i32_b64 s4, s[62:63]
	s_add_i32 s26, s26, s4
	s_bcnt1_i32_b64 s4, s[64:65]
	s_add_i32 s26, s26, s4
	s_cmp_le_u32 s79, 12
	s_cbranch_scc1 .Lsel_fin_bend
	v_ashrrev_i32_e32 v224, 31, v118
	v_or_b32_e32 v224, 0x80000000, v224
	v_xor_b32_e32 v224, v118, v224
	v_ashrrev_i32_e32 v225, 31, v119
	v_or_b32_e32 v225, 0x80000000, v225
	v_xor_b32_e32 v225, v119, v225
	v_ashrrev_i32_e32 v226, 31, v120
	v_or_b32_e32 v226, 0x80000000, v226
	v_xor_b32_e32 v226, v120, v226
	v_ashrrev_i32_e32 v227, 31, v121
	v_or_b32_e32 v227, 0x80000000, v227
	v_xor_b32_e32 v227, v121, v227
	v_cmp_lt_u32_e64 s[58:59], s17, v224
	v_cmp_eq_u32_e64 s[66:67], s17, v224
	v_cmp_lt_u32_e64 s[60:61], s17, v225
	v_cmp_eq_u32_e64 s[68:69], s17, v225
	v_cmp_lt_u32_e64 s[62:63], s17, v226
	v_cmp_eq_u32_e64 s[72:73], s17, v226
	v_cmp_lt_u32_e64 s[64:65], s17, v227
	v_cmp_eq_u32_e64 s[74:75], s17, v227
	s_or_b64 s[4:5], s[66:67], s[68:69]
	s_or_b64 s[6:7], s[72:73], s[74:75]
	s_or_b64 s[4:5], s[4:5], s[6:7]
	s_cmp_lg_u64 s[4:5], 0
	s_cbranch_scc0 .Lsel_fg_st12
	v_mov_b32_e32 v140, s27
	v_mbcnt_lo_u32_b32 v140, s66, v140
	v_mbcnt_hi_u32_b32 v140, s67, v140
	v_mbcnt_lo_u32_b32 v140, s68, v140
	v_mbcnt_hi_u32_b32 v140, s69, v140
	v_mbcnt_lo_u32_b32 v140, s72, v140
	v_mbcnt_hi_u32_b32 v140, s73, v140
	v_mbcnt_lo_u32_b32 v140, s74, v140
	v_mbcnt_hi_u32_b32 v140, s75, v140
	s_mov_b64 exec, s[66:67]
	v_cmp_gt_u32_e64 s[4:5], s15, v140
	v_add_u32_e32 v140, 1, v140
	s_or_b64 s[58:59], s[58:59], s[4:5]
	s_mov_b64 exec, s[68:69]
	v_cmp_gt_u32_e64 s[4:5], s15, v140
	v_add_u32_e32 v140, 1, v140
	s_or_b64 s[60:61], s[60:61], s[4:5]
	s_mov_b64 exec, s[72:73]
	v_cmp_gt_u32_e64 s[4:5], s15, v140
	v_add_u32_e32 v140, 1, v140
	s_or_b64 s[62:63], s[62:63], s[4:5]
	s_mov_b64 exec, s[74:75]
	v_cmp_gt_u32_e64 s[4:5], s15, v140
	v_add_u32_e32 v140, 1, v140
	s_or_b64 s[64:65], s[64:65], s[4:5]
	s_mov_b64 exec, -1
	s_bcnt1_i32_b64 s4, s[66:67]
	s_add_i32 s27, s27, s4
	s_bcnt1_i32_b64 s4, s[68:69]
	s_add_i32 s27, s27, s4
	s_bcnt1_i32_b64 s4, s[72:73]
	s_add_i32 s27, s27, s4
	s_bcnt1_i32_b64 s4, s[74:75]
	s_add_i32 s27, s27, s4
.Lsel_fg_st12:
	v_mov_b32_e32 v139, s26
	v_mbcnt_lo_u32_b32 v139, s58, v139
	v_mbcnt_hi_u32_b32 v139, s59, v139
	v_mbcnt_lo_u32_b32 v139, s60, v139
	v_mbcnt_hi_u32_b32 v139, s61, v139
	v_mbcnt_lo_u32_b32 v139, s62, v139
	v_mbcnt_hi_u32_b32 v139, s63, v139
	v_mbcnt_lo_u32_b32 v139, s64, v139
	v_mbcnt_hi_u32_b32 v139, s65, v139
	s_mov_b64 exec, s[58:59]
	v_lshlrev_b32_e32 v146, 2, v139
	v_add_u32_e32 v139, 1, v139
	v_add_u32_e32 v142, 0xc00, v141
	v_cmpx_gt_u32_e32 vcc, 0x400, v146
	global_store_dword v146, v142, s[40:41]
	s_mov_b64 exec, s[60:61]
	v_lshlrev_b32_e32 v147, 2, v139
	v_add_u32_e32 v139, 1, v139
	v_add_u32_e32 v143, 0xc01, v141
	v_cmpx_gt_u32_e32 vcc, 0x400, v147
	global_store_dword v147, v143, s[40:41]
	s_mov_b64 exec, s[62:63]
	v_lshlrev_b32_e32 v148, 2, v139
	v_add_u32_e32 v139, 1, v139
	v_add_u32_e32 v144, 0xc02, v141
	v_cmpx_gt_u32_e32 vcc, 0x400, v148
	global_store_dword v148, v144, s[40:41]
	s_mov_b64 exec, s[64:65]
	v_lshlrev_b32_e32 v214, 2, v139
	v_add_u32_e32 v139, 1, v139
	v_add_u32_e32 v145, 0xc03, v141
	v_cmpx_gt_u32_e32 vcc, 0x400, v214
	global_store_dword v214, v145, s[40:41]
	s_mov_b64 exec, -1
	s_bcnt1_i32_b64 s4, s[58:59]
	s_add_i32 s26, s26, s4
	s_bcnt1_i32_b64 s4, s[60:61]
	s_add_i32 s26, s26, s4
	s_bcnt1_i32_b64 s4, s[62:63]
	s_add_i32 s26, s26, s4
	s_bcnt1_i32_b64 s4, s[64:65]
	s_add_i32 s26, s26, s4
	s_cmp_le_u32 s79, 13
	s_cbranch_scc1 .Lsel_fin_bend
	v_ashrrev_i32_e32 v224, 31, v122
	v_or_b32_e32 v224, 0x80000000, v224
	v_xor_b32_e32 v224, v122, v224
	v_ashrrev_i32_e32 v225, 31, v123
	v_or_b32_e32 v225, 0x80000000, v225
	v_xor_b32_e32 v225, v123, v225
	v_ashrrev_i32_e32 v226, 31, v124
	v_or_b32_e32 v226, 0x80000000, v226
	v_xor_b32_e32 v226, v124, v226
	v_ashrrev_i32_e32 v227, 31, v125
	v_or_b32_e32 v227, 0x80000000, v227
	v_xor_b32_e32 v227, v125, v227
	v_cmp_lt_u32_e64 s[58:59], s17, v224
	v_cmp_eq_u32_e64 s[66:67], s17, v224
	v_cmp_lt_u32_e64 s[60:61], s17, v225
	v_cmp_eq_u32_e64 s[68:69], s17, v225
	v_cmp_lt_u32_e64 s[62:63], s17, v226
	v_cmp_eq_u32_e64 s[72:73], s17, v226
	v_cmp_lt_u32_e64 s[64:65], s17, v227
	v_cmp_eq_u32_e64 s[74:75], s17, v227
	s_or_b64 s[4:5], s[66:67], s[68:69]
	s_or_b64 s[6:7], s[72:73], s[74:75]
	s_or_b64 s[4:5], s[4:5], s[6:7]
	s_cmp_lg_u64 s[4:5], 0
	s_cbranch_scc0 .Lsel_fg_st13
	v_mov_b32_e32 v140, s27
	v_mbcnt_lo_u32_b32 v140, s66, v140
	v_mbcnt_hi_u32_b32 v140, s67, v140
	v_mbcnt_lo_u32_b32 v140, s68, v140
	v_mbcnt_hi_u32_b32 v140, s69, v140
	v_mbcnt_lo_u32_b32 v140, s72, v140
	v_mbcnt_hi_u32_b32 v140, s73, v140
	v_mbcnt_lo_u32_b32 v140, s74, v140
	v_mbcnt_hi_u32_b32 v140, s75, v140
	s_mov_b64 exec, s[66:67]
	v_cmp_gt_u32_e64 s[4:5], s15, v140
	v_add_u32_e32 v140, 1, v140
	s_or_b64 s[58:59], s[58:59], s[4:5]
	s_mov_b64 exec, s[68:69]
	v_cmp_gt_u32_e64 s[4:5], s15, v140
	v_add_u32_e32 v140, 1, v140
	s_or_b64 s[60:61], s[60:61], s[4:5]
	s_mov_b64 exec, s[72:73]
	v_cmp_gt_u32_e64 s[4:5], s15, v140
	v_add_u32_e32 v140, 1, v140
	s_or_b64 s[62:63], s[62:63], s[4:5]
	s_mov_b64 exec, s[74:75]
	v_cmp_gt_u32_e64 s[4:5], s15, v140
	v_add_u32_e32 v140, 1, v140
	s_or_b64 s[64:65], s[64:65], s[4:5]
	s_mov_b64 exec, -1
	s_bcnt1_i32_b64 s4, s[66:67]
	s_add_i32 s27, s27, s4
	s_bcnt1_i32_b64 s4, s[68:69]
	s_add_i32 s27, s27, s4
	s_bcnt1_i32_b64 s4, s[72:73]
	s_add_i32 s27, s27, s4
	s_bcnt1_i32_b64 s4, s[74:75]
	s_add_i32 s27, s27, s4
.Lsel_fg_st13:
	v_mov_b32_e32 v139, s26
	v_mbcnt_lo_u32_b32 v139, s58, v139
	v_mbcnt_hi_u32_b32 v139, s59, v139
	v_mbcnt_lo_u32_b32 v139, s60, v139
	v_mbcnt_hi_u32_b32 v139, s61, v139
	v_mbcnt_lo_u32_b32 v139, s62, v139
	v_mbcnt_hi_u32_b32 v139, s63, v139
	v_mbcnt_lo_u32_b32 v139, s64, v139
	v_mbcnt_hi_u32_b32 v139, s65, v139
	s_mov_b64 exec, s[58:59]
	v_lshlrev_b32_e32 v146, 2, v139
	v_add_u32_e32 v139, 1, v139
	v_add_u32_e32 v142, 0xd00, v141
	v_cmpx_gt_u32_e32 vcc, 0x400, v146
	global_store_dword v146, v142, s[40:41]
	s_mov_b64 exec, s[60:61]
	v_lshlrev_b32_e32 v147, 2, v139
	v_add_u32_e32 v139, 1, v139
	v_add_u32_e32 v143, 0xd01, v141
	v_cmpx_gt_u32_e32 vcc, 0x400, v147
	global_store_dword v147, v143, s[40:41]
	s_mov_b64 exec, s[62:63]
	v_lshlrev_b32_e32 v148, 2, v139
	v_add_u32_e32 v139, 1, v139
	v_add_u32_e32 v144, 0xd02, v141
	v_cmpx_gt_u32_e32 vcc, 0x400, v148
	global_store_dword v148, v144, s[40:41]
	s_mov_b64 exec, s[64:65]
	v_lshlrev_b32_e32 v214, 2, v139
	v_add_u32_e32 v139, 1, v139
	v_add_u32_e32 v145, 0xd03, v141
	v_cmpx_gt_u32_e32 vcc, 0x400, v214
	global_store_dword v214, v145, s[40:41]
	s_mov_b64 exec, -1
	s_bcnt1_i32_b64 s4, s[58:59]
	s_add_i32 s26, s26, s4
	s_bcnt1_i32_b64 s4, s[60:61]
	s_add_i32 s26, s26, s4
	s_bcnt1_i32_b64 s4, s[62:63]
	s_add_i32 s26, s26, s4
	s_bcnt1_i32_b64 s4, s[64:65]
	s_add_i32 s26, s26, s4
	s_cmp_le_u32 s79, 14
	s_cbranch_scc1 .Lsel_fin_bend
	v_ashrrev_i32_e32 v224, 31, v126
	v_or_b32_e32 v224, 0x80000000, v224
	v_xor_b32_e32 v224, v126, v224
	v_ashrrev_i32_e32 v225, 31, v127
	v_or_b32_e32 v225, 0x80000000, v225
	v_xor_b32_e32 v225, v127, v225
	v_ashrrev_i32_e32 v226, 31, v128
	v_or_b32_e32 v226, 0x80000000, v226
	v_xor_b32_e32 v226, v128, v226
	v_ashrrev_i32_e32 v227, 31, v129
	v_or_b32_e32 v227, 0x80000000, v227
	v_xor_b32_e32 v227, v129, v227
	v_cmp_lt_u32_e64 s[58:59], s17, v224
	v_cmp_eq_u32_e64 s[66:67], s17, v224
	v_cmp_lt_u32_e64 s[60:61], s17, v225
	v_cmp_eq_u32_e64 s[68:69], s17, v225
	v_cmp_lt_u32_e64 s[62:63], s17, v226
	v_cmp_eq_u32_e64 s[72:73], s17, v226
	v_cmp_lt_u32_e64 s[64:65], s17, v227
	v_cmp_eq_u32_e64 s[74:75], s17, v227
	s_or_b64 s[4:5], s[66:67], s[68:69]
	s_or_b64 s[6:7], s[72:73], s[74:75]
	s_or_b64 s[4:5], s[4:5], s[6:7]
	s_cmp_lg_u64 s[4:5], 0
	s_cbranch_scc0 .Lsel_fg_st14
	v_mov_b32_e32 v140, s27
	v_mbcnt_lo_u32_b32 v140, s66, v140
	v_mbcnt_hi_u32_b32 v140, s67, v140
	v_mbcnt_lo_u32_b32 v140, s68, v140
	v_mbcnt_hi_u32_b32 v140, s69, v140
	v_mbcnt_lo_u32_b32 v140, s72, v140
	v_mbcnt_hi_u32_b32 v140, s73, v140
	v_mbcnt_lo_u32_b32 v140, s74, v140
	v_mbcnt_hi_u32_b32 v140, s75, v140
	s_mov_b64 exec, s[66:67]
	v_cmp_gt_u32_e64 s[4:5], s15, v140
	v_add_u32_e32 v140, 1, v140
	s_or_b64 s[58:59], s[58:59], s[4:5]
	s_mov_b64 exec, s[68:69]
	v_cmp_gt_u32_e64 s[4:5], s15, v140
	v_add_u32_e32 v140, 1, v140
	s_or_b64 s[60:61], s[60:61], s[4:5]
	s_mov_b64 exec, s[72:73]
	v_cmp_gt_u32_e64 s[4:5], s15, v140
	v_add_u32_e32 v140, 1, v140
	s_or_b64 s[62:63], s[62:63], s[4:5]
	s_mov_b64 exec, s[74:75]
	v_cmp_gt_u32_e64 s[4:5], s15, v140
	v_add_u32_e32 v140, 1, v140
	s_or_b64 s[64:65], s[64:65], s[4:5]
	s_mov_b64 exec, -1
	s_bcnt1_i32_b64 s4, s[66:67]
	s_add_i32 s27, s27, s4
	s_bcnt1_i32_b64 s4, s[68:69]
	s_add_i32 s27, s27, s4
	s_bcnt1_i32_b64 s4, s[72:73]
	s_add_i32 s27, s27, s4
	s_bcnt1_i32_b64 s4, s[74:75]
	s_add_i32 s27, s27, s4
.Lsel_fg_st14:
	v_mov_b32_e32 v139, s26
	v_mbcnt_lo_u32_b32 v139, s58, v139
	v_mbcnt_hi_u32_b32 v139, s59, v139
	v_mbcnt_lo_u32_b32 v139, s60, v139
	v_mbcnt_hi_u32_b32 v139, s61, v139
	v_mbcnt_lo_u32_b32 v139, s62, v139
	v_mbcnt_hi_u32_b32 v139, s63, v139
	v_mbcnt_lo_u32_b32 v139, s64, v139
	v_mbcnt_hi_u32_b32 v139, s65, v139
	s_mov_b64 exec, s[58:59]
	v_lshlrev_b32_e32 v146, 2, v139
	v_add_u32_e32 v139, 1, v139
	v_add_u32_e32 v142, 0xe00, v141
	v_cmpx_gt_u32_e32 vcc, 0x400, v146
	global_store_dword v146, v142, s[40:41]
	s_mov_b64 exec, s[60:61]
	v_lshlrev_b32_e32 v147, 2, v139
	v_add_u32_e32 v139, 1, v139
	v_add_u32_e32 v143, 0xe01, v141
	v_cmpx_gt_u32_e32 vcc, 0x400, v147
	global_store_dword v147, v143, s[40:41]
	s_mov_b64 exec, s[62:63]
	v_lshlrev_b32_e32 v148, 2, v139
	v_add_u32_e32 v139, 1, v139
	v_add_u32_e32 v144, 0xe02, v141
	v_cmpx_gt_u32_e32 vcc, 0x400, v148
	global_store_dword v148, v144, s[40:41]
	s_mov_b64 exec, s[64:65]
	v_lshlrev_b32_e32 v214, 2, v139
	v_add_u32_e32 v139, 1, v139
	v_add_u32_e32 v145, 0xe03, v141
	v_cmpx_gt_u32_e32 vcc, 0x400, v214
	global_store_dword v214, v145, s[40:41]
	s_mov_b64 exec, -1
	s_bcnt1_i32_b64 s4, s[58:59]
	s_add_i32 s26, s26, s4
	s_bcnt1_i32_b64 s4, s[60:61]
	s_add_i32 s26, s26, s4
	s_bcnt1_i32_b64 s4, s[62:63]
	s_add_i32 s26, s26, s4
	s_bcnt1_i32_b64 s4, s[64:65]
	s_add_i32 s26, s26, s4
	s_cmp_le_u32 s79, 15
	s_cbranch_scc1 .Lsel_fin_bend
	v_ashrrev_i32_e32 v224, 31, v130
	v_or_b32_e32 v224, 0x80000000, v224
	v_xor_b32_e32 v224, v130, v224
	v_ashrrev_i32_e32 v225, 31, v131
	v_or_b32_e32 v225, 0x80000000, v225
	v_xor_b32_e32 v225, v131, v225
	v_ashrrev_i32_e32 v226, 31, v132
	v_or_b32_e32 v226, 0x80000000, v226
	v_xor_b32_e32 v226, v132, v226
	v_ashrrev_i32_e32 v227, 31, v133
	v_or_b32_e32 v227, 0x80000000, v227
	v_xor_b32_e32 v227, v133, v227
	v_cmp_lt_u32_e64 s[58:59], s17, v224
	v_cmp_eq_u32_e64 s[66:67], s17, v224
	v_cmp_lt_u32_e64 s[60:61], s17, v225
	v_cmp_eq_u32_e64 s[68:69], s17, v225
	v_cmp_lt_u32_e64 s[62:63], s17, v226
	v_cmp_eq_u32_e64 s[72:73], s17, v226
	v_cmp_lt_u32_e64 s[64:65], s17, v227
	v_cmp_eq_u32_e64 s[74:75], s17, v227
	s_or_b64 s[4:5], s[66:67], s[68:69]
	s_or_b64 s[6:7], s[72:73], s[74:75]
	s_or_b64 s[4:5], s[4:5], s[6:7]
	s_cmp_lg_u64 s[4:5], 0
	s_cbranch_scc0 .Lsel_fg_st15
	v_mov_b32_e32 v140, s27
	v_mbcnt_lo_u32_b32 v140, s66, v140
	v_mbcnt_hi_u32_b32 v140, s67, v140
	v_mbcnt_lo_u32_b32 v140, s68, v140
	v_mbcnt_hi_u32_b32 v140, s69, v140
	v_mbcnt_lo_u32_b32 v140, s72, v140
	v_mbcnt_hi_u32_b32 v140, s73, v140
	v_mbcnt_lo_u32_b32 v140, s74, v140
	v_mbcnt_hi_u32_b32 v140, s75, v140
	s_mov_b64 exec, s[66:67]
	v_cmp_gt_u32_e64 s[4:5], s15, v140
	v_add_u32_e32 v140, 1, v140
	s_or_b64 s[58:59], s[58:59], s[4:5]
	s_mov_b64 exec, s[68:69]
	v_cmp_gt_u32_e64 s[4:5], s15, v140
	v_add_u32_e32 v140, 1, v140
	s_or_b64 s[60:61], s[60:61], s[4:5]
	s_mov_b64 exec, s[72:73]
	v_cmp_gt_u32_e64 s[4:5], s15, v140
	v_add_u32_e32 v140, 1, v140
	s_or_b64 s[62:63], s[62:63], s[4:5]
	s_mov_b64 exec, s[74:75]
	v_cmp_gt_u32_e64 s[4:5], s15, v140
	v_add_u32_e32 v140, 1, v140
	s_or_b64 s[64:65], s[64:65], s[4:5]
	s_mov_b64 exec, -1
	s_bcnt1_i32_b64 s4, s[66:67]
	s_add_i32 s27, s27, s4
	s_bcnt1_i32_b64 s4, s[68:69]
	s_add_i32 s27, s27, s4
	s_bcnt1_i32_b64 s4, s[72:73]
	s_add_i32 s27, s27, s4
	s_bcnt1_i32_b64 s4, s[74:75]
	s_add_i32 s27, s27, s4
.Lsel_fg_st15:
	v_mov_b32_e32 v139, s26
	v_mbcnt_lo_u32_b32 v139, s58, v139
	v_mbcnt_hi_u32_b32 v139, s59, v139
	v_mbcnt_lo_u32_b32 v139, s60, v139
	v_mbcnt_hi_u32_b32 v139, s61, v139
	v_mbcnt_lo_u32_b32 v139, s62, v139
	v_mbcnt_hi_u32_b32 v139, s63, v139
	v_mbcnt_lo_u32_b32 v139, s64, v139
	v_mbcnt_hi_u32_b32 v139, s65, v139
	s_mov_b64 exec, s[58:59]
	v_lshlrev_b32_e32 v146, 2, v139
	v_add_u32_e32 v139, 1, v139
	v_add_u32_e32 v142, 0xf00, v141
	v_cmpx_gt_u32_e32 vcc, 0x400, v146
	global_store_dword v146, v142, s[40:41]
	s_mov_b64 exec, s[60:61]
	v_lshlrev_b32_e32 v147, 2, v139
	v_add_u32_e32 v139, 1, v139
	v_add_u32_e32 v143, 0xf01, v141
	v_cmpx_gt_u32_e32 vcc, 0x400, v147
	global_store_dword v147, v143, s[40:41]
	s_mov_b64 exec, s[62:63]
	v_lshlrev_b32_e32 v148, 2, v139
	v_add_u32_e32 v139, 1, v139
	v_add_u32_e32 v144, 0xf02, v141
	v_cmpx_gt_u32_e32 vcc, 0x400, v148
	global_store_dword v148, v144, s[40:41]
	s_mov_b64 exec, s[64:65]
	v_lshlrev_b32_e32 v214, 2, v139
	v_add_u32_e32 v139, 1, v139
	v_add_u32_e32 v145, 0xf03, v141
	v_cmpx_gt_u32_e32 vcc, 0x400, v214
	global_store_dword v214, v145, s[40:41]
	s_mov_b64 exec, -1
	s_bcnt1_i32_b64 s4, s[58:59]
	s_add_i32 s26, s26, s4
	s_bcnt1_i32_b64 s4, s[60:61]
	s_add_i32 s26, s26, s4
	s_bcnt1_i32_b64 s4, s[62:63]
	s_add_i32 s26, s26, s4
	s_bcnt1_i32_b64 s4, s[64:65]
	s_add_i32 s26, s26, s4
.Lsel_fin_bend:
	s_mov_b32 s16, s36
	s_cmp_lt_i32 s16, s2
	s_cbranch_scc0 .Lsel_fin_done
	s_waitcnt vmcnt(63)
	s_branch .Lsel_fin_loop

.Lsel_simple:
	s_cmp_lg_u32 s31, 0
	s_cbranch_scc1 .Lsel_simple_neg
	s_mov_b32 s16, 0
	s_waitcnt vmcnt(0)

.Lsel_fsp_body:
	v_add_u32_e32 v141, s16, v56
	v_cmp_ge_i32_e64 s[58:59], v2, s76
	v_cmp_ge_i32_e64 s[60:61], v3, s76
	v_cmp_ge_i32_e64 s[62:63], v4, s76
	v_cmp_ge_i32_e64 s[64:65], v5, s76
	v_mov_b32_e32 v139, s26
	v_mbcnt_lo_u32_b32 v139, s58, v139
	v_mbcnt_hi_u32_b32 v139, s59, v139
	v_mbcnt_lo_u32_b32 v139, s60, v139
	v_mbcnt_hi_u32_b32 v139, s61, v139
	v_mbcnt_lo_u32_b32 v139, s62, v139
	v_mbcnt_hi_u32_b32 v139, s63, v139
	v_mbcnt_lo_u32_b32 v139, s64, v139
	v_mbcnt_hi_u32_b32 v139, s65, v139
	v_lshlrev_b32_e32 v139, 2, v139
	s_mov_b64 exec, s[58:59]
	v_add_u32_e32 v142, 0, v141
	global_store_dword v139, v142, s[40:41]
	v_add_u32_e32 v139, 4, v139
	s_mov_b64 exec, s[60:61]
	v_add_u32_e32 v143, 1, v141
	global_store_dword v139, v143, s[40:41]
	v_add_u32_e32 v139, 4, v139
	s_mov_b64 exec, s[62:63]
	v_add_u32_e32 v144, 2, v141
	global_store_dword v139, v144, s[40:41]
	v_add_u32_e32 v139, 4, v139
	s_mov_b64 exec, s[64:65]
	v_add_u32_e32 v145, 3, v141
	global_store_dword v139, v145, s[40:41]
	v_add_u32_e32 v139, 4, v139
	s_mov_b64 exec, -1
	s_bcnt1_i32_b64 s4, s[58:59]
	s_add_i32 s26, s26, s4
	s_bcnt1_i32_b64 s4, s[60:61]
	s_add_i32 s26, s26, s4
	s_bcnt1_i32_b64 s4, s[62:63]
	s_add_i32 s26, s26, s4
	s_bcnt1_i32_b64 s4, s[64:65]
	s_add_i32 s26, s26, s4
	s_cmp_le_u32 s79, 1
	s_cbranch_scc1 .Lsel_fsp_bend
	v_cmp_ge_i32_e64 s[58:59], v6, s76
	v_cmp_ge_i32_e64 s[60:61], v7, s76
	v_cmp_ge_i32_e64 s[62:63], v8, s76
	v_cmp_ge_i32_e64 s[64:65], v9, s76
	v_mov_b32_e32 v139, s26
	v_mbcnt_lo_u32_b32 v139, s58, v139
	v_mbcnt_hi_u32_b32 v139, s59, v139
	v_mbcnt_lo_u32_b32 v139, s60, v139
	v_mbcnt_hi_u32_b32 v139, s61, v139
	v_mbcnt_lo_u32_b32 v139, s62, v139
	v_mbcnt_hi_u32_b32 v139, s63, v139
	v_mbcnt_lo_u32_b32 v139, s64, v139
	v_mbcnt_hi_u32_b32 v139, s65, v139
	v_lshlrev_b32_e32 v139, 2, v139
	s_mov_b64 exec, s[58:59]
	v_add_u32_e32 v142, 0x100, v141
	global_store_dword v139, v142, s[40:41]
	v_add_u32_e32 v139, 4, v139
	s_mov_b64 exec, s[60:61]
	v_add_u32_e32 v143, 0x101, v141
	global_store_dword v139, v143, s[40:41]
	v_add_u32_e32 v139, 4, v139
	s_mov_b64 exec, s[62:63]
	v_add_u32_e32 v144, 0x102, v141
	global_store_dword v139, v144, s[40:41]
	v_add_u32_e32 v139, 4, v139
	s_mov_b64 exec, s[64:65]
	v_add_u32_e32 v145, 0x103, v141
	global_store_dword v139, v145, s[40:41]
	v_add_u32_e32 v139, 4, v139
	s_mov_b64 exec, -1
	s_bcnt1_i32_b64 s4, s[58:59]
	s_add_i32 s26, s26, s4
	s_bcnt1_i32_b64 s4, s[60:61]
	s_add_i32 s26, s26, s4
	s_bcnt1_i32_b64 s4, s[62:63]
	s_add_i32 s26, s26, s4
	s_bcnt1_i32_b64 s4, s[64:65]
	s_add_i32 s26, s26, s4
	s_cmp_le_u32 s79, 2
	s_cbranch_scc1 .Lsel_fsp_bend
	v_cmp_ge_i32_e64 s[58:59], v10, s76
	v_cmp_ge_i32_e64 s[60:61], v11, s76
	v_cmp_ge_i32_e64 s[62:63], v12, s76
	v_cmp_ge_i32_e64 s[64:65], v13, s76
	v_mov_b32_e32 v139, s26
	v_mbcnt_lo_u32_b32 v139, s58, v139
	v_mbcnt_hi_u32_b32 v139, s59, v139
	v_mbcnt_lo_u32_b32 v139, s60, v139
	v_mbcnt_hi_u32_b32 v139, s61, v139
	v_mbcnt_lo_u32_b32 v139, s62, v139
	v_mbcnt_hi_u32_b32 v139, s63, v139
	v_mbcnt_lo_u32_b32 v139, s64, v139
	v_mbcnt_hi_u32_b32 v139, s65, v139
	v_lshlrev_b32_e32 v139, 2, v139
	s_mov_b64 exec, s[58:59]
	v_add_u32_e32 v142, 0x200, v141
	global_store_dword v139, v142, s[40:41]
	v_add_u32_e32 v139, 4, v139
	s_mov_b64 exec, s[60:61]
	v_add_u32_e32 v143, 0x201, v141
	global_store_dword v139, v143, s[40:41]
	v_add_u32_e32 v139, 4, v139
	s_mov_b64 exec, s[62:63]
	v_add_u32_e32 v144, 0x202, v141
	global_store_dword v139, v144, s[40:41]
	v_add_u32_e32 v139, 4, v139
	s_mov_b64 exec, s[64:65]
	v_add_u32_e32 v145, 0x203, v141
	global_store_dword v139, v145, s[40:41]
	v_add_u32_e32 v139, 4, v139
	s_mov_b64 exec, -1
	s_bcnt1_i32_b64 s4, s[58:59]
	s_add_i32 s26, s26, s4
	s_bcnt1_i32_b64 s4, s[60:61]
	s_add_i32 s26, s26, s4
	s_bcnt1_i32_b64 s4, s[62:63]
	s_add_i32 s26, s26, s4
	s_bcnt1_i32_b64 s4, s[64:65]
	s_add_i32 s26, s26, s4
	s_cmp_le_u32 s79, 3
	s_cbranch_scc1 .Lsel_fsp_bend
	v_cmp_ge_i32_e64 s[58:59], v14, s76
	v_cmp_ge_i32_e64 s[60:61], v15, s76
	v_cmp_ge_i32_e64 s[62:63], v16, s76
	v_cmp_ge_i32_e64 s[64:65], v17, s76
	v_mov_b32_e32 v139, s26
	v_mbcnt_lo_u32_b32 v139, s58, v139
	v_mbcnt_hi_u32_b32 v139, s59, v139
	v_mbcnt_lo_u32_b32 v139, s60, v139
	v_mbcnt_hi_u32_b32 v139, s61, v139
	v_mbcnt_lo_u32_b32 v139, s62, v139
	v_mbcnt_hi_u32_b32 v139, s63, v139
	v_mbcnt_lo_u32_b32 v139, s64, v139
	v_mbcnt_hi_u32_b32 v139, s65, v139
	v_lshlrev_b32_e32 v139, 2, v139
	s_mov_b64 exec, s[58:59]
	v_add_u32_e32 v142, 0x300, v141
	global_store_dword v139, v142, s[40:41]
	v_add_u32_e32 v139, 4, v139
	s_mov_b64 exec, s[60:61]
	v_add_u32_e32 v143, 0x301, v141
	global_store_dword v139, v143, s[40:41]
	v_add_u32_e32 v139, 4, v139
	s_mov_b64 exec, s[62:63]
	v_add_u32_e32 v144, 0x302, v141
	global_store_dword v139, v144, s[40:41]
	v_add_u32_e32 v139, 4, v139
	s_mov_b64 exec, s[64:65]
	v_add_u32_e32 v145, 0x303, v141
	global_store_dword v139, v145, s[40:41]
	v_add_u32_e32 v139, 4, v139
	s_mov_b64 exec, -1
	s_bcnt1_i32_b64 s4, s[58:59]
	s_add_i32 s26, s26, s4
	s_bcnt1_i32_b64 s4, s[60:61]
	s_add_i32 s26, s26, s4
	s_bcnt1_i32_b64 s4, s[62:63]
	s_add_i32 s26, s26, s4
	s_bcnt1_i32_b64 s4, s[64:65]
	s_add_i32 s26, s26, s4
	s_cmp_le_u32 s79, 4
	s_cbranch_scc1 .Lsel_fsp_bend
	v_cmp_ge_i32_e64 s[58:59], v18, s76
	v_cmp_ge_i32_e64 s[60:61], v19, s76
	v_cmp_ge_i32_e64 s[62:63], v20, s76
	v_cmp_ge_i32_e64 s[64:65], v21, s76
	v_mov_b32_e32 v139, s26
	v_mbcnt_lo_u32_b32 v139, s58, v139
	v_mbcnt_hi_u32_b32 v139, s59, v139
	v_mbcnt_lo_u32_b32 v139, s60, v139
	v_mbcnt_hi_u32_b32 v139, s61, v139
	v_mbcnt_lo_u32_b32 v139, s62, v139
	v_mbcnt_hi_u32_b32 v139, s63, v139
	v_mbcnt_lo_u32_b32 v139, s64, v139
	v_mbcnt_hi_u32_b32 v139, s65, v139
	v_lshlrev_b32_e32 v139, 2, v139
	s_mov_b64 exec, s[58:59]
	v_add_u32_e32 v142, 0x400, v141
	global_store_dword v139, v142, s[40:41]
	v_add_u32_e32 v139, 4, v139
	s_mov_b64 exec, s[60:61]
	v_add_u32_e32 v143, 0x401, v141
	global_store_dword v139, v143, s[40:41]
	v_add_u32_e32 v139, 4, v139
	s_mov_b64 exec, s[62:63]
	v_add_u32_e32 v144, 0x402, v141
	global_store_dword v139, v144, s[40:41]
	v_add_u32_e32 v139, 4, v139
	s_mov_b64 exec, s[64:65]
	v_add_u32_e32 v145, 0x403, v141
	global_store_dword v139, v145, s[40:41]
	v_add_u32_e32 v139, 4, v139
	s_mov_b64 exec, -1
	s_bcnt1_i32_b64 s4, s[58:59]
	s_add_i32 s26, s26, s4
	s_bcnt1_i32_b64 s4, s[60:61]
	s_add_i32 s26, s26, s4
	s_bcnt1_i32_b64 s4, s[62:63]
	s_add_i32 s26, s26, s4
	s_bcnt1_i32_b64 s4, s[64:65]
	s_add_i32 s26, s26, s4
	s_cmp_le_u32 s79, 5
	s_cbranch_scc1 .Lsel_fsp_bend
	v_cmp_ge_i32_e64 s[58:59], v22, s76
	v_cmp_ge_i32_e64 s[60:61], v23, s76
	v_cmp_ge_i32_e64 s[62:63], v24, s76
	v_cmp_ge_i32_e64 s[64:65], v25, s76
	v_mov_b32_e32 v139, s26
	v_mbcnt_lo_u32_b32 v139, s58, v139
	v_mbcnt_hi_u32_b32 v139, s59, v139
	v_mbcnt_lo_u32_b32 v139, s60, v139
	v_mbcnt_hi_u32_b32 v139, s61, v139
	v_mbcnt_lo_u32_b32 v139, s62, v139
	v_mbcnt_hi_u32_b32 v139, s63, v139
	v_mbcnt_lo_u32_b32 v139, s64, v139
	v_mbcnt_hi_u32_b32 v139, s65, v139
	v_lshlrev_b32_e32 v139, 2, v139
	s_mov_b64 exec, s[58:59]
	v_add_u32_e32 v142, 0x500, v141
	global_store_dword v139, v142, s[40:41]
	v_add_u32_e32 v139, 4, v139
	s_mov_b64 exec, s[60:61]
	v_add_u32_e32 v143, 0x501, v141
	global_store_dword v139, v143, s[40:41]
	v_add_u32_e32 v139, 4, v139
	s_mov_b64 exec, s[62:63]
	v_add_u32_e32 v144, 0x502, v141
	global_store_dword v139, v144, s[40:41]
	v_add_u32_e32 v139, 4, v139
	s_mov_b64 exec, s[64:65]
	v_add_u32_e32 v145, 0x503, v141
	global_store_dword v139, v145, s[40:41]
	v_add_u32_e32 v139, 4, v139
	s_mov_b64 exec, -1
	s_bcnt1_i32_b64 s4, s[58:59]
	s_add_i32 s26, s26, s4
	s_bcnt1_i32_b64 s4, s[60:61]
	s_add_i32 s26, s26, s4
	s_bcnt1_i32_b64 s4, s[62:63]
	s_add_i32 s26, s26, s4
	s_bcnt1_i32_b64 s4, s[64:65]
	s_add_i32 s26, s26, s4
	s_cmp_le_u32 s79, 6
	s_cbranch_scc1 .Lsel_fsp_bend
	v_cmp_ge_i32_e64 s[58:59], v26, s76
	v_cmp_ge_i32_e64 s[60:61], v27, s76
	v_cmp_ge_i32_e64 s[62:63], v28, s76
	v_cmp_ge_i32_e64 s[64:65], v29, s76
	v_mov_b32_e32 v139, s26
	v_mbcnt_lo_u32_b32 v139, s58, v139
	v_mbcnt_hi_u32_b32 v139, s59, v139
	v_mbcnt_lo_u32_b32 v139, s60, v139
	v_mbcnt_hi_u32_b32 v139, s61, v139
	v_mbcnt_lo_u32_b32 v139, s62, v139
	v_mbcnt_hi_u32_b32 v139, s63, v139
	v_mbcnt_lo_u32_b32 v139, s64, v139
	v_mbcnt_hi_u32_b32 v139, s65, v139
	v_lshlrev_b32_e32 v139, 2, v139
	s_mov_b64 exec, s[58:59]
	v_add_u32_e32 v142, 0x600, v141
	global_store_dword v139, v142, s[40:41]
	v_add_u32_e32 v139, 4, v139
	s_mov_b64 exec, s[60:61]
	v_add_u32_e32 v143, 0x601, v141
	global_store_dword v139, v143, s[40:41]
	v_add_u32_e32 v139, 4, v139
	s_mov_b64 exec, s[62:63]
	v_add_u32_e32 v144, 0x602, v141
	global_store_dword v139, v144, s[40:41]
	v_add_u32_e32 v139, 4, v139
	s_mov_b64 exec, s[64:65]
	v_add_u32_e32 v145, 0x603, v141
	global_store_dword v139, v145, s[40:41]
	v_add_u32_e32 v139, 4, v139
	s_mov_b64 exec, -1
	s_bcnt1_i32_b64 s4, s[58:59]
	s_add_i32 s26, s26, s4
	s_bcnt1_i32_b64 s4, s[60:61]
	s_add_i32 s26, s26, s4
	s_bcnt1_i32_b64 s4, s[62:63]
	s_add_i32 s26, s26, s4
	s_bcnt1_i32_b64 s4, s[64:65]
	s_add_i32 s26, s26, s4
	s_cmp_le_u32 s79, 7
	s_cbranch_scc1 .Lsel_fsp_bend
	v_cmp_ge_i32_e64 s[58:59], v30, s76
	v_cmp_ge_i32_e64 s[60:61], v31, s76
	v_cmp_ge_i32_e64 s[62:63], v32, s76
	v_cmp_ge_i32_e64 s[64:65], v33, s76
	v_mov_b32_e32 v139, s26
	v_mbcnt_lo_u32_b32 v139, s58, v139
	v_mbcnt_hi_u32_b32 v139, s59, v139
	v_mbcnt_lo_u32_b32 v139, s60, v139
	v_mbcnt_hi_u32_b32 v139, s61, v139
	v_mbcnt_lo_u32_b32 v139, s62, v139
	v_mbcnt_hi_u32_b32 v139, s63, v139
	v_mbcnt_lo_u32_b32 v139, s64, v139
	v_mbcnt_hi_u32_b32 v139, s65, v139
	v_lshlrev_b32_e32 v139, 2, v139
	s_mov_b64 exec, s[58:59]
	v_add_u32_e32 v142, 0x700, v141
	global_store_dword v139, v142, s[40:41]
	v_add_u32_e32 v139, 4, v139
	s_mov_b64 exec, s[60:61]
	v_add_u32_e32 v143, 0x701, v141
	global_store_dword v139, v143, s[40:41]
	v_add_u32_e32 v139, 4, v139
	s_mov_b64 exec, s[62:63]
	v_add_u32_e32 v144, 0x702, v141
	global_store_dword v139, v144, s[40:41]
	v_add_u32_e32 v139, 4, v139
	s_mov_b64 exec, s[64:65]
	v_add_u32_e32 v145, 0x703, v141
	global_store_dword v139, v145, s[40:41]
	v_add_u32_e32 v139, 4, v139
	s_mov_b64 exec, -1
	s_bcnt1_i32_b64 s4, s[58:59]
	s_add_i32 s26, s26, s4
	s_bcnt1_i32_b64 s4, s[60:61]
	s_add_i32 s26, s26, s4
	s_bcnt1_i32_b64 s4, s[62:63]
	s_add_i32 s26, s26, s4
	s_bcnt1_i32_b64 s4, s[64:65]
	s_add_i32 s26, s26, s4
	s_cmp_le_u32 s79, 8
	s_cbranch_scc1 .Lsel_fsp_bend
	v_cmp_ge_i32_e64 s[58:59], v34, s76
	v_cmp_ge_i32_e64 s[60:61], v35, s76
	v_cmp_ge_i32_e64 s[62:63], v36, s76
	v_cmp_ge_i32_e64 s[64:65], v37, s76
	v_mov_b32_e32 v139, s26
	v_mbcnt_lo_u32_b32 v139, s58, v139
	v_mbcnt_hi_u32_b32 v139, s59, v139
	v_mbcnt_lo_u32_b32 v139, s60, v139
	v_mbcnt_hi_u32_b32 v139, s61, v139
	v_mbcnt_lo_u32_b32 v139, s62, v139
	v_mbcnt_hi_u32_b32 v139, s63, v139
	v_mbcnt_lo_u32_b32 v139, s64, v139
	v_mbcnt_hi_u32_b32 v139, s65, v139
	v_lshlrev_b32_e32 v139, 2, v139
	s_mov_b64 exec, s[58:59]
	v_add_u32_e32 v142, 0x800, v141
	global_store_dword v139, v142, s[40:41]
	v_add_u32_e32 v139, 4, v139
	s_mov_b64 exec, s[60:61]
	v_add_u32_e32 v143, 0x801, v141
	global_store_dword v139, v143, s[40:41]
	v_add_u32_e32 v139, 4, v139
	s_mov_b64 exec, s[62:63]
	v_add_u32_e32 v144, 0x802, v141
	global_store_dword v139, v144, s[40:41]
	v_add_u32_e32 v139, 4, v139
	s_mov_b64 exec, s[64:65]
	v_add_u32_e32 v145, 0x803, v141
	global_store_dword v139, v145, s[40:41]
	v_add_u32_e32 v139, 4, v139
	s_mov_b64 exec, -1
	s_bcnt1_i32_b64 s4, s[58:59]
	s_add_i32 s26, s26, s4
	s_bcnt1_i32_b64 s4, s[60:61]
	s_add_i32 s26, s26, s4
	s_bcnt1_i32_b64 s4, s[62:63]
	s_add_i32 s26, s26, s4
	s_bcnt1_i32_b64 s4, s[64:65]
	s_add_i32 s26, s26, s4
	s_cmp_le_u32 s79, 9
	s_cbranch_scc1 .Lsel_fsp_bend
	v_cmp_ge_i32_e64 s[58:59], v38, s76
	v_cmp_ge_i32_e64 s[60:61], v39, s76
	v_cmp_ge_i32_e64 s[62:63], v40, s76
	v_cmp_ge_i32_e64 s[64:65], v41, s76
	v_mov_b32_e32 v139, s26
	v_mbcnt_lo_u32_b32 v139, s58, v139
	v_mbcnt_hi_u32_b32 v139, s59, v139
	v_mbcnt_lo_u32_b32 v139, s60, v139
	v_mbcnt_hi_u32_b32 v139, s61, v139
	v_mbcnt_lo_u32_b32 v139, s62, v139
	v_mbcnt_hi_u32_b32 v139, s63, v139
	v_mbcnt_lo_u32_b32 v139, s64, v139
	v_mbcnt_hi_u32_b32 v139, s65, v139
	v_lshlrev_b32_e32 v139, 2, v139
	s_mov_b64 exec, s[58:59]
	v_add_u32_e32 v142, 0x900, v141
	global_store_dword v139, v142, s[40:41]
	v_add_u32_e32 v139, 4, v139
	s_mov_b64 exec, s[60:61]
	v_add_u32_e32 v143, 0x901, v141
	global_store_dword v139, v143, s[40:41]
	v_add_u32_e32 v139, 4, v139
	s_mov_b64 exec, s[62:63]
	v_add_u32_e32 v144, 0x902, v141
	global_store_dword v139, v144, s[40:41]
	v_add_u32_e32 v139, 4, v139
	s_mov_b64 exec, s[64:65]
	v_add_u32_e32 v145, 0x903, v141
	global_store_dword v139, v145, s[40:41]
	v_add_u32_e32 v139, 4, v139
	s_mov_b64 exec, -1
	s_bcnt1_i32_b64 s4, s[58:59]
	s_add_i32 s26, s26, s4
	s_bcnt1_i32_b64 s4, s[60:61]
	s_add_i32 s26, s26, s4
	s_bcnt1_i32_b64 s4, s[62:63]
	s_add_i32 s26, s26, s4
	s_bcnt1_i32_b64 s4, s[64:65]
	s_add_i32 s26, s26, s4
	s_cmp_le_u32 s79, 10
	s_cbranch_scc1 .Lsel_fsp_bend
	v_cmp_ge_i32_e64 s[58:59], v42, s76
	v_cmp_ge_i32_e64 s[60:61], v43, s76
	v_cmp_ge_i32_e64 s[62:63], v44, s76
	v_cmp_ge_i32_e64 s[64:65], v45, s76
	v_mov_b32_e32 v139, s26
	v_mbcnt_lo_u32_b32 v139, s58, v139
	v_mbcnt_hi_u32_b32 v139, s59, v139
	v_mbcnt_lo_u32_b32 v139, s60, v139
	v_mbcnt_hi_u32_b32 v139, s61, v139
	v_mbcnt_lo_u32_b32 v139, s62, v139
	v_mbcnt_hi_u32_b32 v139, s63, v139
	v_mbcnt_lo_u32_b32 v139, s64, v139
	v_mbcnt_hi_u32_b32 v139, s65, v139
	v_lshlrev_b32_e32 v139, 2, v139
	s_mov_b64 exec, s[58:59]
	v_add_u32_e32 v142, 0xa00, v141
	global_store_dword v139, v142, s[40:41]
	v_add_u32_e32 v139, 4, v139
	s_mov_b64 exec, s[60:61]
	v_add_u32_e32 v143, 0xa01, v141
	global_store_dword v139, v143, s[40:41]
	v_add_u32_e32 v139, 4, v139
	s_mov_b64 exec, s[62:63]
	v_add_u32_e32 v144, 0xa02, v141
	global_store_dword v139, v144, s[40:41]
	v_add_u32_e32 v139, 4, v139
	s_mov_b64 exec, s[64:65]
	v_add_u32_e32 v145, 0xa03, v141
	global_store_dword v139, v145, s[40:41]
	v_add_u32_e32 v139, 4, v139
	s_mov_b64 exec, -1
	s_bcnt1_i32_b64 s4, s[58:59]
	s_add_i32 s26, s26, s4
	s_bcnt1_i32_b64 s4, s[60:61]
	s_add_i32 s26, s26, s4
	s_bcnt1_i32_b64 s4, s[62:63]
	s_add_i32 s26, s26, s4
	s_bcnt1_i32_b64 s4, s[64:65]
	s_add_i32 s26, s26, s4
	s_cmp_le_u32 s79, 11
	s_cbranch_scc1 .Lsel_fsp_bend
	v_cmp_ge_i32_e64 s[58:59], v46, s76
	v_cmp_ge_i32_e64 s[60:61], v47, s76
	v_cmp_ge_i32_e64 s[62:63], v48, s76
	v_cmp_ge_i32_e64 s[64:65], v49, s76
	v_mov_b32_e32 v139, s26
	v_mbcnt_lo_u32_b32 v139, s58, v139
	v_mbcnt_hi_u32_b32 v139, s59, v139
	v_mbcnt_lo_u32_b32 v139, s60, v139
	v_mbcnt_hi_u32_b32 v139, s61, v139
	v_mbcnt_lo_u32_b32 v139, s62, v139
	v_mbcnt_hi_u32_b32 v139, s63, v139
	v_mbcnt_lo_u32_b32 v139, s64, v139
	v_mbcnt_hi_u32_b32 v139, s65, v139
	v_lshlrev_b32_e32 v139, 2, v139
	s_mov_b64 exec, s[58:59]
	v_add_u32_e32 v142, 0xb00, v141
	global_store_dword v139, v142, s[40:41]
	v_add_u32_e32 v139, 4, v139
	s_mov_b64 exec, s[60:61]
	v_add_u32_e32 v143, 0xb01, v141
	global_store_dword v139, v143, s[40:41]
	v_add_u32_e32 v139, 4, v139
	s_mov_b64 exec, s[62:63]
	v_add_u32_e32 v144, 0xb02, v141
	global_store_dword v139, v144, s[40:41]
	v_add_u32_e32 v139, 4, v139
	s_mov_b64 exec, s[64:65]
	v_add_u32_e32 v145, 0xb03, v141
	global_store_dword v139, v145, s[40:41]
	v_add_u32_e32 v139, 4, v139
	s_mov_b64 exec, -1
	s_bcnt1_i32_b64 s4, s[58:59]
	s_add_i32 s26, s26, s4
	s_bcnt1_i32_b64 s4, s[60:61]
	s_add_i32 s26, s26, s4
	s_bcnt1_i32_b64 s4, s[62:63]
	s_add_i32 s26, s26, s4
	s_bcnt1_i32_b64 s4, s[64:65]
	s_add_i32 s26, s26, s4
	s_cmp_le_u32 s79, 12
	s_cbranch_scc1 .Lsel_fsp_bend
	v_cmp_ge_i32_e64 s[58:59], v118, s76
	v_cmp_ge_i32_e64 s[60:61], v119, s76
	v_cmp_ge_i32_e64 s[62:63], v120, s76
	v_cmp_ge_i32_e64 s[64:65], v121, s76
	v_mov_b32_e32 v139, s26
	v_mbcnt_lo_u32_b32 v139, s58, v139
	v_mbcnt_hi_u32_b32 v139, s59, v139
	v_mbcnt_lo_u32_b32 v139, s60, v139
	v_mbcnt_hi_u32_b32 v139, s61, v139
	v_mbcnt_lo_u32_b32 v139, s62, v139
	v_mbcnt_hi_u32_b32 v139, s63, v139
	v_mbcnt_lo_u32_b32 v139, s64, v139
	v_mbcnt_hi_u32_b32 v139, s65, v139
	v_lshlrev_b32_e32 v139, 2, v139
	s_mov_b64 exec, s[58:59]
	v_add_u32_e32 v142, 0xc00, v141
	global_store_dword v139, v142, s[40:41]
	v_add_u32_e32 v139, 4, v139
	s_mov_b64 exec, s[60:61]
	v_add_u32_e32 v143, 0xc01, v141
	global_store_dword v139, v143, s[40:41]
	v_add_u32_e32 v139, 4, v139
	s_mov_b64 exec, s[62:63]
	v_add_u32_e32 v144, 0xc02, v141
	global_store_dword v139, v144, s[40:41]
	v_add_u32_e32 v139, 4, v139
	s_mov_b64 exec, s[64:65]
	v_add_u32_e32 v145, 0xc03, v141
	global_store_dword v139, v145, s[40:41]
	v_add_u32_e32 v139, 4, v139
	s_mov_b64 exec, -1
	s_bcnt1_i32_b64 s4, s[58:59]
	s_add_i32 s26, s26, s4
	s_bcnt1_i32_b64 s4, s[60:61]
	s_add_i32 s26, s26, s4
	s_bcnt1_i32_b64 s4, s[62:63]
	s_add_i32 s26, s26, s4
	s_bcnt1_i32_b64 s4, s[64:65]
	s_add_i32 s26, s26, s4
	s_cmp_le_u32 s79, 13
	s_cbranch_scc1 .Lsel_fsp_bend
	v_cmp_ge_i32_e64 s[58:59], v122, s76
	v_cmp_ge_i32_e64 s[60:61], v123, s76
	v_cmp_ge_i32_e64 s[62:63], v124, s76
	v_cmp_ge_i32_e64 s[64:65], v125, s76
	v_mov_b32_e32 v139, s26
	v_mbcnt_lo_u32_b32 v139, s58, v139
	v_mbcnt_hi_u32_b32 v139, s59, v139
	v_mbcnt_lo_u32_b32 v139, s60, v139
	v_mbcnt_hi_u32_b32 v139, s61, v139
	v_mbcnt_lo_u32_b32 v139, s62, v139
	v_mbcnt_hi_u32_b32 v139, s63, v139
	v_mbcnt_lo_u32_b32 v139, s64, v139
	v_mbcnt_hi_u32_b32 v139, s65, v139
	v_lshlrev_b32_e32 v139, 2, v139
	s_mov_b64 exec, s[58:59]
	v_add_u32_e32 v142, 0xd00, v141
	global_store_dword v139, v142, s[40:41]
	v_add_u32_e32 v139, 4, v139
	s_mov_b64 exec, s[60:61]
	v_add_u32_e32 v143, 0xd01, v141
	global_store_dword v139, v143, s[40:41]
	v_add_u32_e32 v139, 4, v139
	s_mov_b64 exec, s[62:63]
	v_add_u32_e32 v144, 0xd02, v141
	global_store_dword v139, v144, s[40:41]
	v_add_u32_e32 v139, 4, v139
	s_mov_b64 exec, s[64:65]
	v_add_u32_e32 v145, 0xd03, v141
	global_store_dword v139, v145, s[40:41]
	v_add_u32_e32 v139, 4, v139
	s_mov_b64 exec, -1
	s_bcnt1_i32_b64 s4, s[58:59]
	s_add_i32 s26, s26, s4
	s_bcnt1_i32_b64 s4, s[60:61]
	s_add_i32 s26, s26, s4
	s_bcnt1_i32_b64 s4, s[62:63]
	s_add_i32 s26, s26, s4
	s_bcnt1_i32_b64 s4, s[64:65]
	s_add_i32 s26, s26, s4
	s_cmp_le_u32 s79, 14
	s_cbranch_scc1 .Lsel_fsp_bend
	v_cmp_ge_i32_e64 s[58:59], v126, s76
	v_cmp_ge_i32_e64 s[60:61], v127, s76
	v_cmp_ge_i32_e64 s[62:63], v128, s76
	v_cmp_ge_i32_e64 s[64:65], v129, s76
	v_mov_b32_e32 v139, s26
	v_mbcnt_lo_u32_b32 v139, s58, v139
	v_mbcnt_hi_u32_b32 v139, s59, v139
	v_mbcnt_lo_u32_b32 v139, s60, v139
	v_mbcnt_hi_u32_b32 v139, s61, v139
	v_mbcnt_lo_u32_b32 v139, s62, v139
	v_mbcnt_hi_u32_b32 v139, s63, v139
	v_mbcnt_lo_u32_b32 v139, s64, v139
	v_mbcnt_hi_u32_b32 v139, s65, v139
	v_lshlrev_b32_e32 v139, 2, v139
	s_mov_b64 exec, s[58:59]
	v_add_u32_e32 v142, 0xe00, v141
	global_store_dword v139, v142, s[40:41]
	v_add_u32_e32 v139, 4, v139
	s_mov_b64 exec, s[60:61]
	v_add_u32_e32 v143, 0xe01, v141
	global_store_dword v139, v143, s[40:41]
	v_add_u32_e32 v139, 4, v139
	s_mov_b64 exec, s[62:63]
	v_add_u32_e32 v144, 0xe02, v141
	global_store_dword v139, v144, s[40:41]
	v_add_u32_e32 v139, 4, v139
	s_mov_b64 exec, s[64:65]
	v_add_u32_e32 v145, 0xe03, v141
	global_store_dword v139, v145, s[40:41]
	v_add_u32_e32 v139, 4, v139
	s_mov_b64 exec, -1
	s_bcnt1_i32_b64 s4, s[58:59]
	s_add_i32 s26, s26, s4
	s_bcnt1_i32_b64 s4, s[60:61]
	s_add_i32 s26, s26, s4
	s_bcnt1_i32_b64 s4, s[62:63]
	s_add_i32 s26, s26, s4
	s_bcnt1_i32_b64 s4, s[64:65]
	s_add_i32 s26, s26, s4
	s_cmp_le_u32 s79, 15
	s_cbranch_scc1 .Lsel_fsp_bend
	v_cmp_ge_i32_e64 s[58:59], v130, s76
	v_cmp_ge_i32_e64 s[60:61], v131, s76
	v_cmp_ge_i32_e64 s[62:63], v132, s76
	v_cmp_ge_i32_e64 s[64:65], v133, s76
	v_mov_b32_e32 v139, s26
	v_mbcnt_lo_u32_b32 v139, s58, v139
	v_mbcnt_hi_u32_b32 v139, s59, v139
	v_mbcnt_lo_u32_b32 v139, s60, v139
	v_mbcnt_hi_u32_b32 v139, s61, v139
	v_mbcnt_lo_u32_b32 v139, s62, v139
	v_mbcnt_hi_u32_b32 v139, s63, v139
	v_mbcnt_lo_u32_b32 v139, s64, v139
	v_mbcnt_hi_u32_b32 v139, s65, v139
	v_lshlrev_b32_e32 v139, 2, v139
	s_mov_b64 exec, s[58:59]
	v_add_u32_e32 v142, 0xf00, v141
	global_store_dword v139, v142, s[40:41]
	v_add_u32_e32 v139, 4, v139
	s_mov_b64 exec, s[60:61]
	v_add_u32_e32 v143, 0xf01, v141
	global_store_dword v139, v143, s[40:41]
	v_add_u32_e32 v139, 4, v139
	s_mov_b64 exec, s[62:63]
	v_add_u32_e32 v144, 0xf02, v141
	global_store_dword v139, v144, s[40:41]
	v_add_u32_e32 v139, 4, v139
	s_mov_b64 exec, s[64:65]
	v_add_u32_e32 v145, 0xf03, v141
	global_store_dword v139, v145, s[40:41]
	v_add_u32_e32 v139, 4, v139
	s_mov_b64 exec, -1
	s_bcnt1_i32_b64 s4, s[58:59]
	s_add_i32 s26, s26, s4
	s_bcnt1_i32_b64 s4, s[60:61]
	s_add_i32 s26, s26, s4
	s_bcnt1_i32_b64 s4, s[62:63]
	s_add_i32 s26, s26, s4
	s_bcnt1_i32_b64 s4, s[64:65]
	s_add_i32 s26, s26, s4

.Lsel_simple_neg:
	s_mov_b32 s16, 0
	s_waitcnt vmcnt(0)

.Lsel_fsn_body:
	v_add_u32_e32 v141, s16, v56
	v_cmp_le_u32_e64 s[58:59], v2, s76
	v_cmp_le_u32_e64 s[60:61], v3, s76
	v_cmp_le_u32_e64 s[62:63], v4, s76
	v_cmp_le_u32_e64 s[64:65], v5, s76
	v_mov_b32_e32 v139, s26
	v_mbcnt_lo_u32_b32 v139, s58, v139
	v_mbcnt_hi_u32_b32 v139, s59, v139
	v_mbcnt_lo_u32_b32 v139, s60, v139
	v_mbcnt_hi_u32_b32 v139, s61, v139
	v_mbcnt_lo_u32_b32 v139, s62, v139
	v_mbcnt_hi_u32_b32 v139, s63, v139
	v_mbcnt_lo_u32_b32 v139, s64, v139
	v_mbcnt_hi_u32_b32 v139, s65, v139
	v_lshlrev_b32_e32 v139, 2, v139
	s_mov_b64 exec, s[58:59]
	v_add_u32_e32 v142, 0, v141
	global_store_dword v139, v142, s[40:41]
	v_add_u32_e32 v139, 4, v139
	s_mov_b64 exec, s[60:61]
	v_add_u32_e32 v143, 1, v141
	global_store_dword v139, v143, s[40:41]
	v_add_u32_e32 v139, 4, v139
	s_mov_b64 exec, s[62:63]
	v_add_u32_e32 v144, 2, v141
	global_store_dword v139, v144, s[40:41]
	v_add_u32_e32 v139, 4, v139
	s_mov_b64 exec, s[64:65]
	v_add_u32_e32 v145, 3, v141
	global_store_dword v139, v145, s[40:41]
	v_add_u32_e32 v139, 4, v139
	s_mov_b64 exec, -1
	s_bcnt1_i32_b64 s4, s[58:59]
	s_add_i32 s26, s26, s4
	s_bcnt1_i32_b64 s4, s[60:61]
	s_add_i32 s26, s26, s4
	s_bcnt1_i32_b64 s4, s[62:63]
	s_add_i32 s26, s26, s4
	s_bcnt1_i32_b64 s4, s[64:65]
	s_add_i32 s26, s26, s4
	s_cmp_le_u32 s79, 1
	s_cbranch_scc1 .Lsel_fsn_bend
	v_cmp_le_u32_e64 s[58:59], v6, s76
	v_cmp_le_u32_e64 s[60:61], v7, s76
	v_cmp_le_u32_e64 s[62:63], v8, s76
	v_cmp_le_u32_e64 s[64:65], v9, s76
	v_mov_b32_e32 v139, s26
	v_mbcnt_lo_u32_b32 v139, s58, v139
	v_mbcnt_hi_u32_b32 v139, s59, v139
	v_mbcnt_lo_u32_b32 v139, s60, v139
	v_mbcnt_hi_u32_b32 v139, s61, v139
	v_mbcnt_lo_u32_b32 v139, s62, v139
	v_mbcnt_hi_u32_b32 v139, s63, v139
	v_mbcnt_lo_u32_b32 v139, s64, v139
	v_mbcnt_hi_u32_b32 v139, s65, v139
	v_lshlrev_b32_e32 v139, 2, v139
	s_mov_b64 exec, s[58:59]
	v_add_u32_e32 v142, 0x100, v141
	global_store_dword v139, v142, s[40:41]
	v_add_u32_e32 v139, 4, v139
	s_mov_b64 exec, s[60:61]
	v_add_u32_e32 v143, 0x101, v141
	global_store_dword v139, v143, s[40:41]
	v_add_u32_e32 v139, 4, v139
	s_mov_b64 exec, s[62:63]
	v_add_u32_e32 v144, 0x102, v141
	global_store_dword v139, v144, s[40:41]
	v_add_u32_e32 v139, 4, v139
	s_mov_b64 exec, s[64:65]
	v_add_u32_e32 v145, 0x103, v141
	global_store_dword v139, v145, s[40:41]
	v_add_u32_e32 v139, 4, v139
	s_mov_b64 exec, -1
	s_bcnt1_i32_b64 s4, s[58:59]
	s_add_i32 s26, s26, s4
	s_bcnt1_i32_b64 s4, s[60:61]
	s_add_i32 s26, s26, s4
	s_bcnt1_i32_b64 s4, s[62:63]
	s_add_i32 s26, s26, s4
	s_bcnt1_i32_b64 s4, s[64:65]
	s_add_i32 s26, s26, s4
	s_cmp_le_u32 s79, 2
	s_cbranch_scc1 .Lsel_fsn_bend
	v_cmp_le_u32_e64 s[58:59], v10, s76
	v_cmp_le_u32_e64 s[60:61], v11, s76
	v_cmp_le_u32_e64 s[62:63], v12, s76
	v_cmp_le_u32_e64 s[64:65], v13, s76
	v_mov_b32_e32 v139, s26
	v_mbcnt_lo_u32_b32 v139, s58, v139
	v_mbcnt_hi_u32_b32 v139, s59, v139
	v_mbcnt_lo_u32_b32 v139, s60, v139
	v_mbcnt_hi_u32_b32 v139, s61, v139
	v_mbcnt_lo_u32_b32 v139, s62, v139
	v_mbcnt_hi_u32_b32 v139, s63, v139
	v_mbcnt_lo_u32_b32 v139, s64, v139
	v_mbcnt_hi_u32_b32 v139, s65, v139
	v_lshlrev_b32_e32 v139, 2, v139
	s_mov_b64 exec, s[58:59]
	v_add_u32_e32 v142, 0x200, v141
	global_store_dword v139, v142, s[40:41]
	v_add_u32_e32 v139, 4, v139
	s_mov_b64 exec, s[60:61]
	v_add_u32_e32 v143, 0x201, v141
	global_store_dword v139, v143, s[40:41]
	v_add_u32_e32 v139, 4, v139
	s_mov_b64 exec, s[62:63]
	v_add_u32_e32 v144, 0x202, v141
	global_store_dword v139, v144, s[40:41]
	v_add_u32_e32 v139, 4, v139
	s_mov_b64 exec, s[64:65]
	v_add_u32_e32 v145, 0x203, v141
	global_store_dword v139, v145, s[40:41]
	v_add_u32_e32 v139, 4, v139
	s_mov_b64 exec, -1
	s_bcnt1_i32_b64 s4, s[58:59]
	s_add_i32 s26, s26, s4
	s_bcnt1_i32_b64 s4, s[60:61]
	s_add_i32 s26, s26, s4
	s_bcnt1_i32_b64 s4, s[62:63]
	s_add_i32 s26, s26, s4
	s_bcnt1_i32_b64 s4, s[64:65]
	s_add_i32 s26, s26, s4
	s_cmp_le_u32 s79, 3
	s_cbranch_scc1 .Lsel_fsn_bend
	v_cmp_le_u32_e64 s[58:59], v14, s76
	v_cmp_le_u32_e64 s[60:61], v15, s76
	v_cmp_le_u32_e64 s[62:63], v16, s76
	v_cmp_le_u32_e64 s[64:65], v17, s76
	v_mov_b32_e32 v139, s26
	v_mbcnt_lo_u32_b32 v139, s58, v139
	v_mbcnt_hi_u32_b32 v139, s59, v139
	v_mbcnt_lo_u32_b32 v139, s60, v139
	v_mbcnt_hi_u32_b32 v139, s61, v139
	v_mbcnt_lo_u32_b32 v139, s62, v139
	v_mbcnt_hi_u32_b32 v139, s63, v139
	v_mbcnt_lo_u32_b32 v139, s64, v139
	v_mbcnt_hi_u32_b32 v139, s65, v139
	v_lshlrev_b32_e32 v139, 2, v139
	s_mov_b64 exec, s[58:59]
	v_add_u32_e32 v142, 0x300, v141
	global_store_dword v139, v142, s[40:41]
	v_add_u32_e32 v139, 4, v139
	s_mov_b64 exec, s[60:61]
	v_add_u32_e32 v143, 0x301, v141
	global_store_dword v139, v143, s[40:41]
	v_add_u32_e32 v139, 4, v139
	s_mov_b64 exec, s[62:63]
	v_add_u32_e32 v144, 0x302, v141
	global_store_dword v139, v144, s[40:41]
	v_add_u32_e32 v139, 4, v139
	s_mov_b64 exec, s[64:65]
	v_add_u32_e32 v145, 0x303, v141
	global_store_dword v139, v145, s[40:41]
	v_add_u32_e32 v139, 4, v139
	s_mov_b64 exec, -1
	s_bcnt1_i32_b64 s4, s[58:59]
	s_add_i32 s26, s26, s4
	s_bcnt1_i32_b64 s4, s[60:61]
	s_add_i32 s26, s26, s4
	s_bcnt1_i32_b64 s4, s[62:63]
	s_add_i32 s26, s26, s4
	s_bcnt1_i32_b64 s4, s[64:65]
	s_add_i32 s26, s26, s4
	s_cmp_le_u32 s79, 4
	s_cbranch_scc1 .Lsel_fsn_bend
	v_cmp_le_u32_e64 s[58:59], v18, s76
	v_cmp_le_u32_e64 s[60:61], v19, s76
	v_cmp_le_u32_e64 s[62:63], v20, s76
	v_cmp_le_u32_e64 s[64:65], v21, s76
	v_mov_b32_e32 v139, s26
	v_mbcnt_lo_u32_b32 v139, s58, v139
	v_mbcnt_hi_u32_b32 v139, s59, v139
	v_mbcnt_lo_u32_b32 v139, s60, v139
	v_mbcnt_hi_u32_b32 v139, s61, v139
	v_mbcnt_lo_u32_b32 v139, s62, v139
	v_mbcnt_hi_u32_b32 v139, s63, v139
	v_mbcnt_lo_u32_b32 v139, s64, v139
	v_mbcnt_hi_u32_b32 v139, s65, v139
	v_lshlrev_b32_e32 v139, 2, v139
	s_mov_b64 exec, s[58:59]
	v_add_u32_e32 v142, 0x400, v141
	global_store_dword v139, v142, s[40:41]
	v_add_u32_e32 v139, 4, v139
	s_mov_b64 exec, s[60:61]
	v_add_u32_e32 v143, 0x401, v141
	global_store_dword v139, v143, s[40:41]
	v_add_u32_e32 v139, 4, v139
	s_mov_b64 exec, s[62:63]
	v_add_u32_e32 v144, 0x402, v141
	global_store_dword v139, v144, s[40:41]
	v_add_u32_e32 v139, 4, v139
	s_mov_b64 exec, s[64:65]
	v_add_u32_e32 v145, 0x403, v141
	global_store_dword v139, v145, s[40:41]
	v_add_u32_e32 v139, 4, v139
	s_mov_b64 exec, -1
	s_bcnt1_i32_b64 s4, s[58:59]
	s_add_i32 s26, s26, s4
	s_bcnt1_i32_b64 s4, s[60:61]
	s_add_i32 s26, s26, s4
	s_bcnt1_i32_b64 s4, s[62:63]
	s_add_i32 s26, s26, s4
	s_bcnt1_i32_b64 s4, s[64:65]
	s_add_i32 s26, s26, s4
	s_cmp_le_u32 s79, 5
	s_cbranch_scc1 .Lsel_fsn_bend
	v_cmp_le_u32_e64 s[58:59], v22, s76
	v_cmp_le_u32_e64 s[60:61], v23, s76
	v_cmp_le_u32_e64 s[62:63], v24, s76
	v_cmp_le_u32_e64 s[64:65], v25, s76
	v_mov_b32_e32 v139, s26
	v_mbcnt_lo_u32_b32 v139, s58, v139
	v_mbcnt_hi_u32_b32 v139, s59, v139
	v_mbcnt_lo_u32_b32 v139, s60, v139
	v_mbcnt_hi_u32_b32 v139, s61, v139
	v_mbcnt_lo_u32_b32 v139, s62, v139
	v_mbcnt_hi_u32_b32 v139, s63, v139
	v_mbcnt_lo_u32_b32 v139, s64, v139
	v_mbcnt_hi_u32_b32 v139, s65, v139
	v_lshlrev_b32_e32 v139, 2, v139
	s_mov_b64 exec, s[58:59]
	v_add_u32_e32 v142, 0x500, v141
	global_store_dword v139, v142, s[40:41]
	v_add_u32_e32 v139, 4, v139
	s_mov_b64 exec, s[60:61]
	v_add_u32_e32 v143, 0x501, v141
	global_store_dword v139, v143, s[40:41]
	v_add_u32_e32 v139, 4, v139
	s_mov_b64 exec, s[62:63]
	v_add_u32_e32 v144, 0x502, v141
	global_store_dword v139, v144, s[40:41]
	v_add_u32_e32 v139, 4, v139
	s_mov_b64 exec, s[64:65]
	v_add_u32_e32 v145, 0x503, v141
	global_store_dword v139, v145, s[40:41]
	v_add_u32_e32 v139, 4, v139
	s_mov_b64 exec, -1
	s_bcnt1_i32_b64 s4, s[58:59]
	s_add_i32 s26, s26, s4
	s_bcnt1_i32_b64 s4, s[60:61]
	s_add_i32 s26, s26, s4
	s_bcnt1_i32_b64 s4, s[62:63]
	s_add_i32 s26, s26, s4
	s_bcnt1_i32_b64 s4, s[64:65]
	s_add_i32 s26, s26, s4
	s_cmp_le_u32 s79, 6
	s_cbranch_scc1 .Lsel_fsn_bend
	v_cmp_le_u32_e64 s[58:59], v26, s76
	v_cmp_le_u32_e64 s[60:61], v27, s76
	v_cmp_le_u32_e64 s[62:63], v28, s76
	v_cmp_le_u32_e64 s[64:65], v29, s76
	v_mov_b32_e32 v139, s26
	v_mbcnt_lo_u32_b32 v139, s58, v139
	v_mbcnt_hi_u32_b32 v139, s59, v139
	v_mbcnt_lo_u32_b32 v139, s60, v139
	v_mbcnt_hi_u32_b32 v139, s61, v139
	v_mbcnt_lo_u32_b32 v139, s62, v139
	v_mbcnt_hi_u32_b32 v139, s63, v139
	v_mbcnt_lo_u32_b32 v139, s64, v139
	v_mbcnt_hi_u32_b32 v139, s65, v139
	v_lshlrev_b32_e32 v139, 2, v139
	s_mov_b64 exec, s[58:59]
	v_add_u32_e32 v142, 0x600, v141
	global_store_dword v139, v142, s[40:41]
	v_add_u32_e32 v139, 4, v139
	s_mov_b64 exec, s[60:61]
	v_add_u32_e32 v143, 0x601, v141
	global_store_dword v139, v143, s[40:41]
	v_add_u32_e32 v139, 4, v139
	s_mov_b64 exec, s[62:63]
	v_add_u32_e32 v144, 0x602, v141
	global_store_dword v139, v144, s[40:41]
	v_add_u32_e32 v139, 4, v139
	s_mov_b64 exec, s[64:65]
	v_add_u32_e32 v145, 0x603, v141
	global_store_dword v139, v145, s[40:41]
	v_add_u32_e32 v139, 4, v139
	s_mov_b64 exec, -1
	s_bcnt1_i32_b64 s4, s[58:59]
	s_add_i32 s26, s26, s4
	s_bcnt1_i32_b64 s4, s[60:61]
	s_add_i32 s26, s26, s4
	s_bcnt1_i32_b64 s4, s[62:63]
	s_add_i32 s26, s26, s4
	s_bcnt1_i32_b64 s4, s[64:65]
	s_add_i32 s26, s26, s4
	s_cmp_le_u32 s79, 7
	s_cbranch_scc1 .Lsel_fsn_bend
	v_cmp_le_u32_e64 s[58:59], v30, s76
	v_cmp_le_u32_e64 s[60:61], v31, s76
	v_cmp_le_u32_e64 s[62:63], v32, s76
	v_cmp_le_u32_e64 s[64:65], v33, s76
	v_mov_b32_e32 v139, s26
	v_mbcnt_lo_u32_b32 v139, s58, v139
	v_mbcnt_hi_u32_b32 v139, s59, v139
	v_mbcnt_lo_u32_b32 v139, s60, v139
	v_mbcnt_hi_u32_b32 v139, s61, v139
	v_mbcnt_lo_u32_b32 v139, s62, v139
	v_mbcnt_hi_u32_b32 v139, s63, v139
	v_mbcnt_lo_u32_b32 v139, s64, v139
	v_mbcnt_hi_u32_b32 v139, s65, v139
	v_lshlrev_b32_e32 v139, 2, v139
	s_mov_b64 exec, s[58:59]
	v_add_u32_e32 v142, 0x700, v141
	global_store_dword v139, v142, s[40:41]
	v_add_u32_e32 v139, 4, v139
	s_mov_b64 exec, s[60:61]
	v_add_u32_e32 v143, 0x701, v141
	global_store_dword v139, v143, s[40:41]
	v_add_u32_e32 v139, 4, v139
	s_mov_b64 exec, s[62:63]
	v_add_u32_e32 v144, 0x702, v141
	global_store_dword v139, v144, s[40:41]
	v_add_u32_e32 v139, 4, v139
	s_mov_b64 exec, s[64:65]
	v_add_u32_e32 v145, 0x703, v141
	global_store_dword v139, v145, s[40:41]
	v_add_u32_e32 v139, 4, v139
	s_mov_b64 exec, -1
	s_bcnt1_i32_b64 s4, s[58:59]
	s_add_i32 s26, s26, s4
	s_bcnt1_i32_b64 s4, s[60:61]
	s_add_i32 s26, s26, s4
	s_bcnt1_i32_b64 s4, s[62:63]
	s_add_i32 s26, s26, s4
	s_bcnt1_i32_b64 s4, s[64:65]
	s_add_i32 s26, s26, s4
	s_cmp_le_u32 s79, 8
	s_cbranch_scc1 .Lsel_fsn_bend
	v_cmp_le_u32_e64 s[58:59], v34, s76
	v_cmp_le_u32_e64 s[60:61], v35, s76
	v_cmp_le_u32_e64 s[62:63], v36, s76
	v_cmp_le_u32_e64 s[64:65], v37, s76
	v_mov_b32_e32 v139, s26
	v_mbcnt_lo_u32_b32 v139, s58, v139
	v_mbcnt_hi_u32_b32 v139, s59, v139
	v_mbcnt_lo_u32_b32 v139, s60, v139
	v_mbcnt_hi_u32_b32 v139, s61, v139
	v_mbcnt_lo_u32_b32 v139, s62, v139
	v_mbcnt_hi_u32_b32 v139, s63, v139
	v_mbcnt_lo_u32_b32 v139, s64, v139
	v_mbcnt_hi_u32_b32 v139, s65, v139
	v_lshlrev_b32_e32 v139, 2, v139
	s_mov_b64 exec, s[58:59]
	v_add_u32_e32 v142, 0x800, v141
	global_store_dword v139, v142, s[40:41]
	v_add_u32_e32 v139, 4, v139
	s_mov_b64 exec, s[60:61]
	v_add_u32_e32 v143, 0x801, v141
	global_store_dword v139, v143, s[40:41]
	v_add_u32_e32 v139, 4, v139
	s_mov_b64 exec, s[62:63]
	v_add_u32_e32 v144, 0x802, v141
	global_store_dword v139, v144, s[40:41]
	v_add_u32_e32 v139, 4, v139
	s_mov_b64 exec, s[64:65]
	v_add_u32_e32 v145, 0x803, v141
	global_store_dword v139, v145, s[40:41]
	v_add_u32_e32 v139, 4, v139
	s_mov_b64 exec, -1
	s_bcnt1_i32_b64 s4, s[58:59]
	s_add_i32 s26, s26, s4
	s_bcnt1_i32_b64 s4, s[60:61]
	s_add_i32 s26, s26, s4
	s_bcnt1_i32_b64 s4, s[62:63]
	s_add_i32 s26, s26, s4
	s_bcnt1_i32_b64 s4, s[64:65]
	s_add_i32 s26, s26, s4
	s_cmp_le_u32 s79, 9
	s_cbranch_scc1 .Lsel_fsn_bend
	v_cmp_le_u32_e64 s[58:59], v38, s76
	v_cmp_le_u32_e64 s[60:61], v39, s76
	v_cmp_le_u32_e64 s[62:63], v40, s76
	v_cmp_le_u32_e64 s[64:65], v41, s76
	v_mov_b32_e32 v139, s26
	v_mbcnt_lo_u32_b32 v139, s58, v139
	v_mbcnt_hi_u32_b32 v139, s59, v139
	v_mbcnt_lo_u32_b32 v139, s60, v139
	v_mbcnt_hi_u32_b32 v139, s61, v139
	v_mbcnt_lo_u32_b32 v139, s62, v139
	v_mbcnt_hi_u32_b32 v139, s63, v139
	v_mbcnt_lo_u32_b32 v139, s64, v139
	v_mbcnt_hi_u32_b32 v139, s65, v139
	v_lshlrev_b32_e32 v139, 2, v139
	s_mov_b64 exec, s[58:59]
	v_add_u32_e32 v142, 0x900, v141
	global_store_dword v139, v142, s[40:41]
	v_add_u32_e32 v139, 4, v139
	s_mov_b64 exec, s[60:61]
	v_add_u32_e32 v143, 0x901, v141
	global_store_dword v139, v143, s[40:41]
	v_add_u32_e32 v139, 4, v139
	s_mov_b64 exec, s[62:63]
	v_add_u32_e32 v144, 0x902, v141
	global_store_dword v139, v144, s[40:41]
	v_add_u32_e32 v139, 4, v139
	s_mov_b64 exec, s[64:65]
	v_add_u32_e32 v145, 0x903, v141
	global_store_dword v139, v145, s[40:41]
	v_add_u32_e32 v139, 4, v139
	s_mov_b64 exec, -1
	s_bcnt1_i32_b64 s4, s[58:59]
	s_add_i32 s26, s26, s4
	s_bcnt1_i32_b64 s4, s[60:61]
	s_add_i32 s26, s26, s4
	s_bcnt1_i32_b64 s4, s[62:63]
	s_add_i32 s26, s26, s4
	s_bcnt1_i32_b64 s4, s[64:65]
	s_add_i32 s26, s26, s4
	s_cmp_le_u32 s79, 10
	s_cbranch_scc1 .Lsel_fsn_bend
	v_cmp_le_u32_e64 s[58:59], v42, s76
	v_cmp_le_u32_e64 s[60:61], v43, s76
	v_cmp_le_u32_e64 s[62:63], v44, s76
	v_cmp_le_u32_e64 s[64:65], v45, s76
	v_mov_b32_e32 v139, s26
	v_mbcnt_lo_u32_b32 v139, s58, v139
	v_mbcnt_hi_u32_b32 v139, s59, v139
	v_mbcnt_lo_u32_b32 v139, s60, v139
	v_mbcnt_hi_u32_b32 v139, s61, v139
	v_mbcnt_lo_u32_b32 v139, s62, v139
	v_mbcnt_hi_u32_b32 v139, s63, v139
	v_mbcnt_lo_u32_b32 v139, s64, v139
	v_mbcnt_hi_u32_b32 v139, s65, v139
	v_lshlrev_b32_e32 v139, 2, v139
	s_mov_b64 exec, s[58:59]
	v_add_u32_e32 v142, 0xa00, v141
	global_store_dword v139, v142, s[40:41]
	v_add_u32_e32 v139, 4, v139
	s_mov_b64 exec, s[60:61]
	v_add_u32_e32 v143, 0xa01, v141
	global_store_dword v139, v143, s[40:41]
	v_add_u32_e32 v139, 4, v139
	s_mov_b64 exec, s[62:63]
	v_add_u32_e32 v144, 0xa02, v141
	global_store_dword v139, v144, s[40:41]
	v_add_u32_e32 v139, 4, v139
	s_mov_b64 exec, s[64:65]
	v_add_u32_e32 v145, 0xa03, v141
	global_store_dword v139, v145, s[40:41]
	v_add_u32_e32 v139, 4, v139
	s_mov_b64 exec, -1
	s_bcnt1_i32_b64 s4, s[58:59]
	s_add_i32 s26, s26, s4
	s_bcnt1_i32_b64 s4, s[60:61]
	s_add_i32 s26, s26, s4
	s_bcnt1_i32_b64 s4, s[62:63]
	s_add_i32 s26, s26, s4
	s_bcnt1_i32_b64 s4, s[64:65]
	s_add_i32 s26, s26, s4
	s_cmp_le_u32 s79, 11
	s_cbranch_scc1 .Lsel_fsn_bend
	v_cmp_le_u32_e64 s[58:59], v46, s76
	v_cmp_le_u32_e64 s[60:61], v47, s76
	v_cmp_le_u32_e64 s[62:63], v48, s76
	v_cmp_le_u32_e64 s[64:65], v49, s76
	v_mov_b32_e32 v139, s26
	v_mbcnt_lo_u32_b32 v139, s58, v139
	v_mbcnt_hi_u32_b32 v139, s59, v139
	v_mbcnt_lo_u32_b32 v139, s60, v139
	v_mbcnt_hi_u32_b32 v139, s61, v139
	v_mbcnt_lo_u32_b32 v139, s62, v139
	v_mbcnt_hi_u32_b32 v139, s63, v139
	v_mbcnt_lo_u32_b32 v139, s64, v139
	v_mbcnt_hi_u32_b32 v139, s65, v139
	v_lshlrev_b32_e32 v139, 2, v139
	s_mov_b64 exec, s[58:59]
	v_add_u32_e32 v142, 0xb00, v141
	global_store_dword v139, v142, s[40:41]
	v_add_u32_e32 v139, 4, v139
	s_mov_b64 exec, s[60:61]
	v_add_u32_e32 v143, 0xb01, v141
	global_store_dword v139, v143, s[40:41]
	v_add_u32_e32 v139, 4, v139
	s_mov_b64 exec, s[62:63]
	v_add_u32_e32 v144, 0xb02, v141
	global_store_dword v139, v144, s[40:41]
	v_add_u32_e32 v139, 4, v139
	s_mov_b64 exec, s[64:65]
	v_add_u32_e32 v145, 0xb03, v141
	global_store_dword v139, v145, s[40:41]
	v_add_u32_e32 v139, 4, v139
	s_mov_b64 exec, -1
	s_bcnt1_i32_b64 s4, s[58:59]
	s_add_i32 s26, s26, s4
	s_bcnt1_i32_b64 s4, s[60:61]
	s_add_i32 s26, s26, s4
	s_bcnt1_i32_b64 s4, s[62:63]
	s_add_i32 s26, s26, s4
	s_bcnt1_i32_b64 s4, s[64:65]
	s_add_i32 s26, s26, s4
	s_cmp_le_u32 s79, 12
	s_cbranch_scc1 .Lsel_fsn_bend
	v_cmp_le_u32_e64 s[58:59], v118, s76
	v_cmp_le_u32_e64 s[60:61], v119, s76
	v_cmp_le_u32_e64 s[62:63], v120, s76
	v_cmp_le_u32_e64 s[64:65], v121, s76
	v_mov_b32_e32 v139, s26
	v_mbcnt_lo_u32_b32 v139, s58, v139
	v_mbcnt_hi_u32_b32 v139, s59, v139
	v_mbcnt_lo_u32_b32 v139, s60, v139
	v_mbcnt_hi_u32_b32 v139, s61, v139
	v_mbcnt_lo_u32_b32 v139, s62, v139
	v_mbcnt_hi_u32_b32 v139, s63, v139
	v_mbcnt_lo_u32_b32 v139, s64, v139
	v_mbcnt_hi_u32_b32 v139, s65, v139
	v_lshlrev_b32_e32 v139, 2, v139
	s_mov_b64 exec, s[58:59]
	v_add_u32_e32 v142, 0xc00, v141
	global_store_dword v139, v142, s[40:41]
	v_add_u32_e32 v139, 4, v139
	s_mov_b64 exec, s[60:61]
	v_add_u32_e32 v143, 0xc01, v141
	global_store_dword v139, v143, s[40:41]
	v_add_u32_e32 v139, 4, v139
	s_mov_b64 exec, s[62:63]
	v_add_u32_e32 v144, 0xc02, v141
	global_store_dword v139, v144, s[40:41]
	v_add_u32_e32 v139, 4, v139
	s_mov_b64 exec, s[64:65]
	v_add_u32_e32 v145, 0xc03, v141
	global_store_dword v139, v145, s[40:41]
	v_add_u32_e32 v139, 4, v139
	s_mov_b64 exec, -1
	s_bcnt1_i32_b64 s4, s[58:59]
	s_add_i32 s26, s26, s4
	s_bcnt1_i32_b64 s4, s[60:61]
	s_add_i32 s26, s26, s4
	s_bcnt1_i32_b64 s4, s[62:63]
	s_add_i32 s26, s26, s4
	s_bcnt1_i32_b64 s4, s[64:65]
	s_add_i32 s26, s26, s4
	s_cmp_le_u32 s79, 13
	s_cbranch_scc1 .Lsel_fsn_bend
	v_cmp_le_u32_e64 s[58:59], v122, s76
	v_cmp_le_u32_e64 s[60:61], v123, s76
	v_cmp_le_u32_e64 s[62:63], v124, s76
	v_cmp_le_u32_e64 s[64:65], v125, s76
	v_mov_b32_e32 v139, s26
	v_mbcnt_lo_u32_b32 v139, s58, v139
	v_mbcnt_hi_u32_b32 v139, s59, v139
	v_mbcnt_lo_u32_b32 v139, s60, v139
	v_mbcnt_hi_u32_b32 v139, s61, v139
	v_mbcnt_lo_u32_b32 v139, s62, v139
	v_mbcnt_hi_u32_b32 v139, s63, v139
	v_mbcnt_lo_u32_b32 v139, s64, v139
	v_mbcnt_hi_u32_b32 v139, s65, v139
	v_lshlrev_b32_e32 v139, 2, v139
	s_mov_b64 exec, s[58:59]
	v_add_u32_e32 v142, 0xd00, v141
	global_store_dword v139, v142, s[40:41]
	v_add_u32_e32 v139, 4, v139
	s_mov_b64 exec, s[60:61]
	v_add_u32_e32 v143, 0xd01, v141
	global_store_dword v139, v143, s[40:41]
	v_add_u32_e32 v139, 4, v139
	s_mov_b64 exec, s[62:63]
	v_add_u32_e32 v144, 0xd02, v141
	global_store_dword v139, v144, s[40:41]
	v_add_u32_e32 v139, 4, v139
	s_mov_b64 exec, s[64:65]
	v_add_u32_e32 v145, 0xd03, v141
	global_store_dword v139, v145, s[40:41]
	v_add_u32_e32 v139, 4, v139
	s_mov_b64 exec, -1
	s_bcnt1_i32_b64 s4, s[58:59]
	s_add_i32 s26, s26, s4
	s_bcnt1_i32_b64 s4, s[60:61]
	s_add_i32 s26, s26, s4
	s_bcnt1_i32_b64 s4, s[62:63]
	s_add_i32 s26, s26, s4
	s_bcnt1_i32_b64 s4, s[64:65]
	s_add_i32 s26, s26, s4
	s_cmp_le_u32 s79, 14
	s_cbranch_scc1 .Lsel_fsn_bend
	v_cmp_le_u32_e64 s[58:59], v126, s76
	v_cmp_le_u32_e64 s[60:61], v127, s76
	v_cmp_le_u32_e64 s[62:63], v128, s76
	v_cmp_le_u32_e64 s[64:65], v129, s76
	v_mov_b32_e32 v139, s26
	v_mbcnt_lo_u32_b32 v139, s58, v139
	v_mbcnt_hi_u32_b32 v139, s59, v139
	v_mbcnt_lo_u32_b32 v139, s60, v139
	v_mbcnt_hi_u32_b32 v139, s61, v139
	v_mbcnt_lo_u32_b32 v139, s62, v139
	v_mbcnt_hi_u32_b32 v139, s63, v139
	v_mbcnt_lo_u32_b32 v139, s64, v139
	v_mbcnt_hi_u32_b32 v139, s65, v139
	v_lshlrev_b32_e32 v139, 2, v139
	s_mov_b64 exec, s[58:59]
	v_add_u32_e32 v142, 0xe00, v141
	global_store_dword v139, v142, s[40:41]
	v_add_u32_e32 v139, 4, v139
	s_mov_b64 exec, s[60:61]
	v_add_u32_e32 v143, 0xe01, v141
	global_store_dword v139, v143, s[40:41]
	v_add_u32_e32 v139, 4, v139
	s_mov_b64 exec, s[62:63]
	v_add_u32_e32 v144, 0xe02, v141
	global_store_dword v139, v144, s[40:41]
	v_add_u32_e32 v139, 4, v139
	s_mov_b64 exec, s[64:65]
	v_add_u32_e32 v145, 0xe03, v141
	global_store_dword v139, v145, s[40:41]
	v_add_u32_e32 v139, 4, v139
	s_mov_b64 exec, -1
	s_bcnt1_i32_b64 s4, s[58:59]
	s_add_i32 s26, s26, s4
	s_bcnt1_i32_b64 s4, s[60:61]
	s_add_i32 s26, s26, s4
	s_bcnt1_i32_b64 s4, s[62:63]
	s_add_i32 s26, s26, s4
	s_bcnt1_i32_b64 s4, s[64:65]
	s_add_i32 s26, s26, s4
	s_cmp_le_u32 s79, 15
	s_cbranch_scc1 .Lsel_fsn_bend
	v_cmp_le_u32_e64 s[58:59], v130, s76
	v_cmp_le_u32_e64 s[60:61], v131, s76
	v_cmp_le_u32_e64 s[62:63], v132, s76
	v_cmp_le_u32_e64 s[64:65], v133, s76
	v_mov_b32_e32 v139, s26
	v_mbcnt_lo_u32_b32 v139, s58, v139
	v_mbcnt_hi_u32_b32 v139, s59, v139
	v_mbcnt_lo_u32_b32 v139, s60, v139
	v_mbcnt_hi_u32_b32 v139, s61, v139
	v_mbcnt_lo_u32_b32 v139, s62, v139
	v_mbcnt_hi_u32_b32 v139, s63, v139
	v_mbcnt_lo_u32_b32 v139, s64, v139
	v_mbcnt_hi_u32_b32 v139, s65, v139
	v_lshlrev_b32_e32 v139, 2, v139
	s_mov_b64 exec, s[58:59]
	v_add_u32_e32 v142, 0xf00, v141
	global_store_dword v139, v142, s[40:41]
	v_add_u32_e32 v139, 4, v139
	s_mov_b64 exec, s[60:61]
	v_add_u32_e32 v143, 0xf01, v141
	global_store_dword v139, v143, s[40:41]
	v_add_u32_e32 v139, 4, v139
	s_mov_b64 exec, s[62:63]
	v_add_u32_e32 v144, 0xf02, v141
	global_store_dword v139, v144, s[40:41]
	v_add_u32_e32 v139, 4, v139
	s_mov_b64 exec, s[64:65]
	v_add_u32_e32 v145, 0xf03, v141
	global_store_dword v139, v145, s[40:41]
	v_add_u32_e32 v139, 4, v139
	s_mov_b64 exec, -1
	s_bcnt1_i32_b64 s4, s[58:59]
	s_add_i32 s26, s26, s4
	s_bcnt1_i32_b64 s4, s[60:61]
	s_add_i32 s26, s26, s4
	s_bcnt1_i32_b64 s4, s[62:63]
	s_add_i32 s26, s26, s4
	s_bcnt1_i32_b64 s4, s[64:65]
	s_add_i32 s26, s26, s4
